# nt on the residual / x tile loads of the pool, per-layer-embedding and Wo epilogues + final RMSNorm rewrite (sc1 output stores)
# baseline (speedup 1.0000x reference)
.LBB0_498:
	v_mov_b32_e32 v188, v0
	s_lshl_b32 s34, s34, 8
	v_readfirstlane_b32 s36, v188
	s_ashr_i32 s29, s36, 6
	s_ashr_i32 s36, s36, 2
	s_mul_i32 s27, s29, 0xb00
	s_and_b32 s29, s29, 3
	s_andn2_b32 s36, s36, 63
	s_lshl_b32 s37, s35, 8
	s_lshl_b32 s38, s29, 6
	s_add_i32 s46, s36, s34
	s_add_i32 s27, s27, 0
	s_or_b32 s38, s38, s37
	s_ashr_i32 s47, s46, 31
	s_add_i32 s27, s27, 0x20000
	s_ashr_i32 s39, s38, 31
	s_lshl_b64 s[40:41], s[46:47], 12
	s_add_u32 s37, s10, s40
	s_addc_u32 s41, s11, s41
	s_lshl_b64 s[44:45], s[38:39], 2
	v_and_b32_e32 v196, 63, v188
	s_add_u32 s40, s37, s44
	v_bfe_u32 v189, v188, 3, 3
	s_addc_u32 s41, s41, s45
	v_lshlrev_b32_e32 v138, 12, v189
	v_lshlrev_b32_e32 v197, 4, v196
	v_or_b32_e32 v190, 8, v189
	v_and_b32_e32 v144, 0x70, v197
	v_mov_b32_e32 v145, v139
	v_lshlrev_b32_e32 v146, 12, v190
	v_mov_b32_e32 v147, v139
	v_lshl_add_u64 v[148:149], s[40:41], 0, v[138:139]
	v_lshl_add_u64 v[164:165], v[148:149], 0, v[144:145]
	v_lshl_add_u64 v[152:153], s[40:41], 0, v[146:147]
	global_load_dwordx4 v[148:151], v[164:165], off nt
	v_lshl_add_u64 v[168:169], v[152:153], 0, v[144:145]
	global_load_dwordx4 v[152:155], v[168:169], off nt
	v_bfe_u32 v198, v188, 4, 2
	s_add_u32 s42, s12, s44
	s_addc_u32 s43, s13, s45
	v_lshlrev_b32_e32 v201, 5, v198
	global_load_dwordx4 v[156:159], v201, s[42:43] nt
	global_load_dwordx4 v[160:163], v201, s[42:43] offset:16 nt
	s_nop 0
	global_load_dwordx4 v[164:167], v[164:165], off offset:128 nt
	s_nop 0
	global_load_dwordx4 v[168:171], v[168:169], off offset:128 nt
	s_nop 0
	global_load_dwordx4 v[172:175], v201, s[42:43] offset:128 nt
	global_load_dwordx4 v[176:179], v201, s[42:43] offset:144 nt
	v_mul_u32_u24_e32 v180, 0x90, v189
	v_and_b32_e32 v199, 15, v188
	v_add3_u32 v200, s27, v180, v144
	v_mov_b32_e32 v180, s27
	v_mad_u32_u24 v203, v199, s67, v180
	v_add_u32_e32 v206, v203, v201
	v_mov_b32_e32 v184, v139
	v_mov_b32_e32 v185, v139
	v_mov_b32_e32 v186, v139
	v_mov_b32_e32 v187, v139
	v_and_b32_e32 v191, 48, v188
	s_lshl_b64 s[40:41], s[46:47], 11
	s_add_u32 s37, s56, s40
	v_add_u32_e32 v203, v203, v191
	s_addc_u32 s49, s57, s41
	s_lshl_b64 s[40:41], s[38:39], 1
	s_add_u32 s48, s37, s40
	s_addc_u32 s49, s49, s41
	v_lshlrev_b32_e32 v204, 3, v198
	v_mov_b32_e32 v191, v139
	v_mov_b32_e32 v208, v139
	v_mov_b32_e32 v209, v139
	s_waitcnt vmcnt(0)
	ds_write_b128 v200, v[148:151]
	ds_write_b128 v200, v[152:155] offset:1152
	ds_read_b128 v[148:151], v206
	ds_read_b128 v[180:183], v206 offset:16
	s_waitcnt lgkmcnt(1)
	v_pk_fma_f32 v[152:153], v[124:125], v[158:159], v[150:151]
	v_pk_fma_f32 v[154:155], v[122:123], v[156:157], v[148:149]
	s_waitcnt lgkmcnt(0)
	v_pk_fma_f32 v[150:151], v[126:127], v[160:161], v[180:181]
	v_pk_fma_f32 v[148:149], v[128:129], v[162:163], v[182:183]
	v_cvt_pk_bf16_f32 v156, v154, v155
	v_cvt_pk_bf16_f32 v157, v152, v153
	v_cvt_pk_bf16_f32 v158, v150, v151
	v_med3_f32 v122, v154, s68, v195
	v_cvt_pk_bf16_f32 v159, v148, v149
	v_med3_f32 v123, v150, s68, v195
	v_med3_f32 v124, v155, s68, v195
	v_med3_f32 v125, v151, s68, v195
	ds_write_b128 v200, v[164:167]
	ds_write_b128 v200, v[168:171] offset:1152
	v_cvt_pk_fp8_f32 v184, v122, v124
	v_cvt_pk_fp8_f32 v185, v123, v125
	ds_read_b128 v[124:127], v206
	ds_read_b128 v[160:163], v206 offset:16
	v_med3_f32 v128, v152, s68, v195
	v_med3_f32 v129, v148, s68, v195
	v_med3_f32 v180, v153, s68, v195
	v_med3_f32 v122, v149, s68, v195
	v_cvt_pk_fp8_f32 v184, v128, v180 op_sel:[0,0,1]
	v_cvt_pk_fp8_f32 v185, v129, v122 op_sel:[0,0,1]
	s_waitcnt lgkmcnt(1)
	v_pk_fma_f32 v[122:123], v[116:117], v[174:175], v[126:127]
	v_pk_fma_f32 v[126:127], v[114:115], v[172:173], v[124:125]
	s_waitcnt lgkmcnt(0)
	v_pk_fma_f32 v[128:129], v[118:119], v[176:177], v[160:161]
	v_pk_fma_f32 v[124:125], v[120:121], v[178:179], v[162:163]
	v_med3_f32 v118, v126, s68, v195
	v_med3_f32 v119, v128, s68, v195
	v_med3_f32 v120, v127, s68, v195
	v_med3_f32 v121, v129, s68, v195
	v_cvt_pk_fp8_f32 v186, v118, v120
	v_cvt_pk_fp8_f32 v187, v119, v121
	v_cvt_pk_bf16_f32 v114, v126, v127
	v_cvt_pk_bf16_f32 v115, v122, v123
	v_cvt_pk_bf16_f32 v116, v128, v129
	v_cvt_pk_bf16_f32 v117, v124, v125
	v_med3_f32 v160, v122, s68, v195
	v_med3_f32 v161, v124, s68, v195
	v_med3_f32 v118, v123, s68, v195
	v_med3_f32 v119, v125, s68, v195
	ds_write_b128 v203, v[156:159]
	ds_write_b128 v203, v[114:117] offset:64
	v_cvt_pk_fp8_f32 v186, v160, v118 op_sel:[0,0,1]
	v_cvt_pk_fp8_f32 v187, v161, v119 op_sel:[0,0,1]
	ds_read_b128 v[116:119], v200
	ds_read_b128 v[156:159], v200 offset:1152
	v_lshlrev_b32_e32 v114, 11, v189
	v_mov_b32_e32 v115, v139
	v_lshl_add_u64 v[120:121], s[48:49], 0, v[114:115]
	v_lshl_add_u64 v[120:121], v[120:121], 0, v[144:145]
	s_waitcnt lgkmcnt(1)
	global_store_dwordx4 v[120:121], v[116:119], off
	v_mov_b32_e32 v121, v139
	v_mov_b32_e32 v189, v139
	v_lshlrev_b32_e32 v116, 11, v190
	v_mov_b32_e32 v117, v139
	v_lshl_add_u64 v[118:119], s[48:49], 0, v[116:117]
	s_lshl_b64 s[48:49], s[46:47], 10
	v_lshl_add_u64 v[118:119], v[118:119], 0, v[144:145]
	s_add_u32 s37, s60, s48
	s_waitcnt lgkmcnt(0)
	global_store_dwordx4 v[118:119], v[156:159], off
	s_addc_u32 s47, s61, s49
	v_mul_u32_u24_e32 v118, 0x50, v199
	v_bfe_u32 v119, v188, 2, 4
	s_add_u32 s48, s37, s38
	v_add3_u32 v204, s27, v118, v204
	v_mul_u32_u24_e32 v120, 0x50, v119
	v_and_b32_e32 v118, 48, v197
	s_addc_u32 s49, s47, s39
	v_add3_u32 v205, s27, v120, v118
	v_lshlrev_b32_e32 v120, 10, v119
	v_lshl_add_u64 v[160:161], s[48:49], 0, v[120:121]
	s_or_b32 s48, s46, 16
	ds_write2_b64 v204, v[184:185], v[186:187] offset1:4
	s_ashr_i32 s49, s48, 31
	ds_read_b128 v[156:159], v205
	s_lshl_b64 s[70:71], s[48:49], 12
	s_add_u32 s37, s10, s70
	s_addc_u32 s47, s11, s71
	v_mov_b32_e32 v119, v139
	s_add_u32 s70, s37, s44
	v_lshl_add_u64 v[160:161], v[160:161], 0, v[118:119]
	s_addc_u32 s71, s47, s45
	s_waitcnt lgkmcnt(0)
	global_store_dwordx4 v[160:161], v[156:159], off
	v_lshl_add_u64 v[160:161], s[70:71], 0, v[146:147]
	v_lshl_add_u64 v[176:177], v[160:161], 0, v[144:145]
	v_lshl_add_u64 v[156:157], s[70:71], 0, v[138:139]
	v_lshl_add_u64 v[172:173], v[156:157], 0, v[144:145]
	global_load_dwordx4 v[156:159], v[172:173], off nt
	global_load_dwordx4 v[160:163], v[176:177], off nt
	global_load_dwordx4 v[164:167], v201, s[42:43] nt
	global_load_dwordx4 v[168:171], v201, s[42:43] offset:16 nt
	s_nop 0
	global_load_dwordx4 v[172:175], v[172:173], off offset:128 nt
	s_nop 0
	global_load_dwordx4 v[176:179], v[176:177], off offset:128 nt
	s_nop 0
	global_load_dwordx4 v[180:183], v201, s[42:43] offset:128 nt
	global_load_dwordx4 v[184:187], v201, s[42:43] offset:144 nt
	s_waitcnt vmcnt(7)
	ds_write_b128 v200, v[156:159]
	s_waitcnt vmcnt(6)
	ds_write_b128 v200, v[160:163] offset:1152
	ds_read_b128 v[156:159], v206
	ds_read_b128 v[160:163], v206 offset:16
	v_mov_b32_e32 v188, v139
	s_lshl_b64 s[70:71], s[48:49], 11
	v_mov_b32_e32 v190, v139
	s_waitcnt vmcnt(5) lgkmcnt(1)
	v_pk_fma_f32 v[156:157], v[106:107], v[164:165], v[156:157]
	s_waitcnt vmcnt(4) lgkmcnt(0)
	v_pk_fma_f32 v[110:111], v[110:111], v[168:169], v[160:161]
	v_pk_fma_f32 v[108:109], v[108:109], v[166:167], v[158:159]
	v_pk_fma_f32 v[106:107], v[112:113], v[170:171], v[162:163]
	v_cvt_pk_bf16_f32 v158, v156, v157
	v_cvt_pk_bf16_f32 v159, v108, v109
	v_cvt_pk_bf16_f32 v160, v110, v111
	v_med3_f32 v112, v156, s68, v195
	v_cvt_pk_bf16_f32 v161, v106, v107
	v_med3_f32 v113, v110, s68, v195
	v_med3_f32 v162, v157, s68, v195
	v_med3_f32 v163, v111, s68, v195
	s_waitcnt vmcnt(3)
	ds_write_b128 v200, v[172:175]
	s_waitcnt vmcnt(2)
	ds_write_b128 v200, v[176:179] offset:1152
	v_cvt_pk_fp8_f32 v188, v112, v162
	v_cvt_pk_fp8_f32 v189, v113, v163
	ds_read_b128 v[162:165], v206
	ds_read_b128 v[166:169], v206 offset:16
	v_med3_f32 v171, v106, s68, v195
	v_med3_f32 v112, v107, s68, v195
	v_cvt_pk_fp8_f32 v189, v171, v112 op_sel:[0,0,1]
	s_waitcnt vmcnt(1) lgkmcnt(1)
	v_pk_fma_f32 v[112:113], v[98:99], v[180:181], v[162:163]
	s_waitcnt vmcnt(0) lgkmcnt(0)
	v_pk_fma_f32 v[102:103], v[102:103], v[184:185], v[166:167]
	v_pk_fma_f32 v[98:99], v[104:105], v[186:187], v[168:169]
	v_med3_f32 v105, v102, s68, v195
	v_med3_f32 v167, v103, s68, v195
	s_add_u32 s37, s56, s70
	v_pk_fma_f32 v[100:101], v[100:101], v[182:183], v[164:165]
	v_cvt_pk_bf16_f32 v162, v112, v113
	v_med3_f32 v104, v112, s68, v195
	v_cvt_pk_bf16_f32 v163, v100, v101
	v_cvt_pk_bf16_f32 v164, v102, v103
	v_cvt_pk_bf16_f32 v165, v98, v99
	v_med3_f32 v166, v113, s68, v195
	v_cvt_pk_fp8_f32 v191, v105, v167
	ds_write_b128 v203, v[158:161]
	ds_write_b128 v203, v[162:165] offset:64
	s_addc_u32 s47, s57, s71
	v_cvt_pk_fp8_f32 v190, v104, v166
	ds_read_b128 v[158:161], v200
	ds_read_b128 v[162:165], v200 offset:1152
	s_add_u32 s70, s37, s40
	v_med3_f32 v170, v108, s68, v195
	v_med3_f32 v207, v109, s68, v195
	v_med3_f32 v169, v98, s68, v195
	v_med3_f32 v104, v99, s68, v195
	s_addc_u32 s71, s47, s41
	s_lshl_b64 s[48:49], s[48:49], 10
	v_cvt_pk_fp8_f32 v188, v170, v207 op_sel:[0,0,1]
	v_med3_f32 v168, v100, s68, v195
	v_med3_f32 v170, v101, s68, v195
	v_cvt_pk_fp8_f32 v191, v169, v104 op_sel:[0,0,1]
	v_lshl_add_u64 v[104:105], s[70:71], 0, v[114:115]
	s_add_u32 s37, s60, s48
	v_cvt_pk_fp8_f32 v190, v168, v170 op_sel:[0,0,1]
	v_lshl_add_u64 v[104:105], v[104:105], 0, v[144:145]
	s_addc_u32 s47, s61, s49
	s_waitcnt lgkmcnt(1)
	global_store_dwordx4 v[104:105], v[158:161], off
	v_lshl_add_u64 v[104:105], s[70:71], 0, v[116:117]
	s_add_u32 s48, s37, s38
	v_lshl_add_u64 v[104:105], v[104:105], 0, v[144:145]
	s_addc_u32 s49, s47, s39
	s_waitcnt lgkmcnt(0)
	global_store_dwordx4 v[104:105], v[162:165], off
	v_lshl_add_u64 v[104:105], s[48:49], 0, v[120:121]
	s_or_b32 s48, s46, 32
	ds_write2_b64 v204, v[188:189], v[190:191] offset1:4
	s_ashr_i32 s49, s48, 31
	ds_read_b128 v[158:161], v205
	s_lshl_b64 s[70:71], s[48:49], 12
	s_add_u32 s37, s10, s70
	s_addc_u32 s47, s11, s71
	s_add_u32 s70, s37, s44
	v_lshl_add_u64 v[104:105], v[104:105], 0, v[118:119]
	s_addc_u32 s71, s47, s45
	s_waitcnt lgkmcnt(0)
	global_store_dwordx4 v[104:105], v[158:161], off
	v_lshl_add_u64 v[104:105], s[70:71], 0, v[138:139]
	v_lshl_add_u64 v[104:105], v[104:105], 0, v[144:145]
	global_load_dwordx4 v[158:161], v[104:105], off nt
	v_lshl_add_u64 v[162:163], s[70:71], 0, v[146:147]
	v_lshl_add_u64 v[178:179], v[162:163], 0, v[144:145]
	global_load_dwordx4 v[162:165], v[178:179], off nt
	global_load_dwordx4 v[166:169], v201, s[42:43] nt
	global_load_dwordx4 v[170:173], v201, s[42:43] offset:16 nt
	global_load_dwordx4 v[174:177], v[104:105], off offset:128 nt
	s_nop 0
	global_load_dwordx4 v[178:181], v[178:179], off offset:128 nt
	s_nop 0
	global_load_dwordx4 v[182:185], v201, s[42:43] offset:128 nt
	global_load_dwordx4 v[186:189], v201, s[42:43] offset:144 nt
	s_lshl_b64 s[70:71], s[48:49], 11
	s_add_u32 s37, s56, s70
	s_addc_u32 s47, s57, s71
	s_add_u32 s70, s37, s40
	s_addc_u32 s71, s47, s41
	s_lshl_b64 s[48:49], s[48:49], 10
	s_waitcnt vmcnt(7)
	ds_write_b128 v200, v[158:161]
	s_waitcnt vmcnt(6)
	ds_write_b128 v200, v[162:165] offset:1152
	s_add_u32 s37, s60, s48
	ds_read_b128 v[158:161], v206
	ds_read_b128 v[162:165], v206 offset:16
	s_addc_u32 s47, s61, s49
	v_lshl_add_u64 v[104:105], s[70:71], 0, v[114:115]
	v_lshl_add_u64 v[210:211], s[70:71], 0, v[116:117]
	s_add_u32 s70, s37, s38
	s_addc_u32 s71, s47, s39
	v_lshl_add_u64 v[212:213], v[104:105], 0, v[144:145]
	v_lshl_add_u64 v[104:105], s[70:71], 0, v[120:121]
	v_lshl_add_u64 v[214:215], v[104:105], 0, v[118:119]
	s_waitcnt vmcnt(5) lgkmcnt(1)
	v_pk_fma_f32 v[104:105], v[90:91], v[166:167], v[158:159]
	s_waitcnt vmcnt(4) lgkmcnt(0)
	v_pk_fma_f32 v[94:95], v[94:95], v[170:171], v[162:163]
	v_mov_b32_e32 v190, v139
	v_mov_b32_e32 v191, v139
	v_pk_fma_f32 v[92:93], v[92:93], v[168:169], v[160:161]
	v_pk_fma_f32 v[90:91], v[96:97], v[172:173], v[164:165]
	v_cvt_pk_bf16_f32 v158, v104, v105
	v_cvt_pk_bf16_f32 v159, v92, v93
	v_cvt_pk_bf16_f32 v160, v94, v95
	v_med3_f32 v96, v104, s68, v195
	v_cvt_pk_bf16_f32 v161, v90, v91
	v_med3_f32 v97, v94, s68, v195
	v_med3_f32 v162, v105, s68, v195
	v_med3_f32 v163, v95, s68, v195
	s_waitcnt vmcnt(3)
	ds_write_b128 v200, v[174:177]
	s_waitcnt vmcnt(2)
	ds_write_b128 v200, v[178:181] offset:1152
	v_cvt_pk_fp8_f32 v190, v96, v162
	v_cvt_pk_fp8_f32 v191, v97, v163
	ds_read_b128 v[162:165], v206
	ds_read_b128 v[166:169], v206 offset:16
	v_med3_f32 v171, v90, s68, v195
	v_med3_f32 v96, v91, s68, v195
	v_cvt_pk_fp8_f32 v191, v171, v96 op_sel:[0,0,1]
	s_waitcnt vmcnt(1) lgkmcnt(1)
	v_pk_fma_f32 v[96:97], v[82:83], v[182:183], v[162:163]
	s_waitcnt vmcnt(0) lgkmcnt(0)
	v_pk_fma_f32 v[86:87], v[86:87], v[186:187], v[166:167]
	v_pk_fma_f32 v[82:83], v[88:89], v[188:189], v[168:169]
	v_med3_f32 v88, v96, s68, v195
	v_med3_f32 v89, v86, s68, v195
	v_med3_f32 v166, v97, s68, v195
	v_med3_f32 v167, v87, s68, v195
	v_cvt_pk_fp8_f32 v208, v88, v166
	v_cvt_pk_fp8_f32 v209, v89, v167
	v_med3_f32 v170, v92, s68, v195
	v_med3_f32 v172, v93, s68, v195
	v_pk_fma_f32 v[84:85], v[84:85], v[184:185], v[164:165]
	v_cvt_pk_fp8_f32 v190, v170, v172 op_sel:[0,0,1]
	v_med3_f32 v168, v84, s68, v195
	v_med3_f32 v169, v82, s68, v195
	v_med3_f32 v170, v85, s68, v195
	v_med3_f32 v88, v83, s68, v195
	v_cvt_pk_fp8_f32 v208, v168, v170 op_sel:[0,0,1]
	v_cvt_pk_fp8_f32 v209, v169, v88 op_sel:[0,0,1]
	s_or_b32 s48, s46, 48
	s_ashr_i32 s49, s48, 31
	v_cvt_pk_bf16_f32 v162, v96, v97
	v_cvt_pk_bf16_f32 v163, v84, v85
	v_cvt_pk_bf16_f32 v164, v86, v87
	v_cvt_pk_bf16_f32 v165, v82, v83
	ds_write_b128 v203, v[158:161]
	ds_write_b128 v203, v[162:165] offset:64
	ds_read_b128 v[158:161], v200
	ds_read_b128 v[162:165], v200 offset:1152
	s_lshl_b64 s[70:71], s[48:49], 12
	ds_write2_b64 v204, v[190:191], v[208:209] offset1:4
	s_add_u32 s37, s10, s70
	ds_read_b128 v[166:169], v205
	s_addc_u32 s47, s11, s71
	s_add_u32 s70, s37, s44
	s_addc_u32 s71, s47, s45
	v_lshl_add_u64 v[210:211], v[210:211], 0, v[144:145]
	s_waitcnt lgkmcnt(3)
	global_store_dwordx4 v[212:213], v[158:161], off
	s_waitcnt lgkmcnt(2)
	global_store_dwordx4 v[210:211], v[162:165], off
	s_waitcnt lgkmcnt(0)
	global_store_dwordx4 v[214:215], v[166:169], off
	v_lshl_add_u64 v[88:89], s[70:71], 0, v[138:139]
	v_lshl_add_u64 v[88:89], v[88:89], 0, v[144:145]
	global_load_dwordx4 v[158:161], v[88:89], off nt
	v_lshl_add_u64 v[162:163], s[70:71], 0, v[146:147]
	v_lshl_add_u64 v[178:179], v[162:163], 0, v[144:145]
	global_load_dwordx4 v[162:165], v[178:179], off nt
	global_load_dwordx4 v[166:169], v201, s[42:43] nt
	global_load_dwordx4 v[170:173], v201, s[42:43] offset:16 nt
	global_load_dwordx4 v[174:177], v[88:89], off offset:128 nt
	s_nop 0
	global_load_dwordx4 v[178:181], v[178:179], off offset:128 nt
	s_nop 0
	global_load_dwordx4 v[182:185], v201, s[42:43] offset:128 nt
	global_load_dwordx4 v[186:189], v201, s[42:43] offset:144 nt
	s_lshl_b64 s[70:71], s[48:49], 11
	s_add_u32 s37, s56, s70
	s_addc_u32 s47, s57, s71
	s_add_u32 s70, s37, s40
	s_addc_u32 s71, s47, s41
	v_lshl_add_u64 v[208:209], s[70:71], 0, v[116:117]
	s_waitcnt vmcnt(7)
	ds_write_b128 v200, v[158:161]
	s_waitcnt vmcnt(6)
	ds_write_b128 v200, v[162:165] offset:1152
	v_lshl_add_u64 v[216:217], v[208:209], 0, v[144:145]
	ds_read_b128 v[158:161], v206
	ds_read_b128 v[208:211], v206 offset:16
	s_lshl_b64 s[48:49], s[48:49], 10
	v_mov_b32_e32 v190, v139
	v_mov_b32_e32 v191, v139
	s_waitcnt vmcnt(5) lgkmcnt(1)
	v_pk_fma_f32 v[164:165], v[74:75], v[166:167], v[158:159]
	s_waitcnt vmcnt(4) lgkmcnt(0)
	v_pk_fma_f32 v[166:167], v[78:79], v[170:171], v[208:209]
	s_add_u32 s37, s60, s48
	v_pk_fma_f32 v[160:161], v[76:77], v[168:169], v[160:161]
	v_pk_fma_f32 v[162:163], v[80:81], v[172:173], v[210:211]
	v_cvt_pk_bf16_f32 v74, v164, v165
	v_cvt_pk_bf16_f32 v75, v160, v161
	v_cvt_pk_bf16_f32 v76, v166, v167
	v_med3_f32 v78, v164, s68, v195
	v_cvt_pk_bf16_f32 v77, v162, v163
	v_med3_f32 v79, v166, s68, v195
	v_med3_f32 v80, v165, s68, v195
	v_med3_f32 v81, v167, s68, v195
	s_waitcnt vmcnt(3)
	ds_write_b128 v200, v[174:177]
	s_waitcnt vmcnt(2)
	ds_write_b128 v200, v[178:181] offset:1152
	s_addc_u32 s47, s61, s49
	v_cvt_pk_fp8_f32 v190, v78, v80
	v_cvt_pk_fp8_f32 v191, v79, v81
	ds_read_b128 v[78:81], v206
	ds_read_b128 v[172:175], v206 offset:16
	v_lshl_add_u64 v[88:89], s[70:71], 0, v[114:115]
	s_add_u32 s70, s37, s38
	s_addc_u32 s71, s47, s39
	v_lshl_add_u64 v[214:215], v[88:89], 0, v[144:145]
	v_lshl_add_u64 v[88:89], s[70:71], 0, v[120:121]
	v_lshl_add_u64 v[218:219], v[88:89], 0, v[118:119]
	v_med3_f32 v88, v160, s68, v195
	v_med3_f32 v89, v162, s68, v195
	v_med3_f32 v158, v161, s68, v195
	v_med3_f32 v159, v163, s68, v195
	v_cvt_pk_fp8_f32 v190, v88, v158 op_sel:[0,0,1]
	v_cvt_pk_fp8_f32 v191, v89, v159 op_sel:[0,0,1]
	s_waitcnt vmcnt(1) lgkmcnt(1)
	v_pk_fma_f32 v[170:171], v[66:67], v[182:183], v[78:79]
	s_waitcnt vmcnt(0) lgkmcnt(0)
	v_pk_fma_f32 v[158:159], v[70:71], v[186:187], v[172:173]
	v_mov_b32_e32 v212, v139
	v_mov_b32_e32 v213, v139
	v_pk_fma_f32 v[88:89], v[72:73], v[188:189], v[174:175]
	v_med3_f32 v70, v170, s68, v195
	v_med3_f32 v71, v158, s68, v195
	v_med3_f32 v72, v171, s68, v195
	v_med3_f32 v73, v159, s68, v195
	v_cvt_pk_fp8_f32 v212, v70, v72
	v_cvt_pk_fp8_f32 v213, v71, v73
	v_pk_fma_f32 v[168:169], v[68:69], v[184:185], v[80:81]
	v_med3_f32 v79, v88, s68, v195
	v_med3_f32 v78, v168, s68, v195
	v_med3_f32 v80, v169, s68, v195
	v_med3_f32 v70, v89, s68, v195
	v_cvt_pk_fp8_f32 v212, v78, v80 op_sel:[0,0,1]
	v_cvt_pk_fp8_f32 v213, v79, v70 op_sel:[0,0,1]
	s_add_i32 s48, s46, 0x80
	s_ashr_i32 s49, s48, 31
	v_cvt_pk_bf16_f32 v66, v170, v171
	v_cvt_pk_bf16_f32 v67, v168, v169
	v_cvt_pk_bf16_f32 v68, v158, v159
	v_cvt_pk_bf16_f32 v69, v88, v89
	ds_write_b128 v203, v[74:77]
	ds_write_b128 v203, v[66:69] offset:64
	s_lshl_b64 s[70:71], s[48:49], 12
	ds_read_b128 v[66:69], v200
	ds_read_b128 v[70:73], v200 offset:1152
	s_add_u32 s37, s10, s70
	ds_write2_b64 v204, v[190:191], v[212:213] offset1:4
	s_addc_u32 s47, s11, s71
	ds_read_b128 v[74:77], v205
	s_add_u32 s70, s37, s44
	s_addc_u32 s71, s47, s45
	v_lshl_add_u64 v[220:221], s[70:71], 0, v[138:139]
	s_waitcnt lgkmcnt(3)
	global_store_dwordx4 v[214:215], v[66:69], off
	s_waitcnt lgkmcnt(2)
	global_store_dwordx4 v[216:217], v[70:73], off
	s_waitcnt lgkmcnt(0)
	global_store_dwordx4 v[218:219], v[74:77], off
	v_lshl_add_u64 v[222:223], s[70:71], 0, v[146:147]
	v_lshl_add_u64 v[172:173], v[220:221], 0, v[144:145]
	v_lshl_add_u64 v[174:175], v[222:223], 0, v[144:145]
	global_load_dwordx4 v[66:69], v[172:173], off nt
	global_load_dwordx4 v[70:73], v[174:175], off nt
	global_load_dwordx4 v[74:77], v201, s[42:43] nt
	global_load_dwordx4 v[78:81], v201, s[42:43] offset:16 nt
	global_load_dwordx4 v[180:183], v[172:173], off offset:128 nt
	global_load_dwordx4 v[184:187], v[174:175], off offset:128 nt
	global_load_dwordx4 v[188:191], v201, s[42:43] offset:128 nt
	global_load_dwordx4 v[208:211], v201, s[42:43] offset:144 nt
	s_lshl_b64 s[70:71], s[48:49], 11
	s_add_u32 s37, s56, s70
	s_addc_u32 s47, s57, s71
	s_add_u32 s70, s37, s40
	s_waitcnt vmcnt(7)
	ds_write_b128 v200, v[66:69]
	s_waitcnt vmcnt(6)
	ds_write_b128 v200, v[70:73] offset:1152
	s_addc_u32 s71, s47, s41
	s_lshl_b64 s[48:49], s[48:49], 10
	ds_read_b128 v[66:69], v206
	ds_read_b128 v[70:73], v206 offset:16
	s_add_u32 s37, s60, s48
	s_addc_u32 s47, s61, s49
	v_lshl_add_u64 v[172:173], s[70:71], 0, v[114:115]
	v_lshl_add_u64 v[174:175], s[70:71], 0, v[116:117]
	s_add_u32 s70, s37, s38
	s_addc_u32 s71, s47, s39
	v_lshl_add_u64 v[216:217], v[172:173], 0, v[144:145]
	v_lshl_add_u64 v[172:173], s[70:71], 0, v[120:121]
	s_waitcnt vmcnt(5) lgkmcnt(1)
	v_pk_fma_f32 v[178:179], v[58:59], v[74:75], v[66:67]
	s_waitcnt vmcnt(4) lgkmcnt(0)
	v_pk_fma_f32 v[176:177], v[62:63], v[78:79], v[70:71]
	v_mov_b32_e32 v212, v139
	v_mov_b32_e32 v213, v139
	v_lshl_add_u64 v[218:219], v[174:175], 0, v[144:145]
	v_lshl_add_u64 v[220:221], v[172:173], 0, v[118:119]
	v_pk_fma_f32 v[174:175], v[60:61], v[76:77], v[68:69]
	v_pk_fma_f32 v[172:173], v[64:65], v[80:81], v[72:73]
	v_cvt_pk_bf16_f32 v58, v178, v179
	v_cvt_pk_bf16_f32 v59, v174, v175
	v_cvt_pk_bf16_f32 v60, v176, v177
	v_med3_f32 v62, v178, s68, v195
	v_cvt_pk_bf16_f32 v61, v172, v173
	v_med3_f32 v63, v176, s68, v195
	v_med3_f32 v64, v179, s68, v195
	v_med3_f32 v65, v177, s68, v195
	s_waitcnt vmcnt(3)
	ds_write_b128 v200, v[180:183]
	s_waitcnt vmcnt(2)
	ds_write_b128 v200, v[184:187] offset:1152
	v_cvt_pk_fp8_f32 v212, v62, v64
	v_cvt_pk_fp8_f32 v213, v63, v65
	ds_read_b128 v[62:65], v206
	ds_read_b128 v[66:69], v206 offset:16
	v_mov_b32_e32 v214, v139
	v_mov_b32_e32 v215, v139
	v_med3_f32 v70, v174, s68, v195
	s_waitcnt vmcnt(1) lgkmcnt(1)
	v_pk_fma_f32 v[186:187], v[50:51], v[188:189], v[62:63]
	s_waitcnt vmcnt(0) lgkmcnt(0)
	v_pk_fma_f32 v[184:185], v[54:55], v[208:209], v[66:67]
	v_pk_fma_f32 v[180:181], v[56:57], v[210:211], v[68:69]
	v_med3_f32 v54, v186, s68, v195
	v_med3_f32 v55, v184, s68, v195
	v_med3_f32 v56, v187, s68, v195
	v_med3_f32 v57, v185, s68, v195
	v_cvt_pk_fp8_f32 v214, v54, v56
	v_cvt_pk_fp8_f32 v215, v55, v57
	v_pk_fma_f32 v[182:183], v[52:53], v[190:191], v[64:65]
	v_med3_f32 v71, v172, s68, v195
	v_med3_f32 v72, v175, s68, v195
	v_med3_f32 v73, v173, s68, v195
	v_med3_f32 v62, v182, s68, v195
	v_med3_f32 v63, v180, s68, v195
	v_med3_f32 v64, v183, s68, v195
	v_med3_f32 v54, v181, s68, v195
	v_cvt_pk_fp8_f32 v212, v70, v72 op_sel:[0,0,1]
	v_cvt_pk_fp8_f32 v213, v71, v73 op_sel:[0,0,1]
	v_cvt_pk_fp8_f32 v214, v62, v64 op_sel:[0,0,1]
	v_cvt_pk_fp8_f32 v215, v63, v54 op_sel:[0,0,1]
	s_add_i32 s48, s46, 0x90
	s_ashr_i32 s49, s48, 31
	v_cvt_pk_bf16_f32 v50, v186, v187
	v_cvt_pk_bf16_f32 v51, v182, v183
	v_cvt_pk_bf16_f32 v52, v184, v185
	v_cvt_pk_bf16_f32 v53, v180, v181
	ds_write_b128 v203, v[58:61]
	ds_write_b128 v203, v[50:53] offset:64
	s_lshl_b64 s[70:71], s[48:49], 12
	ds_read_b128 v[50:53], v200
	ds_read_b128 v[54:57], v200 offset:1152
	s_add_u32 s37, s10, s70
	ds_write2_b64 v204, v[212:213], v[214:215] offset1:4
	s_addc_u32 s47, s11, s71
	ds_read_b128 v[58:61], v205
	s_add_u32 s70, s37, s44
	s_addc_u32 s71, s47, s45
	v_lshl_add_u64 v[222:223], s[70:71], 0, v[138:139]
	v_lshl_add_u64 v[224:225], s[70:71], 0, v[146:147]
	s_waitcnt lgkmcnt(3)
	global_store_dwordx4 v[216:217], v[50:53], off
	s_waitcnt lgkmcnt(2)
	global_store_dwordx4 v[218:219], v[54:57], off
	s_waitcnt lgkmcnt(0)
	global_store_dwordx4 v[220:221], v[58:61], off
	v_lshl_add_u64 v[62:63], v[222:223], 0, v[144:145]
	v_lshl_add_u64 v[64:65], v[224:225], 0, v[144:145]
	global_load_dwordx4 v[74:77], v[62:63], off nt
	global_load_dwordx4 v[78:81], v[64:65], off nt
	global_load_dwordx4 v[70:73], v201, s[42:43] nt
	global_load_dwordx4 v[66:69], v201, s[42:43] offset:16 nt
	global_load_dwordx4 v[58:61], v[62:63], off offset:128 nt
	s_nop 0
	global_load_dwordx4 v[62:65], v[64:65], off offset:128 nt
	s_nop 0
	global_load_dwordx4 v[54:57], v201, s[42:43] offset:128 nt
	global_load_dwordx4 v[50:53], v201, s[42:43] offset:144 nt
	s_waitcnt vmcnt(7)
	ds_write_b128 v200, v[74:77]
	s_waitcnt vmcnt(6)
	ds_write_b128 v200, v[78:81] offset:1152
	ds_read_b128 v[74:77], v206
	ds_read_b128 v[78:81], v206 offset:16
	v_mov_b32_e32 v190, v139
	v_mov_b32_e32 v191, v139
	s_lshl_b64 s[70:71], s[48:49], 11
	s_waitcnt vmcnt(5) lgkmcnt(1)
	v_pk_fma_f32 v[72:73], v[44:45], v[72:73], v[76:77]
	v_pk_fma_f32 v[70:71], v[42:43], v[70:71], v[74:75]
	s_waitcnt vmcnt(4) lgkmcnt(0)
	v_pk_fma_f32 v[44:45], v[46:47], v[66:67], v[78:79]
	v_pk_fma_f32 v[42:43], v[48:49], v[68:69], v[80:81]
	v_cvt_pk_bf16_f32 v66, v70, v71
	v_cvt_pk_bf16_f32 v67, v72, v73
	v_cvt_pk_bf16_f32 v68, v44, v45
	v_med3_f32 v46, v70, s68, v195
	v_cvt_pk_bf16_f32 v69, v42, v43
	v_med3_f32 v47, v44, s68, v195
	v_med3_f32 v48, v71, s68, v195
	v_med3_f32 v49, v45, s68, v195
	s_waitcnt vmcnt(3)
	ds_write_b128 v200, v[58:61]
	s_waitcnt vmcnt(2)
	ds_write_b128 v200, v[62:65] offset:1152
	v_cvt_pk_fp8_f32 v190, v46, v48
	v_cvt_pk_fp8_f32 v191, v47, v49
	ds_read_b128 v[46:49], v206
	ds_read_b128 v[58:61], v206 offset:16
	s_add_u32 s37, s56, s70
	v_mov_b32_e32 v208, v139
	v_mov_b32_e32 v209, v139
	s_waitcnt vmcnt(1) lgkmcnt(1)
	v_pk_fma_f32 v[46:47], v[34:35], v[54:55], v[46:47]
	s_waitcnt vmcnt(0) lgkmcnt(0)
	v_pk_fma_f32 v[38:39], v[38:39], v[50:51], v[58:59]
	s_addc_u32 s47, s57, s71
	v_pk_fma_f32 v[34:35], v[40:41], v[52:53], v[60:61]
	v_med3_f32 v40, v46, s68, v195
	v_med3_f32 v41, v38, s68, v195
	v_med3_f32 v52, v47, s68, v195
	v_med3_f32 v53, v39, s68, v195
	s_add_u32 s70, s37, s40
	v_cvt_pk_fp8_f32 v208, v40, v52
	v_cvt_pk_fp8_f32 v209, v41, v53
	s_addc_u32 s71, s47, s41
	s_lshl_b64 s[48:49], s[48:49], 10
	s_add_u32 s37, s60, s48
	v_pk_fma_f32 v[36:37], v[36:37], v[56:57], v[48:49]
	s_addc_u32 s47, s61, s49
	v_med3_f32 v74, v72, s68, v195
	v_med3_f32 v75, v42, s68, v195
	v_med3_f32 v76, v73, s68, v195
	v_med3_f32 v62, v43, s68, v195
	v_med3_f32 v54, v36, s68, v195
	v_med3_f32 v55, v34, s68, v195
	v_med3_f32 v56, v37, s68, v195
	v_med3_f32 v40, v35, s68, v195
	v_lshl_add_u64 v[210:211], s[70:71], 0, v[114:115]
	v_lshl_add_u64 v[212:213], s[70:71], 0, v[116:117]
	s_add_u32 s70, s37, s38
	v_cvt_pk_fp8_f32 v190, v74, v76 op_sel:[0,0,1]
	v_cvt_pk_fp8_f32 v191, v75, v62 op_sel:[0,0,1]
	v_cvt_pk_fp8_f32 v208, v54, v56 op_sel:[0,0,1]
	v_cvt_pk_fp8_f32 v209, v55, v40 op_sel:[0,0,1]
	s_addc_u32 s71, s47, s39
	s_add_i32 s48, s46, 0xa0
	s_ashr_i32 s49, s48, 31
	v_cvt_pk_bf16_f32 v48, v46, v47
	v_cvt_pk_bf16_f32 v49, v36, v37
	v_cvt_pk_bf16_f32 v50, v38, v39
	v_cvt_pk_bf16_f32 v51, v34, v35
	ds_write_b128 v203, v[66:69]
	ds_write_b128 v203, v[48:51] offset:64
	v_lshl_add_u64 v[214:215], s[70:71], 0, v[120:121]
	s_lshl_b64 s[70:71], s[48:49], 12
	ds_read_b128 v[48:51], v200
	ds_read_b128 v[52:55], v200 offset:1152
	s_add_u32 s37, s10, s70
	ds_write2_b64 v204, v[190:191], v[208:209] offset1:4
	s_addc_u32 s47, s11, s71
	ds_read_b128 v[56:59], v205
	s_add_u32 s70, s37, s44
	v_lshl_add_u64 v[210:211], v[210:211], 0, v[144:145]
	s_addc_u32 s71, s47, s45
	v_lshl_add_u64 v[212:213], v[212:213], 0, v[144:145]
	v_lshl_add_u64 v[214:215], v[214:215], 0, v[118:119]
	v_lshl_add_u64 v[216:217], s[70:71], 0, v[138:139]
	s_waitcnt lgkmcnt(3)
	global_store_dwordx4 v[210:211], v[48:51], off
	s_waitcnt lgkmcnt(2)
	global_store_dwordx4 v[212:213], v[52:55], off
	s_waitcnt lgkmcnt(0)
	global_store_dwordx4 v[214:215], v[56:59], off
	v_lshl_add_u64 v[218:219], s[70:71], 0, v[146:147]
	v_lshl_add_u64 v[216:217], v[216:217], 0, v[144:145]
	v_lshl_add_u64 v[218:219], v[218:219], 0, v[144:145]
	global_load_dwordx4 v[48:51], v[216:217], off nt
	global_load_dwordx4 v[52:55], v[218:219], off nt
	v_mul_f32_e32 v41, v127, v127
	v_mul_f32_e32 v64, v123, v123
	v_mul_f32_e32 v65, v129, v129
	v_mul_f32_e32 v66, v125, v125
	v_fmac_f32_e32 v41, v126, v126
	v_fmac_f32_e32 v64, v122, v122
	v_fmac_f32_e32 v65, v128, v128
	v_fmac_f32_e32 v66, v124, v124
	global_load_dwordx4 v[56:59], v201, s[42:43] offset:16 nt
	global_load_dwordx4 v[60:63], v201, s[42:43] nt
	v_add_f32_e32 v41, v41, v64
	v_add_f32_e32 v64, v65, v66
	v_add_f32_e32 v41, v41, v64
	global_load_dwordx4 v[64:67], v[216:217], off offset:128 nt
	global_load_dwordx4 v[74:77], v[218:219], off offset:128 nt
	v_mul_f32_e32 v155, v155, v155
	v_mul_f32_e32 v153, v153, v153
	v_mul_f32_e32 v151, v151, v151
	v_mul_f32_e32 v149, v149, v149
	v_fmac_f32_e32 v155, v154, v154
	v_fmac_f32_e32 v153, v152, v152
	v_fmac_f32_e32 v151, v150, v150
	v_fmac_f32_e32 v149, v148, v148
	v_add_f32_e32 v148, v155, v153
	v_add_f32_e32 v40, v151, v149
	v_add_f32_e32 v40, v148, v40
	v_add_f32_e32 v122, v40, v41
	v_mul_f32_e32 v41, v109, v109
	v_mul_f32_e32 v69, v107, v107
	v_fmac_f32_e32 v41, v108, v108
	v_fmac_f32_e32 v69, v106, v106
	global_load_dwordx4 v[78:81], v201, s[42:43] offset:144 nt
	global_load_dwordx4 v[106:109], v201, s[42:43] offset:128 nt
	v_mul_f32_e32 v40, v157, v157
	v_mul_f32_e32 v68, v111, v111
	v_fmac_f32_e32 v40, v156, v156
	v_fmac_f32_e32 v68, v110, v110
	v_add_f32_e32 v40, v40, v41
	v_add_f32_e32 v41, v68, v69
	v_add_f32_e32 v40, v40, v41
	v_mul_f32_e32 v41, v113, v113
	v_mul_f32_e32 v68, v101, v101
	v_mul_f32_e32 v69, v103, v103
	v_mul_f32_e32 v99, v99, v99
	v_fmac_f32_e32 v41, v112, v112
	v_fmac_f32_e32 v68, v100, v100
	v_fmac_f32_e32 v69, v102, v102
	v_fmac_f32_e32 v99, v98, v98
	v_add_f32_e32 v41, v41, v68
	v_add_f32_e32 v68, v69, v99
	v_add_f32_e32 v41, v41, v68
	v_add_f32_e32 v98, v40, v41
	v_mul_f32_e32 v40, v105, v105
	v_mul_f32_e32 v41, v93, v93
	v_mul_f32_e32 v68, v95, v95
	v_mul_f32_e32 v69, v91, v91
	v_fmac_f32_e32 v40, v104, v104
	v_fmac_f32_e32 v41, v92, v92
	v_fmac_f32_e32 v68, v94, v94
	v_fmac_f32_e32 v69, v90, v90
	v_add_f32_e32 v40, v40, v41
	v_add_f32_e32 v41, v68, v69
	v_add_f32_e32 v40, v40, v41
	v_mul_f32_e32 v41, v97, v97
	v_mul_f32_e32 v68, v85, v85
	v_mul_f32_e32 v69, v87, v87
	v_mul_f32_e32 v83, v83, v83
	v_fmac_f32_e32 v41, v96, v96
	v_fmac_f32_e32 v68, v84, v84
	v_fmac_f32_e32 v69, v86, v86
	v_fmac_f32_e32 v83, v82, v82
	v_add_f32_e32 v41, v41, v68
	v_add_f32_e32 v68, v69, v83
	s_waitcnt vmcnt(7)
	ds_write_b128 v200, v[48:51]
	s_waitcnt vmcnt(6)
	ds_write_b128 v200, v[52:55] offset:1152
	v_add_f32_e32 v41, v41, v68
	ds_read_b128 v[48:51], v206
	ds_read_b128 v[52:55], v206 offset:16
	v_add_f32_e32 v86, v40, v41
	v_mul_f32_e32 v40, v165, v165
	v_mul_f32_e32 v41, v161, v161
	v_mul_f32_e32 v68, v167, v167
	v_mul_f32_e32 v69, v163, v163
	v_fmac_f32_e32 v40, v164, v164
	v_fmac_f32_e32 v41, v160, v160
	v_fmac_f32_e32 v68, v166, v166
	v_fmac_f32_e32 v69, v162, v162
	v_add_f32_e32 v40, v40, v41
	v_add_f32_e32 v41, v68, v69
	v_add_f32_e32 v87, v40, v41
	v_mul_f32_e32 v40, v171, v171
	v_mul_f32_e32 v41, v169, v169
	v_fmac_f32_e32 v40, v170, v170
	v_fmac_f32_e32 v41, v168, v168
	s_waitcnt vmcnt(4) lgkmcnt(1)
	v_pk_fma_f32 v[68:69], v[26:27], v[60:61], v[48:49]
	s_waitcnt lgkmcnt(0)
	v_pk_fma_f32 v[84:85], v[30:31], v[56:57], v[52:53]
	v_mov_b32_e32 v188, v139
	v_mov_b32_e32 v189, v139
	v_add_f32_e32 v91, v40, v41
	v_pk_fma_f32 v[40:41], v[28:29], v[62:63], v[50:51]
	v_pk_fma_f32 v[82:83], v[32:33], v[58:59], v[54:55]
	v_cvt_pk_bf16_f32 v26, v68, v69
	v_cvt_pk_bf16_f32 v27, v40, v41
	v_cvt_pk_bf16_f32 v28, v84, v85
	v_med3_f32 v30, v68, s68, v195
	v_cvt_pk_bf16_f32 v29, v82, v83
	v_med3_f32 v31, v84, s68, v195
	v_med3_f32 v32, v69, s68, v195
	v_med3_f32 v33, v85, s68, v195
	s_waitcnt vmcnt(3)
	ds_write_b128 v200, v[64:67]
	s_waitcnt vmcnt(2)
	ds_write_b128 v200, v[74:77] offset:1152
	v_cvt_pk_fp8_f32 v188, v30, v32
	v_cvt_pk_fp8_f32 v189, v31, v33
	ds_read_b128 v[30:33], v206
	ds_read_b128 v[48:51], v206 offset:16
	s_lshl_b64 s[70:71], s[48:49], 11
	s_add_u32 s37, s56, s70
	s_addc_u32 s47, s57, s71
	s_waitcnt vmcnt(0) lgkmcnt(1)
	v_pk_fma_f32 v[66:67], v[22:23], v[106:107], v[30:31]
	s_waitcnt lgkmcnt(0)
	v_pk_fma_f32 v[76:77], v[18:19], v[78:79], v[48:49]
	v_pk_fma_f32 v[64:65], v[24:25], v[108:109], v[32:33]
	v_med3_f32 v22, v66, s68, v195
	v_med3_f32 v23, v76, s68, v195
	v_med3_f32 v24, v67, s68, v195
	v_med3_f32 v25, v77, s68, v195
	v_mov_b32_e32 v30, v139
	v_mov_b32_e32 v31, v139
	v_cvt_pk_fp8_f32 v30, v22, v24
	v_cvt_pk_fp8_f32 v31, v23, v25
	v_pk_fma_f32 v[74:75], v[20:21], v[80:81], v[50:51]
	v_cvt_pk_bf16_f32 v18, v66, v67
	v_cvt_pk_bf16_f32 v19, v64, v65
	v_cvt_pk_bf16_f32 v20, v76, v77
	s_add_u32 s70, s37, s40
	v_cvt_pk_bf16_f32 v21, v74, v75
	ds_write_b128 v203, v[26:29]
	ds_write_b128 v203, v[18:21] offset:64
	ds_read_b128 v[18:21], v200
	v_med3_f32 v52, v40, s68, v195
	v_med3_f32 v53, v82, s68, v195
	v_med3_f32 v54, v41, s68, v195
	v_med3_f32 v55, v83, s68, v195
	v_med3_f32 v32, v64, s68, v195
	v_med3_f32 v33, v74, s68, v195
	v_med3_f32 v22, v65, s68, v195
	v_med3_f32 v23, v75, s68, v195
	s_addc_u32 s71, s47, s41
	s_lshl_b64 s[48:49], s[48:49], 10
	v_cvt_pk_fp8_f32 v188, v52, v54 op_sel:[0,0,1]
	v_cvt_pk_fp8_f32 v189, v53, v55 op_sel:[0,0,1]
	v_cvt_pk_fp8_f32 v30, v32, v22 op_sel:[0,0,1]
	v_cvt_pk_fp8_f32 v31, v33, v23 op_sel:[0,0,1]
	ds_read_b128 v[22:25], v200 offset:1152
	s_add_u32 s37, s60, s48
	v_lshl_add_u64 v[26:27], s[70:71], 0, v[114:115]
	s_addc_u32 s47, s61, s49
	v_lshl_add_u64 v[26:27], v[26:27], 0, v[144:145]
	s_add_u32 s48, s37, s38
	s_waitcnt lgkmcnt(1)
	global_store_dwordx4 v[26:27], v[18:21], off
	s_addc_u32 s49, s47, s39
	s_addk_i32 s46, 0xb0
	v_lshl_add_u64 v[18:19], s[70:71], 0, v[116:117]
	v_lshl_add_u64 v[18:19], v[18:19], 0, v[144:145]
	ds_write2_b64 v204, v[188:189], v[30:31] offset1:4
	s_ashr_i32 s47, s46, 31
	s_waitcnt lgkmcnt(1)
	global_store_dwordx4 v[18:19], v[22:25], off
	ds_read_b128 v[18:21], v205
	v_mul_f32_e32 v90, v159, v159
	v_lshl_add_u64 v[22:23], s[48:49], 0, v[120:121]
	s_lshl_b64 s[48:49], s[46:47], 12
	s_add_u32 s37, s10, s48
	s_addc_u32 s48, s11, s49
	s_add_u32 s44, s37, s44
	v_lshl_add_u64 v[22:23], v[22:23], 0, v[118:119]
	s_addc_u32 s45, s48, s45
	v_mul_f32_e32 v26, v89, v89
	s_waitcnt lgkmcnt(0)
	global_store_dwordx4 v[22:23], v[18:21], off
	v_fmac_f32_e32 v90, v158, v158
	v_fmac_f32_e32 v26, v88, v88
	v_lshl_add_u64 v[18:19], s[44:45], 0, v[138:139]
	v_lshl_add_u64 v[48:49], v[18:19], 0, v[144:145]
	v_lshl_add_u64 v[22:23], s[44:45], 0, v[146:147]
	v_add_f32_e32 v50, v90, v26
	global_load_dwordx4 v[18:21], v[48:49], off nt
	v_lshl_add_u64 v[52:53], v[22:23], 0, v[144:145]
	v_add_f32_e32 v50, v91, v50
	global_load_dwordx4 v[22:25], v[52:53], off nt
	v_add_f32_e32 v78, v87, v50
	v_mul_f32_e32 v50, v179, v179
	v_mul_f32_e32 v51, v175, v175
	v_fmac_f32_e32 v50, v178, v178
	v_fmac_f32_e32 v51, v174, v174
	v_add_f32_e32 v50, v50, v51
	v_mul_f32_e32 v51, v177, v177
	v_mul_f32_e32 v54, v173, v173
	v_fmac_f32_e32 v51, v176, v176
	v_fmac_f32_e32 v54, v172, v172
	v_add_f32_e32 v51, v51, v54
	global_load_dwordx4 v[26:29], v201, s[42:43] offset:16 nt
	global_load_dwordx4 v[30:33], v201, s[42:43] nt
	v_add_f32_e32 v50, v50, v51
	v_mul_f32_e32 v51, v187, v187
	v_mul_f32_e32 v54, v183, v183
	v_fmac_f32_e32 v51, v186, v186
	v_fmac_f32_e32 v54, v182, v182
	v_add_f32_e32 v51, v51, v54
	v_mul_f32_e32 v54, v185, v185
	v_mul_f32_e32 v55, v181, v181
	v_fmac_f32_e32 v54, v184, v184
	v_fmac_f32_e32 v55, v180, v180
	v_add_f32_e32 v54, v54, v55
	v_add_f32_e32 v51, v51, v54
	v_add_f32_e32 v79, v50, v51
	global_load_dwordx4 v[48:51], v[48:49], off offset:128 nt
	s_nop 0
	global_load_dwordx4 v[52:55], v[52:53], off offset:128 nt
	v_mul_f32_e32 v56, v71, v71
	v_mul_f32_e32 v57, v73, v73
	v_fmac_f32_e32 v56, v70, v70
	v_fmac_f32_e32 v57, v72, v72
	v_add_f32_e32 v70, v56, v57
	global_load_dwordx4 v[56:59], v201, s[42:43] offset:144 nt
	global_load_dwordx4 v[60:63], v201, s[42:43] offset:128 nt
	s_waitcnt vmcnt(7)
	ds_write_b128 v200, v[18:21]
	s_waitcnt vmcnt(6)
	ds_write_b128 v200, v[22:25] offset:1152
	ds_read_b128 v[18:21], v206
	ds_read_b128 v[22:25], v206 offset:16
	v_mul_f32_e32 v45, v45, v45
	v_mul_f32_e32 v43, v43, v43
	v_fmac_f32_e32 v45, v44, v44
	v_fmac_f32_e32 v43, v42, v42
	v_add_f32_e32 v42, v45, v43
	v_mul_f32_e32 v43, v47, v47
	v_mul_f32_e32 v37, v37, v37
	s_lshl_b64 s[42:43], s[46:47], 11
	v_fmac_f32_e32 v43, v46, v46
	v_fmac_f32_e32 v37, v36, v36
	s_waitcnt vmcnt(4) lgkmcnt(1)
	v_pk_fma_f32 v[16:17], v[16:17], v[32:33], v[20:21]
	v_pk_fma_f32 v[14:15], v[14:15], v[30:31], v[18:19]
	s_waitcnt lgkmcnt(0)
	v_pk_fma_f32 v[20:21], v[10:11], v[26:27], v[22:23]
	v_mul_f32_e32 v10, v15, v15
	v_mul_f32_e32 v11, v17, v17
	v_pk_fma_f32 v[18:19], v[12:13], v[28:29], v[24:25]
	v_fmac_f32_e32 v10, v14, v14
	v_fmac_f32_e32 v11, v16, v16
	v_add_f32_e32 v10, v10, v11
	v_mul_f32_e32 v11, v21, v21
	v_mul_f32_e32 v12, v19, v19
	v_fmac_f32_e32 v11, v20, v20
	v_fmac_f32_e32 v12, v18, v18
	v_add_f32_e32 v11, v11, v12
	v_add_f32_e32 v24, v10, v11
	v_cvt_pk_bf16_f32 v10, v14, v15
	v_cvt_pk_bf16_f32 v11, v16, v17
	v_cvt_pk_bf16_f32 v12, v20, v21
	v_cvt_pk_bf16_f32 v13, v18, v19
	v_med3_f32 v14, v14, s68, v195
	v_med3_f32 v15, v15, s68, v195
	v_mov_b32_e32 v22, v139
	s_waitcnt vmcnt(3)
	ds_write_b128 v200, v[48:51]
	s_waitcnt vmcnt(2)
	ds_write_b128 v200, v[52:55] offset:1152
	v_med3_f32 v20, v20, s68, v195
	v_med3_f32 v21, v21, s68, v195
	v_med3_f32 v25, v16, s68, v195
	v_med3_f32 v27, v17, s68, v195
	v_cvt_pk_fp8_f32 v22, v14, v15
	v_mov_b32_e32 v23, v139
	ds_read_b128 v[14:17], v206
	v_med3_f32 v26, v18, s68, v195
	v_cvt_pk_fp8_f32 v23, v20, v21
	v_med3_f32 v28, v19, s68, v195
	ds_read_b128 v[18:21], v206 offset:16
	s_waitcnt vmcnt(0) lgkmcnt(1)
	v_pk_fma_f32 v[8:9], v[8:9], v[62:63], v[16:17]
	v_pk_fma_f32 v[6:7], v[6:7], v[60:61], v[14:15]
	s_add_u32 s37, s56, s42
	v_add_f32_e32 v36, v43, v37
	s_waitcnt lgkmcnt(0)
	v_pk_fma_f32 v[16:17], v[2:3], v[56:57], v[18:19]
	v_mul_f32_e32 v2, v7, v7
	v_mul_f32_e32 v3, v9, v9
	v_pk_fma_f32 v[14:15], v[4:5], v[58:59], v[20:21]
	v_fmac_f32_e32 v2, v6, v6
	v_fmac_f32_e32 v3, v8, v8
	v_add_f32_e32 v2, v2, v3
	v_mul_f32_e32 v3, v17, v17
	v_mul_f32_e32 v4, v15, v15
	v_fmac_f32_e32 v3, v16, v16
	v_fmac_f32_e32 v4, v14, v14
	v_add_f32_e32 v3, v3, v4
	v_add_f32_e32 v2, v2, v3
	v_add_f32_e32 v18, v24, v2
	v_cvt_pk_bf16_f32 v2, v6, v7
	v_cvt_pk_bf16_f32 v3, v8, v9
	v_cvt_pk_bf16_f32 v4, v16, v17
	v_med3_f32 v6, v6, s68, v195
	v_med3_f32 v19, v16, s68, v195
	v_med3_f32 v7, v7, s68, v195
	v_med3_f32 v20, v17, s68, v195
	v_mov_b32_e32 v16, v139
	v_mov_b32_e32 v17, v139
	v_cvt_pk_fp8_f32 v16, v6, v7
	v_cvt_pk_fp8_f32 v17, v19, v20
	v_cvt_pk_bf16_f32 v5, v14, v15
	ds_write_b128 v203, v[10:13]
	ds_write_b128 v203, v[2:5] offset:64
	v_mul_f32_e32 v37, v39, v39
	v_mul_f32_e32 v35, v35, v35
	s_addc_u32 s42, s57, s43
	ds_read_b128 v[2:5], v200
	v_fmac_f32_e32 v37, v38, v38
	v_fmac_f32_e32 v35, v34, v34
	v_med3_f32 v8, v8, s68, v195
	v_med3_f32 v14, v14, s68, v195
	v_med3_f32 v6, v9, s68, v195
	v_med3_f32 v7, v15, s68, v195
	s_add_u32 s40, s37, s40
	v_add_f32_e32 v34, v37, v35
	v_cvt_pk_fp8_f32 v22, v25, v27 op_sel:[0,0,1]
	v_cvt_pk_fp8_f32 v23, v26, v28 op_sel:[0,0,1]
	v_cvt_pk_fp8_f32 v16, v8, v6 op_sel:[0,0,1]
	v_cvt_pk_fp8_f32 v17, v14, v7 op_sel:[0,0,1]
	s_addc_u32 s41, s42, s41
	ds_read_b128 v[6:9], v200 offset:1152
	v_add_f32_e32 v34, v36, v34
	v_mul_f32_e32 v35, v69, v69
	v_mul_f32_e32 v36, v41, v41
	v_lshl_add_u64 v[10:11], s[40:41], 0, v[114:115]
	v_fmac_f32_e32 v35, v68, v68
	v_fmac_f32_e32 v36, v40, v40
	v_lshl_add_u64 v[10:11], v[10:11], 0, v[144:145]
	v_add_f32_e32 v35, v35, v36
	v_mul_f32_e32 v36, v85, v85
	v_mul_f32_e32 v37, v83, v83
	s_waitcnt lgkmcnt(1)
	global_store_dwordx4 v[10:11], v[2:5], off
	v_fmac_f32_e32 v36, v84, v84
	v_fmac_f32_e32 v37, v82, v82
	v_lshl_add_u64 v[2:3], s[40:41], 0, v[116:117]
	s_lshl_b64 s[40:41], s[46:47], 10
	v_lshl_add_u64 v[2:3], v[2:3], 0, v[144:145]
	s_add_u32 s37, s60, s40
	ds_write2_b64 v204, v[22:23], v[16:17] offset1:4
	v_add_f32_e32 v36, v36, v37
	s_waitcnt lgkmcnt(1)
	global_store_dwordx4 v[2:3], v[6:9], off
	s_addc_u32 s40, s61, s41
	ds_read_b128 v[2:5], v205
	v_add_f32_e32 v35, v35, v36
	v_mul_f32_e32 v36, v67, v67
	v_mul_f32_e32 v37, v65, v65
	s_add_u32 s38, s37, s38
	v_fmac_f32_e32 v36, v66, v66
	v_fmac_f32_e32 v37, v64, v64
	s_addc_u32 s39, s40, s39
	v_add_f32_e32 v36, v36, v37
	v_mul_f32_e32 v37, v77, v77
	v_mul_f32_e32 v38, v75, v75
	v_lshl_add_u64 v[6:7], s[38:39], 0, v[120:121]
	v_fmac_f32_e32 v37, v76, v76
	v_fmac_f32_e32 v38, v74, v74
	v_lshl_add_u64 v[6:7], v[6:7], 0, v[118:119]
	v_add_f32_e32 v37, v37, v38
	s_waitcnt lgkmcnt(0)
	global_store_dwordx4 v[6:7], v[2:5], off
	s_lshl_b32 s35, s35, 2
	v_add_f32_e32 v42, v70, v42
	v_lshlrev_b32_e32 v2, 2, v198
	v_lshlrev_b32_e32 v3, 4, v199
	v_add_f32_e32 v36, v36, v37
	s_or_b32 s38, s29, s35
	v_add3_u32 v2, s27, v2, v3
	v_add_f32_e32 v34, v42, v34
	v_add_f32_e32 v35, v35, v36
	ds_write2st64_b32 v2, v122, v98 offset1:1
	ds_write2st64_b32 v2, v86, v78 offset0:2 offset1:3
	ds_write2st64_b32 v2, v79, v34 offset0:4 offset1:5
	ds_write2st64_b32 v2, v35, v18 offset0:6 offset1:7
	v_add_u32_e32 v6, s27, v197
	s_ashr_i32 s39, s38, 31
	s_ashr_i32 s35, s34, 31
	s_ashr_i32 s37, s36, 31
	s_lshl_b64 s[38:39], s[38:39], 18
	ds_read_b128 v[2:5], v6
	s_add_u32 s27, s58, s38
	s_addc_u32 s29, s59, s39
	s_lshl_b64 s[34:35], s[34:35], 2
	ds_read_b128 v[6:9], v6 offset:1024
	s_add_u32 s27, s27, s34
	s_addc_u32 s29, s29, s35
	s_lshl_b64 s[34:35], s[36:37], 2
	s_add_u32 s34, s27, s34
	s_waitcnt lgkmcnt(1)
	v_add_f32_e32 v2, v2, v3
	v_add_f32_e32 v3, v4, v5
	s_addc_u32 s35, s29, s35
	v_lshlrev_b32_e32 v10, 2, v196
	v_add_f32_e32 v2, v2, v3
	global_store_dword v10, v2, s[34:35]
	s_waitcnt lgkmcnt(0)
	v_add_f32_e32 v2, v6, v7
	v_add_f32_e32 v3, v8, v9
	v_add_f32_e32 v2, v2, v3
	s_andn2_b64 vcc, exec, s[6:7]
	s_mov_b64 s[6:7], -1
	global_store_dword v10, v2, s[34:35] offset:512
	s_cbranch_vccnz .LBB0_487
	v_mov_b32_e32 v2, v0
	s_andn2_b64 vcc, exec, s[14:15]
	s_cbranch_vccnz .LBB0_486
	s_barrier
	s_branch .LBB0_486

.LBB0_1780:
	v_mov_b32_e32 v209, v0
	s_lshl_b32 s47, s64, 8
	v_readfirstlane_b32 s10, v209
	s_ashr_i32 s45, s10, 6
	s_mul_i32 s11, s45, 0xb00
	s_and_b32 s45, s45, 3
	s_lshl_b32 s68, s45, 6
	s_ashr_i32 s10, s10, 8
	s_or_b32 s74, s68, s47
	s_lshl_b32 s47, s72, 2
	s_add_i32 s68, s47, s64
	s_lshl_b32 s47, s10, 2
	s_or_b32 s70, s47, s45
	s_add_i32 s11, s11, 0
	s_ashr_i32 s69, s68, 31
	s_ashr_i32 s71, s70, 31
	s_add_i32 s11, s11, 0x20000
	s_lshl_b64 s[68:69], s[68:69], 16
	s_lshl_b64 s[70:71], s[70:71], 13
	s_add_u32 s47, s41, s68
	s_addc_u32 s68, s43, s69
	s_add_u32 s78, s47, s70
	s_addc_u32 s79, s68, s71
	s_lshl_b32 s72, s72, 8
	s_lshl_b32 s10, s10, 6
	s_add_i32 s80, s10, s72
	s_ashr_i32 s81, s80, 31
	s_ashr_i32 s75, s74, 31
	s_lshl_b64 s[82:83], s[80:81], 11
	s_add_u32 s47, s54, s82
	s_addc_u32 s69, s55, s83
	s_lshl_b64 s[76:77], s[74:75], 1
	v_and_b32_e32 v204, 63, v209
	s_add_u32 s68, s47, s76
	v_bfe_u32 v190, v209, 3, 3
	v_lshlrev_b32_e32 v174, 4, v204
	s_addc_u32 s69, s69, s77
	v_lshlrev_b32_e32 v182, 11, v190
	v_mov_b32_e32 v183, v175
	v_lshl_add_u64 v[146:147], s[68:69], 0, v[182:183]
	v_and_b32_e32 v180, 0x70, v174
	v_mov_b32_e32 v181, v175
	v_lshl_add_u64 v[146:147], v[146:147], 0, v[180:181]
	v_or_b32_e32 v184, 0x4000, v182
	v_mov_b32_e32 v185, v175
	global_load_dwordx4 v[162:165], v[146:147], off nt
	v_lshl_add_u64 v[146:147], s[68:69], 0, v[184:185]
	v_lshl_add_u64 v[146:147], v[146:147], 0, v[180:181]
	global_load_dwordx4 v[186:189], v[146:147], off nt
	global_load_dwordx4 v[158:161], v174, s[78:79] nt
	s_or_b32 s47, s72, 16
	s_add_i32 s68, s10, s47
	s_ashr_i32 s69, s68, 31
	s_lshl_b64 s[68:69], s[68:69], 11
	s_add_u32 s68, s54, s68
	s_addc_u32 s69, s55, s69
	s_add_u32 s68, s68, s76
	s_addc_u32 s69, s69, s77
	v_lshl_add_u64 v[150:151], s[68:69], 0, v[182:183]
	v_lshl_add_u64 v[150:151], v[150:151], 0, v[180:181]
	v_lshl_add_u64 v[154:155], s[68:69], 0, v[184:185]
	global_load_dwordx4 v[150:153], v[150:151], off nt
	v_lshl_add_u64 v[154:155], v[154:155], 0, v[180:181]
	global_load_dwordx4 v[146:149], v174, s[78:79] offset:1024 nt
	v_mul_u32_u24_e32 v190, 0x90, v190
	global_load_dwordx4 v[154:157], v[154:155], off nt
	v_and_b32_e32 v205, 15, v209
	v_add3_u32 v207, s11, v190, v180
	v_pk_fma_f32 v[144:145], v[144:145], s[38:39], v[16:17] op_sel_hi:[1,0,1]
	v_pk_fma_f32 v[142:143], v[142:143], s[38:39], v[14:15] op_sel_hi:[1,0,1]
	v_pk_fma_f32 v[138:139], v[138:139], s[38:39], v[10:11] op_sel_hi:[1,0,1]
	v_pk_fma_f32 v[210:211], v[140:141], s[38:39], v[12:13] op_sel_hi:[1,0,1]
	v_pk_mul_f32 v[140:141], v[142:143], s[40:41] op_sel_hi:[1,0]
	v_pk_mul_f32 v[138:139], v[138:139], s[40:41] op_sel_hi:[1,0]
	v_pk_mul_f32 v[142:143], v[144:145], s[40:41] op_sel_hi:[1,0]
	v_exp_f32_e32 v138, v138
	v_exp_f32_e32 v139, v139
	v_exp_f32_e32 v142, v142
	v_exp_f32_e32 v143, v143
	v_pk_mul_f32 v[144:145], v[210:211], s[40:41] op_sel_hi:[1,0]
	s_waitcnt vmcnt(0)
	v_pk_fma_f32 v[136:137], v[136:137], s[38:39], v[8:9] op_sel_hi:[1,0,1]
	v_exp_f32_e32 v144, v144
	v_exp_f32_e32 v145, v145
	v_pk_fma_f32 v[134:135], v[134:135], s[38:39], v[6:7] op_sel_hi:[1,0,1]
	v_pk_fma_f32 v[132:133], v[132:133], s[38:39], v[4:5] op_sel_hi:[1,0,1]
	v_pk_fma_f32 v[130:131], v[130:131], s[38:39], v[2:3] op_sel_hi:[1,0,1]
	v_exp_f32_e32 v140, v140
	v_exp_f32_e32 v141, v141
	v_pk_add_f32 v[138:139], v[138:139], 1.0 op_sel_hi:[1,0]
	v_pk_add_f32 v[142:143], v[142:143], 1.0 op_sel_hi:[1,0]
	v_pk_mul_f32 v[134:135], v[134:135], s[40:41] op_sel_hi:[1,0]
	v_pk_mul_f32 v[130:131], v[130:131], s[40:41] op_sel_hi:[1,0]
	v_pk_mul_f32 v[136:137], v[136:137], s[40:41] op_sel_hi:[1,0]
	v_pk_mul_f32 v[132:133], v[132:133], s[40:41] op_sel_hi:[1,0]
	v_rcp_f32_e32 v138, v138
	v_rcp_f32_e32 v139, v139
	v_rcp_f32_e32 v142, v142
	v_rcp_f32_e32 v143, v143
	v_exp_f32_e32 v134, v134
	v_exp_f32_e32 v135, v135
	v_exp_f32_e32 v130, v130
	v_exp_f32_e32 v131, v131
	v_exp_f32_e32 v136, v136
	s_waitcnt vmcnt(0)
	ds_write_b128 v207, v[162:165]
	ds_write_b128 v207, v[186:189] offset:1152
	v_mul_u32_u24_e32 v162, 0x90, v205
	v_and_b32_e32 v163, 48, v209
	v_add3_u32 v208, s11, v162, v163
	ds_read_b128 v[194:197], v208
	ds_read_b128 v[162:165], v208 offset:64
	v_cvt_pk_f32_fp8_sdwa v[198:199], v158 src0_sel:WORD_1
	v_cvt_pk_f32_fp8_e32 v[200:201], v159
	v_exp_f32_e32 v137, v137
	s_waitcnt lgkmcnt(0)
	v_lshlrev_b32_e32 v186, 16, v196
	v_and_b32_e32 v187, 0xffff0000, v196
	v_lshlrev_b32_e32 v190, 16, v197
	v_and_b32_e32 v191, 0xffff0000, v197
	v_cvt_pk_f32_fp8_e32 v[196:197], v158
	v_exp_f32_e32 v132, v132
	v_exp_f32_e32 v133, v133
	v_pk_add_f32 v[144:145], v[144:145], 1.0 op_sel_hi:[1,0]
	v_lshlrev_b32_e32 v188, 16, v194
	v_and_b32_e32 v189, 0xffff0000, v194
	v_lshlrev_b32_e32 v194, 16, v195
	v_and_b32_e32 v195, 0xffff0000, v195
	v_cvt_pk_f32_fp8_sdwa v[158:159], v159 src0_sel:WORD_1
	v_pk_add_f32 v[140:141], v[140:141], 1.0 op_sel_hi:[1,0]
	v_rcp_f32_e32 v210, v144
	v_rcp_f32_e32 v211, v145
	v_pk_mul_f32 v[144:145], v[196:197], s[42:43] op_sel_hi:[1,0]
	v_pk_mul_f32 v[196:197], v[198:199], s[42:43] op_sel_hi:[1,0]
	v_pk_mul_f32 v[198:199], v[200:201], s[42:43] op_sel_hi:[1,0]
	v_rcp_f32_e32 v140, v140
	v_rcp_f32_e32 v141, v141
	v_pk_fma_f32 v[142:143], v[142:143], v[196:197], v[194:195]
	v_pk_fma_f32 v[186:187], v[138:139], v[198:199], v[186:187]
	v_cvt_pk_f32_fp8_e32 v[194:195], v160
	v_cvt_pk_f32_fp8_sdwa v[196:197], v160 src0_sel:WORD_1
	v_cvt_pk_f32_fp8_e32 v[198:199], v161
	v_cvt_pk_f32_fp8_sdwa v[160:161], v161 src0_sel:WORD_1
	v_pk_add_f32 v[134:135], v[134:135], 1.0 op_sel_hi:[1,0]
	v_pk_add_f32 v[130:131], v[130:131], 1.0 op_sel_hi:[1,0]
	v_pk_add_f32 v[136:137], v[136:137], 1.0 op_sel_hi:[1,0]
	v_pk_add_f32 v[132:133], v[132:133], 1.0 op_sel_hi:[1,0]
	v_rcp_f32_e32 v134, v134
	v_rcp_f32_e32 v135, v135
	v_rcp_f32_e32 v130, v130
	v_rcp_f32_e32 v131, v131
	v_rcp_f32_e32 v136, v136
	v_rcp_f32_e32 v137, v137
	v_rcp_f32_e32 v132, v132
	v_rcp_f32_e32 v133, v133
	v_pk_mul_f32 v[158:159], v[158:159], s[42:43] op_sel_hi:[1,0]
	v_pk_fma_f32 v[144:145], v[140:141], v[144:145], v[188:189]
	v_pk_fma_f32 v[158:159], v[210:211], v[158:159], v[190:191]
	v_cvt_pk_bf16_f32 v138, v144, v145
	v_cvt_pk_bf16_f32 v139, v142, v143
	v_cvt_pk_bf16_f32 v140, v186, v187
	v_lshlrev_b32_e32 v188, 16, v162
	v_cvt_pk_bf16_f32 v141, v158, v159
	v_and_b32_e32 v189, 0xffff0000, v162
	v_lshlrev_b32_e32 v162, 16, v163
	v_and_b32_e32 v163, 0xffff0000, v163
	v_lshlrev_b32_e32 v190, 16, v164
	v_and_b32_e32 v191, 0xffff0000, v164
	v_lshlrev_b32_e32 v164, 16, v165
	v_and_b32_e32 v165, 0xffff0000, v165
	v_pk_mul_f32 v[194:195], v[194:195], s[42:43] op_sel_hi:[1,0]
	v_pk_mul_f32 v[196:197], v[196:197], s[42:43] op_sel_hi:[1,0]
	v_pk_mul_f32 v[198:199], v[198:199], s[42:43] op_sel_hi:[1,0]
	v_pk_mul_f32 v[200:201], v[160:161], s[42:43] op_sel_hi:[1,0]
	s_add_u32 s68, s56, s82
	v_pk_fma_f32 v[160:161], v[136:137], v[196:197], v[162:163]
	v_pk_fma_f32 v[162:163], v[134:135], v[194:195], v[188:189]
	v_pk_fma_f32 v[164:165], v[132:133], v[200:201], v[164:165]
	v_pk_fma_f32 v[188:189], v[130:131], v[198:199], v[190:191]
	v_cvt_pk_bf16_f32 v130, v162, v163
	v_cvt_pk_bf16_f32 v131, v160, v161
	s_addc_u32 s69, s57, s83
	v_cvt_pk_bf16_f32 v132, v188, v189
	v_cvt_pk_bf16_f32 v133, v164, v165
	ds_write_b128 v208, v[138:141]
	ds_write_b128 v208, v[130:133] offset:64
	s_add_u32 s68, s68, s76
	ds_read_b128 v[130:133], v207
	ds_read_b128 v[134:137], v207 offset:1152
	s_addc_u32 s69, s69, s77
	v_lshl_add_u64 v[138:139], s[68:69], 0, v[182:183]
	v_lshl_add_u64 v[138:139], v[138:139], 0, v[180:181]
	s_waitcnt lgkmcnt(1)
	global_store_dwordx4 v[138:139], v[130:133], off
	v_bfe_u32 v206, v209, 4, 2
	v_bfe_u32 v195, v209, 2, 4
	v_lshl_add_u64 v[130:131], s[68:69], 0, v[184:185]
	v_lshl_add_u64 v[130:131], v[130:131], 0, v[180:181]
	s_waitcnt lgkmcnt(0)
	global_store_dwordx4 v[130:131], v[134:137], off
	v_mov_b32_e32 v131, v175
	v_mov_b32_e32 v130, v175
	v_mov_b32_e32 v133, v175
	v_mov_b32_e32 v132, v175
	v_cvt_pk_fp8_f32 v131, v188, v189
	v_cvt_pk_fp8_f32 v130, v162, v163
	v_cvt_pk_fp8_f32 v133, v186, v187
	v_cvt_pk_fp8_f32 v132, v144, v145
	v_cvt_pk_fp8_f32 v131, v164, v165 op_sel:[0,0,1]
	v_cvt_pk_fp8_f32 v130, v160, v161 op_sel:[0,0,1]
	v_cvt_pk_fp8_f32 v133, v158, v159 op_sel:[0,0,1]
	v_cvt_pk_fp8_f32 v132, v142, v143 op_sel:[0,0,1]
	v_mul_u32_u24_e32 v134, 0x50, v205
	v_lshlrev_b32_e32 v135, 3, v206
	v_add3_u32 v194, s11, v134, v135
	s_or_b32 s69, s72, 32
	ds_write2_b64 v194, v[132:133], v[130:131] offset1:4
	v_mul_u32_u24_e32 v130, 0x50, v195
	v_and_b32_e32 v190, 48, v174
	v_or_b32_e32 v134, s72, v195
	s_add_i32 s70, s10, s69
	v_pk_fma_f32 v[126:127], v[126:127], s[38:39], v[14:15] op_sel_hi:[1,0,1]
	v_add3_u32 v196, s11, v130, v190
	v_add_u32_e32 v134, s10, v134
	s_ashr_i32 s71, s70, 31
	v_pk_mul_f32 v[126:127], v[126:127], s[40:41] op_sel_hi:[1,0]
	ds_read_b128 v[130:133], v196
	v_ashrrev_i32_e32 v135, 31, v134
	s_lshl_b64 s[70:71], s[70:71], 11
	v_exp_f32_e32 v126, v126
	v_exp_f32_e32 v127, v127
	v_lshlrev_b64 v[134:135], 10, v[134:135]
	s_add_u32 s68, s54, s70
	v_lshl_add_u64 v[134:135], s[16:17], 0, v[134:135]
	s_addc_u32 s71, s55, s71
	v_lshl_add_u64 v[134:135], v[134:135], 0, s[74:75]
	v_mov_b32_e32 v191, v175
	s_add_u32 s70, s68, s76
	v_lshl_add_u64 v[134:135], v[134:135], 0, v[190:191]
	s_addc_u32 s71, s71, s77
	v_pk_fma_f32 v[128:129], v[128:129], s[38:39], v[16:17] op_sel_hi:[1,0,1]
	v_pk_fma_f32 v[122:123], v[122:123], s[38:39], v[10:11] op_sel_hi:[1,0,1]
	v_pk_add_f32 v[126:127], v[126:127], 1.0 op_sel_hi:[1,0]
	s_waitcnt lgkmcnt(0)
	global_store_dwordx4 v[134:135], v[130:133], off
	v_lshl_add_u64 v[134:135], s[70:71], 0, v[182:183]
	v_pk_mul_f32 v[122:123], v[122:123], s[40:41] op_sel_hi:[1,0]
	v_rcp_f32_e32 v216, v126
	v_rcp_f32_e32 v217, v127
	v_pk_mul_f32 v[126:127], v[128:129], s[40:41] op_sel_hi:[1,0]
	v_lshl_add_u64 v[134:135], v[134:135], 0, v[180:181]
	v_lshl_add_u64 v[138:139], s[70:71], 0, v[184:185]
	v_exp_f32_e32 v122, v122
	v_exp_f32_e32 v123, v123
	v_exp_f32_e32 v126, v126
	v_exp_f32_e32 v127, v127
	global_load_dwordx4 v[130:133], v174, s[78:79] offset:2048 nt
	v_lshl_add_u64 v[138:139], v[138:139], 0, v[180:181]
	global_load_dwordx4 v[134:137], v[134:135], off nt
	v_pk_fma_f32 v[124:125], v[124:125], s[38:39], v[12:13] op_sel_hi:[1,0,1]
	global_load_dwordx4 v[138:141], v[138:139], off nt
	ds_write_b128 v207, v[150:153]
	ds_write_b128 v207, v[154:157] offset:1152
	v_pk_mul_f32 v[124:125], v[124:125], s[40:41] op_sel_hi:[1,0]
	v_pk_fma_f32 v[120:121], v[120:121], s[38:39], v[8:9] op_sel_hi:[1,0,1]
	v_pk_fma_f32 v[118:119], v[118:119], s[38:39], v[6:7] op_sel_hi:[1,0,1]
	v_pk_fma_f32 v[116:117], v[116:117], s[38:39], v[4:5] op_sel_hi:[1,0,1]
	v_pk_fma_f32 v[114:115], v[114:115], s[38:39], v[2:3] op_sel_hi:[1,0,1]
	ds_read_b128 v[150:153], v208
	ds_read_b128 v[154:157], v208 offset:64
	v_cvt_pk_f32_fp8_e32 v[210:211], v146
	v_cvt_pk_f32_fp8_sdwa v[212:213], v146 src0_sel:WORD_1
	v_cvt_pk_f32_fp8_e32 v[214:215], v147
	v_pk_add_f32 v[122:123], v[122:123], 1.0 op_sel_hi:[1,0]
	v_exp_f32_e32 v124, v124
	v_exp_f32_e32 v125, v125
	v_pk_add_f32 v[126:127], v[126:127], 1.0 op_sel_hi:[1,0]
	v_pk_mul_f32 v[118:119], v[118:119], s[40:41] op_sel_hi:[1,0]
	v_pk_mul_f32 v[114:115], v[114:115], s[40:41] op_sel_hi:[1,0]
	v_pk_mul_f32 v[120:121], v[120:121], s[40:41] op_sel_hi:[1,0]
	v_pk_mul_f32 v[116:117], v[116:117], s[40:41] op_sel_hi:[1,0]
	v_rcp_f32_e32 v122, v122
	v_rcp_f32_e32 v123, v123
	v_rcp_f32_e32 v126, v126
	v_rcp_f32_e32 v127, v127
	v_exp_f32_e32 v118, v118
	v_exp_f32_e32 v119, v119
	v_exp_f32_e32 v114, v114
	v_exp_f32_e32 v115, v115
	v_exp_f32_e32 v120, v120
	v_exp_f32_e32 v121, v121
	v_exp_f32_e32 v116, v116
	v_exp_f32_e32 v117, v117
	s_waitcnt lgkmcnt(1)
	v_lshlrev_b32_e32 v198, 16, v150
	v_and_b32_e32 v199, 0xffff0000, v150
	v_lshlrev_b32_e32 v150, 16, v151
	v_and_b32_e32 v151, 0xffff0000, v151
	v_lshlrev_b32_e32 v200, 16, v152
	v_and_b32_e32 v201, 0xffff0000, v152
	v_cvt_pk_f32_fp8_sdwa v[146:147], v147 src0_sel:WORD_1
	v_pk_add_f32 v[124:125], v[124:125], 1.0 op_sel_hi:[1,0]
	v_pk_mul_f32 v[128:129], v[210:211], s[42:43] op_sel_hi:[1,0]
	v_pk_mul_f32 v[210:211], v[212:213], s[42:43] op_sel_hi:[1,0]
	v_pk_mul_f32 v[212:213], v[214:215], s[42:43] op_sel_hi:[1,0]
	v_rcp_f32_e32 v124, v124
	v_rcp_f32_e32 v125, v125
	v_pk_fma_f32 v[126:127], v[126:127], v[210:211], v[150:151]
	v_pk_fma_f32 v[150:151], v[122:123], v[212:213], v[200:201]
	v_cvt_pk_f32_fp8_e32 v[200:201], v148
	v_cvt_pk_f32_fp8_sdwa v[210:211], v148 src0_sel:WORD_1
	v_cvt_pk_f32_fp8_e32 v[212:213], v149
	v_cvt_pk_f32_fp8_sdwa v[148:149], v149 src0_sel:WORD_1
	v_pk_add_f32 v[118:119], v[118:119], 1.0 op_sel_hi:[1,0]
	v_pk_add_f32 v[114:115], v[114:115], 1.0 op_sel_hi:[1,0]
	v_pk_add_f32 v[120:121], v[120:121], 1.0 op_sel_hi:[1,0]
	v_pk_add_f32 v[116:117], v[116:117], 1.0 op_sel_hi:[1,0]
	v_rcp_f32_e32 v118, v118
	v_rcp_f32_e32 v119, v119
	v_rcp_f32_e32 v114, v114
	v_rcp_f32_e32 v115, v115
	v_rcp_f32_e32 v120, v120
	v_rcp_f32_e32 v121, v121
	v_rcp_f32_e32 v116, v116
	v_rcp_f32_e32 v117, v117
	s_or_b32 s70, s80, 16
	s_ashr_i32 s71, s70, 31
	v_lshlrev_b32_e32 v152, 16, v153
	v_and_b32_e32 v153, 0xffff0000, v153
	v_pk_mul_f32 v[146:147], v[146:147], s[42:43] op_sel_hi:[1,0]
	s_lshl_b64 s[70:71], s[70:71], 11
	v_pk_fma_f32 v[128:129], v[216:217], v[128:129], v[198:199]
	v_pk_fma_f32 v[146:147], v[124:125], v[146:147], v[152:153]
	v_cvt_pk_bf16_f32 v122, v128, v129
	v_cvt_pk_bf16_f32 v123, v126, v127
	v_cvt_pk_bf16_f32 v124, v150, v151
	s_waitcnt lgkmcnt(0)
	v_lshlrev_b32_e32 v152, 16, v154
	v_cvt_pk_bf16_f32 v125, v146, v147
	v_and_b32_e32 v153, 0xffff0000, v154
	v_lshlrev_b32_e32 v154, 16, v155
	v_and_b32_e32 v155, 0xffff0000, v155
	v_lshlrev_b32_e32 v198, 16, v156
	v_and_b32_e32 v199, 0xffff0000, v156
	v_lshlrev_b32_e32 v156, 16, v157
	v_and_b32_e32 v157, 0xffff0000, v157
	v_pk_mul_f32 v[200:201], v[200:201], s[42:43] op_sel_hi:[1,0]
	v_pk_mul_f32 v[210:211], v[210:211], s[42:43] op_sel_hi:[1,0]
	v_pk_mul_f32 v[212:213], v[212:213], s[42:43] op_sel_hi:[1,0]
	v_pk_mul_f32 v[214:215], v[148:149], s[42:43] op_sel_hi:[1,0]
	s_add_u32 s68, s56, s70
	v_pk_fma_f32 v[148:149], v[120:121], v[210:211], v[154:155]
	v_pk_fma_f32 v[152:153], v[118:119], v[200:201], v[152:153]
	v_pk_fma_f32 v[154:155], v[116:117], v[214:215], v[156:157]
	v_pk_fma_f32 v[156:157], v[114:115], v[212:213], v[198:199]
	v_cvt_pk_bf16_f32 v114, v152, v153
	v_cvt_pk_bf16_f32 v115, v148, v149
	s_addc_u32 s71, s57, s71
	v_cvt_pk_bf16_f32 v116, v156, v157
	v_cvt_pk_bf16_f32 v117, v154, v155
	ds_write_b128 v208, v[122:125]
	ds_write_b128 v208, v[114:117] offset:64
	s_add_u32 s70, s68, s76
	ds_read_b128 v[114:117], v207
	ds_read_b128 v[118:121], v207 offset:1152
	s_addc_u32 s71, s71, s77
	v_lshl_add_u64 v[122:123], s[70:71], 0, v[182:183]
	v_lshl_add_u64 v[122:123], v[122:123], 0, v[180:181]
	s_waitcnt lgkmcnt(1)
	global_store_dwordx4 v[122:123], v[114:117], off
	s_or_b32 s68, s72, 48
	v_pk_fma_f32 v[110:111], v[110:111], s[38:39], v[14:15] op_sel_hi:[1,0,1]
	v_lshl_add_u64 v[114:115], s[70:71], 0, v[184:185]
	v_lshl_add_u64 v[114:115], v[114:115], 0, v[180:181]
	s_waitcnt lgkmcnt(0)
	global_store_dwordx4 v[114:115], v[118:121], off
	v_mov_b32_e32 v115, v175
	v_mov_b32_e32 v114, v175
	v_mov_b32_e32 v117, v175
	v_mov_b32_e32 v116, v175
	v_cvt_pk_fp8_f32 v115, v156, v157
	v_cvt_pk_fp8_f32 v114, v152, v153
	v_cvt_pk_fp8_f32 v117, v150, v151
	v_cvt_pk_fp8_f32 v116, v128, v129
	v_cvt_pk_fp8_f32 v115, v154, v155 op_sel:[0,0,1]
	v_cvt_pk_fp8_f32 v114, v148, v149 op_sel:[0,0,1]
	v_cvt_pk_fp8_f32 v117, v146, v147 op_sel:[0,0,1]
	v_cvt_pk_fp8_f32 v116, v126, v127 op_sel:[0,0,1]
	v_or_b32_e32 v118, s47, v195
	s_add_i32 s70, s10, s68
	v_add_u32_e32 v118, s10, v118
	ds_write2_b64 v194, v[116:117], v[114:115] offset1:4
	s_ashr_i32 s71, s70, 31
	ds_read_b128 v[114:117], v196
	v_ashrrev_i32_e32 v119, 31, v118
	s_lshl_b64 s[70:71], s[70:71], 11
	v_lshlrev_b64 v[118:119], 10, v[118:119]
	s_add_u32 s47, s54, s70
	v_lshl_add_u64 v[118:119], s[16:17], 0, v[118:119]
	s_addc_u32 s71, s55, s71
	v_lshl_add_u64 v[118:119], v[118:119], 0, s[74:75]
	s_add_u32 s70, s47, s76
	v_lshl_add_u64 v[118:119], v[118:119], 0, v[190:191]
	s_addc_u32 s71, s71, s77
	s_waitcnt lgkmcnt(0)
	global_store_dwordx4 v[118:119], v[114:117], off
	v_lshl_add_u64 v[118:119], s[70:71], 0, v[182:183]
	v_lshl_add_u64 v[118:119], v[118:119], 0, v[180:181]
	v_lshl_add_u64 v[122:123], s[70:71], 0, v[184:185]
	global_load_dwordx4 v[114:117], v174, s[78:79] offset:3072 nt
	v_lshl_add_u64 v[122:123], v[122:123], 0, v[180:181]
	global_load_dwordx4 v[118:121], v[118:119], off nt
	v_pk_mul_f32 v[110:111], v[110:111], s[40:41] op_sel_hi:[1,0]
	global_load_dwordx4 v[122:125], v[122:123], off nt
	v_exp_f32_e32 v110, v110
	v_exp_f32_e32 v111, v111
	v_pk_fma_f32 v[112:113], v[112:113], s[38:39], v[16:17] op_sel_hi:[1,0,1]
	v_pk_fma_f32 v[106:107], v[106:107], s[38:39], v[10:11] op_sel_hi:[1,0,1]
	v_pk_fma_f32 v[108:109], v[108:109], s[38:39], v[12:13] op_sel_hi:[1,0,1]
	v_pk_add_f32 v[110:111], v[110:111], 1.0 op_sel_hi:[1,0]
	v_pk_mul_f32 v[106:107], v[106:107], s[40:41] op_sel_hi:[1,0]
	v_rcp_f32_e32 v216, v110
	v_rcp_f32_e32 v217, v111
	v_pk_mul_f32 v[110:111], v[112:113], s[40:41] op_sel_hi:[1,0]
	v_exp_f32_e32 v106, v106
	v_exp_f32_e32 v107, v107
	v_exp_f32_e32 v110, v110
	v_exp_f32_e32 v111, v111
	s_waitcnt vmcnt(7)
	ds_write_b128 v207, v[134:137]
	s_waitcnt vmcnt(6)
	ds_write_b128 v207, v[138:141] offset:1152
	v_pk_mul_f32 v[108:109], v[108:109], s[40:41] op_sel_hi:[1,0]
	v_pk_fma_f32 v[104:105], v[104:105], s[38:39], v[8:9] op_sel_hi:[1,0,1]
	v_pk_fma_f32 v[102:103], v[102:103], s[38:39], v[6:7] op_sel_hi:[1,0,1]
	v_pk_fma_f32 v[100:101], v[100:101], s[38:39], v[4:5] op_sel_hi:[1,0,1]
	v_pk_fma_f32 v[98:99], v[98:99], s[38:39], v[2:3] op_sel_hi:[1,0,1]
	ds_read_b128 v[134:137], v208
	ds_read_b128 v[138:141], v208 offset:64
	v_cvt_pk_f32_fp8_e32 v[210:211], v130
	v_cvt_pk_f32_fp8_sdwa v[212:213], v130 src0_sel:WORD_1
	v_cvt_pk_f32_fp8_e32 v[214:215], v131
	v_pk_add_f32 v[106:107], v[106:107], 1.0 op_sel_hi:[1,0]
	v_exp_f32_e32 v108, v108
	v_exp_f32_e32 v109, v109
	v_pk_add_f32 v[110:111], v[110:111], 1.0 op_sel_hi:[1,0]
	v_pk_mul_f32 v[102:103], v[102:103], s[40:41] op_sel_hi:[1,0]
	v_pk_mul_f32 v[98:99], v[98:99], s[40:41] op_sel_hi:[1,0]
	v_pk_mul_f32 v[104:105], v[104:105], s[40:41] op_sel_hi:[1,0]
	v_pk_mul_f32 v[100:101], v[100:101], s[40:41] op_sel_hi:[1,0]
	v_rcp_f32_e32 v106, v106
	v_rcp_f32_e32 v107, v107
	v_rcp_f32_e32 v110, v110
	v_rcp_f32_e32 v111, v111
	v_exp_f32_e32 v102, v102
	v_exp_f32_e32 v103, v103
	v_exp_f32_e32 v98, v98
	v_exp_f32_e32 v99, v99
	v_exp_f32_e32 v104, v104
	v_exp_f32_e32 v105, v105
	v_exp_f32_e32 v100, v100
	v_exp_f32_e32 v101, v101
	s_waitcnt lgkmcnt(1)
	v_lshlrev_b32_e32 v198, 16, v134
	v_and_b32_e32 v199, 0xffff0000, v134
	v_lshlrev_b32_e32 v134, 16, v135
	v_and_b32_e32 v135, 0xffff0000, v135
	v_lshlrev_b32_e32 v200, 16, v136
	v_and_b32_e32 v201, 0xffff0000, v136
	v_cvt_pk_f32_fp8_sdwa v[130:131], v131 src0_sel:WORD_1
	v_pk_add_f32 v[108:109], v[108:109], 1.0 op_sel_hi:[1,0]
	v_pk_mul_f32 v[112:113], v[210:211], s[42:43] op_sel_hi:[1,0]
	v_pk_mul_f32 v[210:211], v[212:213], s[42:43] op_sel_hi:[1,0]
	v_pk_mul_f32 v[212:213], v[214:215], s[42:43] op_sel_hi:[1,0]
	v_rcp_f32_e32 v108, v108
	v_rcp_f32_e32 v109, v109
	v_pk_fma_f32 v[110:111], v[110:111], v[210:211], v[134:135]
	v_pk_fma_f32 v[134:135], v[106:107], v[212:213], v[200:201]
	v_cvt_pk_f32_fp8_e32 v[200:201], v132
	v_cvt_pk_f32_fp8_sdwa v[210:211], v132 src0_sel:WORD_1
	v_cvt_pk_f32_fp8_e32 v[212:213], v133
	v_cvt_pk_f32_fp8_sdwa v[132:133], v133 src0_sel:WORD_1
	v_pk_add_f32 v[102:103], v[102:103], 1.0 op_sel_hi:[1,0]
	v_pk_add_f32 v[98:99], v[98:99], 1.0 op_sel_hi:[1,0]
	v_pk_add_f32 v[104:105], v[104:105], 1.0 op_sel_hi:[1,0]
	v_pk_add_f32 v[100:101], v[100:101], 1.0 op_sel_hi:[1,0]
	v_rcp_f32_e32 v102, v102
	v_rcp_f32_e32 v103, v103
	v_rcp_f32_e32 v98, v98
	v_rcp_f32_e32 v99, v99
	v_rcp_f32_e32 v104, v104
	v_rcp_f32_e32 v105, v105
	v_rcp_f32_e32 v100, v100
	v_rcp_f32_e32 v101, v101
	s_or_b32 s70, s80, 32
	s_ashr_i32 s71, s70, 31
	v_lshlrev_b32_e32 v136, 16, v137
	v_and_b32_e32 v137, 0xffff0000, v137
	v_pk_mul_f32 v[130:131], v[130:131], s[42:43] op_sel_hi:[1,0]
	s_lshl_b64 s[70:71], s[70:71], 11
	v_pk_fma_f32 v[112:113], v[216:217], v[112:113], v[198:199]
	v_pk_fma_f32 v[130:131], v[108:109], v[130:131], v[136:137]
	v_cvt_pk_bf16_f32 v106, v112, v113
	v_cvt_pk_bf16_f32 v107, v110, v111
	v_cvt_pk_bf16_f32 v108, v134, v135
	s_waitcnt lgkmcnt(0)
	v_lshlrev_b32_e32 v136, 16, v138
	v_cvt_pk_bf16_f32 v109, v130, v131
	v_and_b32_e32 v137, 0xffff0000, v138
	v_lshlrev_b32_e32 v138, 16, v139
	v_and_b32_e32 v139, 0xffff0000, v139
	v_lshlrev_b32_e32 v198, 16, v140
	v_and_b32_e32 v199, 0xffff0000, v140
	v_lshlrev_b32_e32 v140, 16, v141
	v_and_b32_e32 v141, 0xffff0000, v141
	v_pk_mul_f32 v[200:201], v[200:201], s[42:43] op_sel_hi:[1,0]
	v_pk_mul_f32 v[210:211], v[210:211], s[42:43] op_sel_hi:[1,0]
	v_pk_mul_f32 v[212:213], v[212:213], s[42:43] op_sel_hi:[1,0]
	v_pk_mul_f32 v[214:215], v[132:133], s[42:43] op_sel_hi:[1,0]
	s_add_u32 s47, s56, s70
	v_pk_fma_f32 v[132:133], v[104:105], v[210:211], v[138:139]
	v_pk_fma_f32 v[136:137], v[102:103], v[200:201], v[136:137]
	v_pk_fma_f32 v[138:139], v[100:101], v[214:215], v[140:141]
	v_pk_fma_f32 v[140:141], v[98:99], v[212:213], v[198:199]
	v_cvt_pk_bf16_f32 v98, v136, v137
	v_cvt_pk_bf16_f32 v99, v132, v133
	s_addc_u32 s71, s57, s71
	v_cvt_pk_bf16_f32 v100, v140, v141
	v_cvt_pk_bf16_f32 v101, v138, v139
	ds_write_b128 v208, v[106:109]
	ds_write_b128 v208, v[98:101] offset:64
	s_add_u32 s70, s47, s76
	ds_read_b128 v[98:101], v207
	ds_read_b128 v[102:105], v207 offset:1152
	s_addc_u32 s71, s71, s77
	v_lshl_add_u64 v[106:107], s[70:71], 0, v[182:183]
	v_lshl_add_u64 v[106:107], v[106:107], 0, v[180:181]
	s_waitcnt lgkmcnt(1)
	global_store_dwordx4 v[106:107], v[98:101], off
	s_or_b32 s47, s72, 0x80
	v_lshl_add_u64 v[192:193], s[78:79], 0, v[174:175]
	v_lshl_add_u64 v[98:99], s[70:71], 0, v[184:185]
	v_lshl_add_u64 v[98:99], v[98:99], 0, v[180:181]
	s_waitcnt lgkmcnt(0)
	global_store_dwordx4 v[98:99], v[102:105], off
	v_mov_b32_e32 v99, v175
	v_mov_b32_e32 v98, v175
	v_mov_b32_e32 v101, v175
	v_mov_b32_e32 v100, v175
	v_cvt_pk_fp8_f32 v99, v140, v141
	v_cvt_pk_fp8_f32 v98, v136, v137
	v_cvt_pk_fp8_f32 v101, v134, v135
	v_cvt_pk_fp8_f32 v100, v112, v113
	v_cvt_pk_fp8_f32 v99, v138, v139 op_sel:[0,0,1]
	v_cvt_pk_fp8_f32 v98, v132, v133 op_sel:[0,0,1]
	v_cvt_pk_fp8_f32 v101, v130, v131 op_sel:[0,0,1]
	v_cvt_pk_fp8_f32 v100, v110, v111 op_sel:[0,0,1]
	v_or_b32_e32 v102, s69, v195
	s_add_i32 s78, s10, s47
	v_pk_fma_f32 v[94:95], v[94:95], s[38:39], v[14:15] op_sel_hi:[1,0,1]
	ds_write2_b64 v194, v[100:101], v[98:99] offset1:4
	v_add_u32_e32 v102, s10, v102
	s_ashr_i32 s79, s78, 31
	v_pk_mul_f32 v[94:95], v[94:95], s[40:41] op_sel_hi:[1,0]
	ds_read_b128 v[98:101], v196
	v_ashrrev_i32_e32 v103, 31, v102
	s_movk_i32 s69, 0x1000
	s_lshl_b64 s[82:83], s[78:79], 11
	v_exp_f32_e32 v94, v94
	v_exp_f32_e32 v95, v95
	v_lshlrev_b64 v[102:103], 10, v[102:103]
	v_add_co_u32_e32 v192, vcc, s69, v192
	s_add_u32 s69, s54, s82
	v_lshl_add_u64 v[102:103], s[16:17], 0, v[102:103]
	s_addc_u32 s71, s55, s83
	v_lshl_add_u64 v[102:103], v[102:103], 0, s[74:75]
	s_add_u32 s70, s69, s76
	v_lshl_add_u64 v[102:103], v[102:103], 0, v[190:191]
	s_addc_u32 s71, s71, s77
	v_pk_fma_f32 v[96:97], v[96:97], s[38:39], v[16:17] op_sel_hi:[1,0,1]
	v_pk_fma_f32 v[90:91], v[90:91], s[38:39], v[10:11] op_sel_hi:[1,0,1]
	v_pk_add_f32 v[94:95], v[94:95], 1.0 op_sel_hi:[1,0]
	s_waitcnt lgkmcnt(0)
	global_store_dwordx4 v[102:103], v[98:101], off
	v_lshl_add_u64 v[102:103], s[70:71], 0, v[182:183]
	v_pk_mul_f32 v[90:91], v[90:91], s[40:41] op_sel_hi:[1,0]
	v_rcp_f32_e32 v216, v94
	v_rcp_f32_e32 v217, v95
	v_pk_mul_f32 v[94:95], v[96:97], s[40:41] op_sel_hi:[1,0]
	v_lshl_add_u64 v[102:103], v[102:103], 0, v[180:181]
	v_lshl_add_u64 v[106:107], s[70:71], 0, v[184:185]
	v_exp_f32_e32 v90, v90
	v_exp_f32_e32 v91, v91
	v_exp_f32_e32 v94, v94
	v_exp_f32_e32 v95, v95
	v_addc_co_u32_e32 v193, vcc, 0, v193, vcc
	global_load_dwordx4 v[102:105], v[102:103], off nt
	v_lshl_add_u64 v[106:107], v[106:107], 0, v[180:181]
	global_load_dwordx4 v[98:101], v[192:193], off nt
	v_pk_fma_f32 v[92:93], v[92:93], s[38:39], v[12:13] op_sel_hi:[1,0,1]
	global_load_dwordx4 v[106:109], v[106:107], off nt
	s_waitcnt vmcnt(7)
	ds_write_b128 v207, v[118:121]
	s_waitcnt vmcnt(6)
	ds_write_b128 v207, v[122:125] offset:1152
	v_pk_mul_f32 v[92:93], v[92:93], s[40:41] op_sel_hi:[1,0]
	v_pk_fma_f32 v[88:89], v[88:89], s[38:39], v[8:9] op_sel_hi:[1,0,1]
	v_pk_fma_f32 v[86:87], v[86:87], s[38:39], v[6:7] op_sel_hi:[1,0,1]
	v_pk_fma_f32 v[84:85], v[84:85], s[38:39], v[4:5] op_sel_hi:[1,0,1]
	v_pk_fma_f32 v[82:83], v[82:83], s[38:39], v[2:3] op_sel_hi:[1,0,1]
	ds_read_b128 v[118:121], v208
	ds_read_b128 v[122:125], v208 offset:64
	v_cvt_pk_f32_fp8_e32 v[210:211], v114
	v_cvt_pk_f32_fp8_sdwa v[212:213], v114 src0_sel:WORD_1
	v_cvt_pk_f32_fp8_e32 v[214:215], v115
	v_pk_add_f32 v[90:91], v[90:91], 1.0 op_sel_hi:[1,0]
	v_exp_f32_e32 v92, v92
	v_exp_f32_e32 v93, v93
	v_pk_add_f32 v[94:95], v[94:95], 1.0 op_sel_hi:[1,0]
	v_pk_mul_f32 v[86:87], v[86:87], s[40:41] op_sel_hi:[1,0]
	v_pk_mul_f32 v[82:83], v[82:83], s[40:41] op_sel_hi:[1,0]
	v_pk_mul_f32 v[88:89], v[88:89], s[40:41] op_sel_hi:[1,0]
	v_pk_mul_f32 v[84:85], v[84:85], s[40:41] op_sel_hi:[1,0]
	v_rcp_f32_e32 v90, v90
	v_rcp_f32_e32 v91, v91
	v_rcp_f32_e32 v94, v94
	v_rcp_f32_e32 v95, v95
	v_exp_f32_e32 v86, v86
	v_exp_f32_e32 v87, v87
	v_exp_f32_e32 v82, v82
	v_exp_f32_e32 v83, v83
	v_exp_f32_e32 v88, v88
	v_exp_f32_e32 v89, v89
	v_exp_f32_e32 v84, v84
	v_exp_f32_e32 v85, v85
	s_waitcnt lgkmcnt(1)
	v_lshlrev_b32_e32 v198, 16, v118
	v_and_b32_e32 v199, 0xffff0000, v118
	v_lshlrev_b32_e32 v118, 16, v119
	v_and_b32_e32 v119, 0xffff0000, v119
	v_lshlrev_b32_e32 v200, 16, v120
	v_and_b32_e32 v201, 0xffff0000, v120
	v_cvt_pk_f32_fp8_sdwa v[114:115], v115 src0_sel:WORD_1
	v_pk_add_f32 v[92:93], v[92:93], 1.0 op_sel_hi:[1,0]
	v_pk_mul_f32 v[96:97], v[210:211], s[42:43] op_sel_hi:[1,0]
	v_pk_mul_f32 v[210:211], v[212:213], s[42:43] op_sel_hi:[1,0]
	v_pk_mul_f32 v[212:213], v[214:215], s[42:43] op_sel_hi:[1,0]
	v_rcp_f32_e32 v92, v92
	v_rcp_f32_e32 v93, v93
	v_pk_fma_f32 v[94:95], v[94:95], v[210:211], v[118:119]
	v_pk_fma_f32 v[118:119], v[90:91], v[212:213], v[200:201]
	v_cvt_pk_f32_fp8_e32 v[200:201], v116
	v_cvt_pk_f32_fp8_sdwa v[210:211], v116 src0_sel:WORD_1
	v_cvt_pk_f32_fp8_e32 v[212:213], v117
	v_cvt_pk_f32_fp8_sdwa v[116:117], v117 src0_sel:WORD_1
	v_pk_add_f32 v[86:87], v[86:87], 1.0 op_sel_hi:[1,0]
	v_pk_add_f32 v[82:83], v[82:83], 1.0 op_sel_hi:[1,0]
	v_pk_add_f32 v[88:89], v[88:89], 1.0 op_sel_hi:[1,0]
	v_pk_add_f32 v[84:85], v[84:85], 1.0 op_sel_hi:[1,0]
	v_rcp_f32_e32 v86, v86
	v_rcp_f32_e32 v87, v87
	v_rcp_f32_e32 v82, v82
	v_rcp_f32_e32 v83, v83
	v_rcp_f32_e32 v88, v88
	v_rcp_f32_e32 v89, v89
	v_rcp_f32_e32 v84, v84
	v_rcp_f32_e32 v85, v85
	s_or_b32 s70, s80, 48
	s_ashr_i32 s71, s70, 31
	v_lshlrev_b32_e32 v120, 16, v121
	v_and_b32_e32 v121, 0xffff0000, v121
	v_pk_mul_f32 v[114:115], v[114:115], s[42:43] op_sel_hi:[1,0]
	s_lshl_b64 s[70:71], s[70:71], 11
	v_pk_fma_f32 v[96:97], v[216:217], v[96:97], v[198:199]
	v_pk_fma_f32 v[114:115], v[92:93], v[114:115], v[120:121]
	v_cvt_pk_bf16_f32 v90, v96, v97
	v_cvt_pk_bf16_f32 v91, v94, v95
	v_cvt_pk_bf16_f32 v92, v118, v119
	s_waitcnt lgkmcnt(0)
	v_lshlrev_b32_e32 v120, 16, v122
	v_cvt_pk_bf16_f32 v93, v114, v115
	v_and_b32_e32 v121, 0xffff0000, v122
	v_lshlrev_b32_e32 v122, 16, v123
	v_and_b32_e32 v123, 0xffff0000, v123
	v_lshlrev_b32_e32 v198, 16, v124
	v_and_b32_e32 v199, 0xffff0000, v124
	v_lshlrev_b32_e32 v124, 16, v125
	v_and_b32_e32 v125, 0xffff0000, v125
	v_pk_mul_f32 v[200:201], v[200:201], s[42:43] op_sel_hi:[1,0]
	v_pk_mul_f32 v[210:211], v[210:211], s[42:43] op_sel_hi:[1,0]
	v_pk_mul_f32 v[212:213], v[212:213], s[42:43] op_sel_hi:[1,0]
	v_pk_mul_f32 v[214:215], v[116:117], s[42:43] op_sel_hi:[1,0]
	s_add_u32 s69, s56, s70
	v_pk_fma_f32 v[116:117], v[88:89], v[210:211], v[122:123]
	v_pk_fma_f32 v[120:121], v[86:87], v[200:201], v[120:121]
	v_pk_fma_f32 v[122:123], v[84:85], v[214:215], v[124:125]
	v_pk_fma_f32 v[124:125], v[82:83], v[212:213], v[198:199]
	v_cvt_pk_bf16_f32 v82, v120, v121
	v_cvt_pk_bf16_f32 v83, v116, v117
	s_addc_u32 s71, s57, s71
	v_cvt_pk_bf16_f32 v84, v124, v125
	v_cvt_pk_bf16_f32 v85, v122, v123
	ds_write_b128 v208, v[90:93]
	ds_write_b128 v208, v[82:85] offset:64
	s_add_u32 s70, s69, s76
	ds_read_b128 v[82:85], v207
	ds_read_b128 v[86:89], v207 offset:1152
	s_addc_u32 s71, s71, s77
	v_lshl_add_u64 v[90:91], s[70:71], 0, v[182:183]
	v_lshl_add_u64 v[90:91], v[90:91], 0, v[180:181]
	s_waitcnt lgkmcnt(1)
	global_store_dwordx4 v[90:91], v[82:85], off
	v_pk_fma_f32 v[80:81], v[80:81], s[38:39], v[16:17] op_sel_hi:[1,0,1]
	v_pk_fma_f32 v[78:79], v[78:79], s[38:39], v[14:15] op_sel_hi:[1,0,1]
	v_lshl_add_u64 v[82:83], s[70:71], 0, v[184:185]
	v_lshl_add_u64 v[82:83], v[82:83], 0, v[180:181]
	s_waitcnt lgkmcnt(0)
	global_store_dwordx4 v[82:83], v[86:89], off
	v_mov_b32_e32 v83, v175
	v_mov_b32_e32 v82, v175
	v_mov_b32_e32 v85, v175
	v_mov_b32_e32 v84, v175
	v_cvt_pk_fp8_f32 v83, v124, v125
	v_cvt_pk_fp8_f32 v82, v120, v121
	v_cvt_pk_fp8_f32 v85, v118, v119
	v_cvt_pk_fp8_f32 v84, v96, v97
	v_cvt_pk_fp8_f32 v83, v122, v123 op_sel:[0,0,1]
	v_cvt_pk_fp8_f32 v82, v116, v117 op_sel:[0,0,1]
	v_cvt_pk_fp8_f32 v85, v114, v115 op_sel:[0,0,1]
	v_cvt_pk_fp8_f32 v84, v94, v95 op_sel:[0,0,1]
	v_or_b32_e32 v86, s68, v195
	s_or_b32 s68, s72, 0x90
	s_add_i32 s70, s10, s68
	ds_write2_b64 v194, v[84:85], v[82:83] offset1:4
	v_add_u32_e32 v86, s10, v86
	s_ashr_i32 s71, s70, 31
	ds_read_b128 v[82:85], v196
	v_ashrrev_i32_e32 v87, 31, v86
	s_lshl_b64 s[70:71], s[70:71], 11
	v_lshlrev_b64 v[86:87], 10, v[86:87]
	s_add_u32 s69, s54, s70
	v_lshl_add_u64 v[86:87], s[16:17], 0, v[86:87]
	s_addc_u32 s71, s55, s71
	v_lshl_add_u64 v[86:87], v[86:87], 0, s[74:75]
	s_add_u32 s70, s69, s76
	v_lshl_add_u64 v[86:87], v[86:87], 0, v[190:191]
	s_addc_u32 s71, s71, s77
	s_waitcnt lgkmcnt(0)
	global_store_dwordx4 v[86:87], v[82:85], off
	v_lshl_add_u64 v[86:87], s[70:71], 0, v[182:183]
	v_lshl_add_u64 v[86:87], v[86:87], 0, v[180:181]
	v_lshl_add_u64 v[90:91], s[70:71], 0, v[184:185]
	global_load_dwordx4 v[86:89], v[86:87], off nt
	v_lshl_add_u64 v[90:91], v[90:91], 0, v[180:181]
	global_load_dwordx4 v[82:85], v[192:193], off offset:1024 nt
	v_pk_fma_f32 v[74:75], v[74:75], s[38:39], v[10:11] op_sel_hi:[1,0,1]
	global_load_dwordx4 v[90:93], v[90:91], off nt
	v_pk_mul_f32 v[78:79], v[78:79], s[40:41] op_sel_hi:[1,0]
	v_pk_mul_f32 v[74:75], v[74:75], s[40:41] op_sel_hi:[1,0]
	v_pk_mul_f32 v[80:81], v[80:81], s[40:41] op_sel_hi:[1,0]
	v_exp_f32_e32 v78, v78
	v_exp_f32_e32 v79, v79
	v_exp_f32_e32 v74, v74
	v_exp_f32_e32 v75, v75
	v_exp_f32_e32 v80, v80
	v_exp_f32_e32 v81, v81
	v_pk_fma_f32 v[76:77], v[76:77], s[38:39], v[12:13] op_sel_hi:[1,0,1]
	s_waitcnt vmcnt(8)
	ds_write_b128 v207, v[102:105]
	s_waitcnt vmcnt(6)
	ds_write_b128 v207, v[106:109] offset:1152
	v_pk_mul_f32 v[76:77], v[76:77], s[40:41] op_sel_hi:[1,0]
	v_pk_fma_f32 v[72:73], v[72:73], s[38:39], v[8:9] op_sel_hi:[1,0,1]
	v_pk_fma_f32 v[70:71], v[70:71], s[38:39], v[6:7] op_sel_hi:[1,0,1]
	v_pk_fma_f32 v[68:69], v[68:69], s[38:39], v[4:5] op_sel_hi:[1,0,1]
	v_pk_fma_f32 v[66:67], v[66:67], s[38:39], v[2:3] op_sel_hi:[1,0,1]
	ds_read_b128 v[102:105], v208
	ds_read_b128 v[106:109], v208 offset:64
	v_cvt_pk_f32_fp8_e32 v[210:211], v98
	v_cvt_pk_f32_fp8_sdwa v[212:213], v98 src0_sel:WORD_1
	v_cvt_pk_f32_fp8_e32 v[214:215], v99
	v_cvt_pk_f32_fp8_sdwa v[98:99], v99 src0_sel:WORD_1
	v_pk_add_f32 v[78:79], v[78:79], 1.0 op_sel_hi:[1,0]
	v_pk_add_f32 v[74:75], v[74:75], 1.0 op_sel_hi:[1,0]
	v_exp_f32_e32 v76, v76
	v_exp_f32_e32 v77, v77
	v_pk_add_f32 v[80:81], v[80:81], 1.0 op_sel_hi:[1,0]
	v_pk_mul_f32 v[70:71], v[70:71], s[40:41] op_sel_hi:[1,0]
	v_pk_mul_f32 v[66:67], v[66:67], s[40:41] op_sel_hi:[1,0]
	v_pk_mul_f32 v[72:73], v[72:73], s[40:41] op_sel_hi:[1,0]
	v_pk_mul_f32 v[68:69], v[68:69], s[40:41] op_sel_hi:[1,0]
	v_rcp_f32_e32 v78, v78
	v_rcp_f32_e32 v79, v79
	v_rcp_f32_e32 v74, v74
	v_rcp_f32_e32 v75, v75
	v_rcp_f32_e32 v80, v80
	v_rcp_f32_e32 v81, v81
	v_exp_f32_e32 v70, v70
	v_exp_f32_e32 v71, v71
	v_exp_f32_e32 v66, v66
	v_exp_f32_e32 v67, v67
	v_exp_f32_e32 v72, v72
	v_exp_f32_e32 v73, v73
	v_exp_f32_e32 v68, v68
	v_exp_f32_e32 v69, v69
	s_waitcnt lgkmcnt(1)
	v_lshlrev_b32_e32 v198, 16, v102
	v_and_b32_e32 v199, 0xffff0000, v102
	v_lshlrev_b32_e32 v102, 16, v103
	v_and_b32_e32 v103, 0xffff0000, v103
	v_lshlrev_b32_e32 v200, 16, v104
	v_and_b32_e32 v201, 0xffff0000, v104
	v_pk_add_f32 v[76:77], v[76:77], 1.0 op_sel_hi:[1,0]
	v_pk_mul_f32 v[212:213], v[212:213], s[42:43] op_sel_hi:[1,0]
	v_pk_mul_f32 v[210:211], v[210:211], s[42:43] op_sel_hi:[1,0]
	v_pk_mul_f32 v[216:217], v[98:99], s[42:43] op_sel_hi:[1,0]
	v_pk_mul_f32 v[98:99], v[214:215], s[42:43] op_sel_hi:[1,0]
	v_rcp_f32_e32 v76, v76
	v_rcp_f32_e32 v77, v77
	v_pk_fma_f32 v[78:79], v[78:79], v[210:211], v[198:199]
	v_pk_fma_f32 v[80:81], v[80:81], v[212:213], v[102:103]
	v_pk_fma_f32 v[98:99], v[74:75], v[98:99], v[200:201]
	v_cvt_pk_f32_fp8_e32 v[200:201], v100
	v_cvt_pk_f32_fp8_sdwa v[210:211], v100 src0_sel:WORD_1
	v_cvt_pk_f32_fp8_e32 v[212:213], v101
	v_cvt_pk_f32_fp8_sdwa v[100:101], v101 src0_sel:WORD_1
	v_pk_add_f32 v[70:71], v[70:71], 1.0 op_sel_hi:[1,0]
	v_pk_add_f32 v[66:67], v[66:67], 1.0 op_sel_hi:[1,0]
	v_pk_add_f32 v[72:73], v[72:73], 1.0 op_sel_hi:[1,0]
	v_pk_add_f32 v[68:69], v[68:69], 1.0 op_sel_hi:[1,0]
	v_rcp_f32_e32 v70, v70
	v_rcp_f32_e32 v71, v71
	v_rcp_f32_e32 v66, v66
	v_rcp_f32_e32 v67, v67
	v_rcp_f32_e32 v72, v72
	v_rcp_f32_e32 v73, v73
	v_rcp_f32_e32 v68, v68
	v_rcp_f32_e32 v69, v69
	v_lshlrev_b32_e32 v104, 16, v105
	v_and_b32_e32 v105, 0xffff0000, v105
	v_pk_fma_f32 v[102:103], v[76:77], v[216:217], v[104:105]
	v_cvt_pk_bf16_f32 v74, v78, v79
	v_cvt_pk_bf16_f32 v75, v80, v81
	v_cvt_pk_bf16_f32 v76, v98, v99
	s_waitcnt lgkmcnt(0)
	v_lshlrev_b32_e32 v104, 16, v106
	v_cvt_pk_bf16_f32 v77, v102, v103
	v_and_b32_e32 v105, 0xffff0000, v106
	v_lshlrev_b32_e32 v106, 16, v107
	v_and_b32_e32 v107, 0xffff0000, v107
	v_lshlrev_b32_e32 v198, 16, v108
	v_and_b32_e32 v199, 0xffff0000, v108
	v_lshlrev_b32_e32 v108, 16, v109
	v_and_b32_e32 v109, 0xffff0000, v109
	v_pk_mul_f32 v[210:211], v[210:211], s[42:43] op_sel_hi:[1,0]
	v_pk_mul_f32 v[200:201], v[200:201], s[42:43] op_sel_hi:[1,0]
	v_pk_mul_f32 v[214:215], v[100:101], s[42:43] op_sel_hi:[1,0]
	v_pk_mul_f32 v[212:213], v[212:213], s[42:43] op_sel_hi:[1,0]
	s_add_u32 s69, s56, s82
	v_pk_fma_f32 v[100:101], v[70:71], v[200:201], v[104:105]
	v_pk_fma_f32 v[104:105], v[72:73], v[210:211], v[106:107]
	v_pk_fma_f32 v[106:107], v[66:67], v[212:213], v[198:199]
	v_pk_fma_f32 v[108:109], v[68:69], v[214:215], v[108:109]
	v_cvt_pk_bf16_f32 v66, v100, v101
	v_cvt_pk_bf16_f32 v67, v104, v105
	v_cvt_pk_bf16_f32 v68, v106, v107
	s_addc_u32 s71, s57, s83
	v_cvt_pk_bf16_f32 v69, v108, v109
	ds_write_b128 v208, v[74:77]
	ds_write_b128 v208, v[66:69] offset:64
	s_add_u32 s70, s69, s76
	ds_read_b128 v[66:69], v207
	ds_read_b128 v[70:73], v207 offset:1152
	s_addc_u32 s71, s71, s77
	v_lshl_add_u64 v[74:75], s[70:71], 0, v[182:183]
	v_lshl_add_u64 v[74:75], v[74:75], 0, v[180:181]
	s_waitcnt lgkmcnt(1)
	global_store_dwordx4 v[74:75], v[66:69], off
	v_pk_fma_f32 v[64:65], v[64:65], s[38:39], v[16:17] op_sel_hi:[1,0,1]
	v_pk_fma_f32 v[62:63], v[62:63], s[38:39], v[14:15] op_sel_hi:[1,0,1]
	v_lshl_add_u64 v[66:67], s[70:71], 0, v[184:185]
	v_lshl_add_u64 v[66:67], v[66:67], 0, v[180:181]
	s_waitcnt lgkmcnt(0)
	global_store_dwordx4 v[66:67], v[70:73], off
	v_mov_b32_e32 v67, v175
	v_mov_b32_e32 v66, v175
	v_mov_b32_e32 v69, v175
	v_mov_b32_e32 v68, v175
	v_cvt_pk_fp8_f32 v67, v106, v107
	v_cvt_pk_fp8_f32 v66, v100, v101
	v_cvt_pk_fp8_f32 v69, v98, v99
	v_cvt_pk_fp8_f32 v68, v78, v79
	v_cvt_pk_fp8_f32 v67, v108, v109 op_sel:[0,0,1]
	v_cvt_pk_fp8_f32 v66, v104, v105 op_sel:[0,0,1]
	v_cvt_pk_fp8_f32 v69, v102, v103 op_sel:[0,0,1]
	v_cvt_pk_fp8_f32 v68, v80, v81 op_sel:[0,0,1]
	v_or_b32_e32 v70, s47, v195
	v_add_u32_e32 v70, s10, v70
	s_or_b32 s47, s72, 0xa0
	ds_write2_b64 v194, v[68:69], v[66:67] offset1:4
	ds_read_b128 v[66:69], v196
	v_ashrrev_i32_e32 v71, 31, v70
	s_add_i32 s70, s10, s47
	v_lshlrev_b64 v[70:71], 10, v[70:71]
	s_ashr_i32 s71, s70, 31
	v_lshl_add_u64 v[70:71], s[16:17], 0, v[70:71]
	s_lshl_b64 s[70:71], s[70:71], 11
	v_lshl_add_u64 v[70:71], v[70:71], 0, s[74:75]
	s_add_u32 s69, s54, s70
	v_lshl_add_u64 v[70:71], v[70:71], 0, v[190:191]
	s_addc_u32 s71, s55, s71
	v_pk_fma_f32 v[58:59], v[58:59], s[38:39], v[10:11] op_sel_hi:[1,0,1]
	s_waitcnt lgkmcnt(0)
	global_store_dwordx4 v[70:71], v[66:69], off
	s_add_u32 s70, s69, s76
	v_pk_mul_f32 v[62:63], v[62:63], s[40:41] op_sel_hi:[1,0]
	v_pk_mul_f32 v[58:59], v[58:59], s[40:41] op_sel_hi:[1,0]
	v_pk_mul_f32 v[64:65], v[64:65], s[40:41] op_sel_hi:[1,0]
	s_addc_u32 s71, s71, s77
	v_exp_f32_e32 v62, v62
	v_exp_f32_e32 v63, v63
	v_exp_f32_e32 v58, v58
	v_exp_f32_e32 v59, v59
	v_exp_f32_e32 v64, v64
	v_exp_f32_e32 v65, v65
	global_load_dwordx4 v[66:69], v[192:193], off offset:2048 nt
	v_lshl_add_u64 v[70:71], s[70:71], 0, v[182:183]
	v_lshl_add_u64 v[74:75], s[70:71], 0, v[184:185]
	v_lshl_add_u64 v[70:71], v[70:71], 0, v[180:181]
	v_lshl_add_u64 v[74:75], v[74:75], 0, v[180:181]
	v_pk_fma_f32 v[60:61], v[60:61], s[38:39], v[12:13] op_sel_hi:[1,0,1]
	global_load_dwordx4 v[70:73], v[70:71], off nt
	v_pk_mul_f32 v[60:61], v[60:61], s[40:41] op_sel_hi:[1,0]
	global_load_dwordx4 v[74:77], v[74:75], off nt
	s_waitcnt vmcnt(8)
	ds_write_b128 v207, v[86:89]
	s_waitcnt vmcnt(6)
	ds_write_b128 v207, v[90:93] offset:1152
	v_pk_fma_f32 v[56:57], v[56:57], s[38:39], v[8:9] op_sel_hi:[1,0,1]
	v_pk_fma_f32 v[54:55], v[54:55], s[38:39], v[6:7] op_sel_hi:[1,0,1]
	v_pk_fma_f32 v[52:53], v[52:53], s[38:39], v[4:5] op_sel_hi:[1,0,1]
	v_pk_fma_f32 v[50:51], v[50:51], s[38:39], v[2:3] op_sel_hi:[1,0,1]
	ds_read_b128 v[86:89], v208
	ds_read_b128 v[90:93], v208 offset:64
	v_cvt_pk_f32_fp8_e32 v[210:211], v82
	v_cvt_pk_f32_fp8_sdwa v[212:213], v82 src0_sel:WORD_1
	v_cvt_pk_f32_fp8_e32 v[214:215], v83
	v_cvt_pk_f32_fp8_sdwa v[82:83], v83 src0_sel:WORD_1
	v_pk_add_f32 v[62:63], v[62:63], 1.0 op_sel_hi:[1,0]
	v_pk_add_f32 v[58:59], v[58:59], 1.0 op_sel_hi:[1,0]
	v_exp_f32_e32 v60, v60
	v_exp_f32_e32 v61, v61
	v_pk_add_f32 v[64:65], v[64:65], 1.0 op_sel_hi:[1,0]
	v_pk_mul_f32 v[54:55], v[54:55], s[40:41] op_sel_hi:[1,0]
	v_pk_mul_f32 v[50:51], v[50:51], s[40:41] op_sel_hi:[1,0]
	v_pk_mul_f32 v[56:57], v[56:57], s[40:41] op_sel_hi:[1,0]
	v_pk_mul_f32 v[52:53], v[52:53], s[40:41] op_sel_hi:[1,0]
	v_rcp_f32_e32 v62, v62
	v_rcp_f32_e32 v63, v63
	v_rcp_f32_e32 v58, v58
	v_rcp_f32_e32 v59, v59
	v_rcp_f32_e32 v64, v64
	v_rcp_f32_e32 v65, v65
	v_exp_f32_e32 v54, v54
	v_exp_f32_e32 v55, v55
	v_exp_f32_e32 v50, v50
	v_exp_f32_e32 v51, v51
	v_exp_f32_e32 v56, v56
	v_exp_f32_e32 v57, v57
	v_exp_f32_e32 v52, v52
	v_exp_f32_e32 v53, v53
	s_waitcnt lgkmcnt(1)
	v_lshlrev_b32_e32 v198, 16, v86
	v_and_b32_e32 v199, 0xffff0000, v86
	v_lshlrev_b32_e32 v86, 16, v87
	v_and_b32_e32 v87, 0xffff0000, v87
	v_lshlrev_b32_e32 v200, 16, v88
	v_and_b32_e32 v201, 0xffff0000, v88
	v_pk_add_f32 v[60:61], v[60:61], 1.0 op_sel_hi:[1,0]
	v_pk_mul_f32 v[212:213], v[212:213], s[42:43] op_sel_hi:[1,0]
	v_pk_mul_f32 v[210:211], v[210:211], s[42:43] op_sel_hi:[1,0]
	v_pk_mul_f32 v[216:217], v[82:83], s[42:43] op_sel_hi:[1,0]
	v_pk_mul_f32 v[82:83], v[214:215], s[42:43] op_sel_hi:[1,0]
	v_rcp_f32_e32 v60, v60
	v_rcp_f32_e32 v61, v61
	v_pk_fma_f32 v[62:63], v[62:63], v[210:211], v[198:199]
	v_pk_fma_f32 v[64:65], v[64:65], v[212:213], v[86:87]
	v_pk_fma_f32 v[82:83], v[58:59], v[82:83], v[200:201]
	v_cvt_pk_f32_fp8_e32 v[200:201], v84
	v_cvt_pk_f32_fp8_sdwa v[210:211], v84 src0_sel:WORD_1
	v_cvt_pk_f32_fp8_e32 v[212:213], v85
	v_cvt_pk_f32_fp8_sdwa v[84:85], v85 src0_sel:WORD_1
	v_pk_add_f32 v[54:55], v[54:55], 1.0 op_sel_hi:[1,0]
	v_pk_add_f32 v[50:51], v[50:51], 1.0 op_sel_hi:[1,0]
	v_pk_add_f32 v[56:57], v[56:57], 1.0 op_sel_hi:[1,0]
	v_pk_add_f32 v[52:53], v[52:53], 1.0 op_sel_hi:[1,0]
	v_rcp_f32_e32 v54, v54
	v_rcp_f32_e32 v55, v55
	v_rcp_f32_e32 v50, v50
	v_rcp_f32_e32 v51, v51
	v_rcp_f32_e32 v56, v56
	v_rcp_f32_e32 v57, v57
	v_rcp_f32_e32 v52, v52
	v_rcp_f32_e32 v53, v53
	s_or_b32 s70, s78, 16
	s_ashr_i32 s71, s70, 31
	v_lshlrev_b32_e32 v88, 16, v89
	v_and_b32_e32 v89, 0xffff0000, v89
	s_lshl_b64 s[70:71], s[70:71], 11
	v_pk_fma_f32 v[86:87], v[60:61], v[216:217], v[88:89]
	v_cvt_pk_bf16_f32 v58, v62, v63
	v_cvt_pk_bf16_f32 v59, v64, v65
	v_cvt_pk_bf16_f32 v60, v82, v83
	s_waitcnt lgkmcnt(0)
	v_lshlrev_b32_e32 v88, 16, v90
	v_cvt_pk_bf16_f32 v61, v86, v87
	v_and_b32_e32 v89, 0xffff0000, v90
	v_lshlrev_b32_e32 v90, 16, v91
	v_and_b32_e32 v91, 0xffff0000, v91
	v_lshlrev_b32_e32 v198, 16, v92
	v_and_b32_e32 v199, 0xffff0000, v92
	v_lshlrev_b32_e32 v92, 16, v93
	v_and_b32_e32 v93, 0xffff0000, v93
	v_pk_mul_f32 v[210:211], v[210:211], s[42:43] op_sel_hi:[1,0]
	v_pk_mul_f32 v[200:201], v[200:201], s[42:43] op_sel_hi:[1,0]
	v_pk_mul_f32 v[214:215], v[84:85], s[42:43] op_sel_hi:[1,0]
	v_pk_mul_f32 v[212:213], v[212:213], s[42:43] op_sel_hi:[1,0]
	s_add_u32 s69, s56, s70
	v_pk_fma_f32 v[84:85], v[54:55], v[200:201], v[88:89]
	v_pk_fma_f32 v[88:89], v[56:57], v[210:211], v[90:91]
	v_pk_fma_f32 v[90:91], v[50:51], v[212:213], v[198:199]
	v_pk_fma_f32 v[92:93], v[52:53], v[214:215], v[92:93]
	v_cvt_pk_bf16_f32 v50, v84, v85
	v_cvt_pk_bf16_f32 v51, v88, v89
	v_cvt_pk_bf16_f32 v52, v90, v91
	s_addc_u32 s71, s57, s71
	v_cvt_pk_bf16_f32 v53, v92, v93
	ds_write_b128 v208, v[58:61]
	ds_write_b128 v208, v[50:53] offset:64
	s_add_u32 s70, s69, s76
	ds_read_b128 v[50:53], v207
	ds_read_b128 v[54:57], v207 offset:1152
	s_addc_u32 s71, s71, s77
	v_lshl_add_u64 v[58:59], s[70:71], 0, v[182:183]
	v_lshl_add_u64 v[58:59], v[58:59], 0, v[180:181]
	s_waitcnt lgkmcnt(1)
	global_store_dwordx4 v[58:59], v[50:53], off
	v_pk_fma_f32 v[42:43], v[42:43], s[38:39], v[10:11] op_sel_hi:[1,0,1]
	v_pk_fma_f32 v[48:49], v[48:49], s[38:39], v[16:17] op_sel_hi:[1,0,1]
	v_lshl_add_u64 v[50:51], s[70:71], 0, v[184:185]
	v_lshl_add_u64 v[50:51], v[50:51], 0, v[180:181]
	s_waitcnt lgkmcnt(0)
	global_store_dwordx4 v[50:51], v[54:57], off
	v_mov_b32_e32 v51, v175
	v_mov_b32_e32 v50, v175
	v_mov_b32_e32 v53, v175
	v_mov_b32_e32 v52, v175
	v_cvt_pk_fp8_f32 v51, v90, v91
	v_cvt_pk_fp8_f32 v50, v84, v85
	v_cvt_pk_fp8_f32 v53, v82, v83
	v_cvt_pk_fp8_f32 v52, v62, v63
	v_cvt_pk_fp8_f32 v51, v92, v93 op_sel:[0,0,1]
	v_cvt_pk_fp8_f32 v50, v88, v89 op_sel:[0,0,1]
	v_cvt_pk_fp8_f32 v53, v86, v87 op_sel:[0,0,1]
	v_cvt_pk_fp8_f32 v52, v64, v65 op_sel:[0,0,1]
	v_or_b32_e32 v54, s68, v195
	s_or_b32 s68, s72, 0xb0
	s_add_i32 s70, s10, s68
	ds_write2_b64 v194, v[52:53], v[50:51] offset1:4
	v_add_u32_e32 v54, s10, v54
	s_ashr_i32 s71, s70, 31
	ds_read_b128 v[50:53], v196
	v_ashrrev_i32_e32 v55, 31, v54
	s_lshl_b64 s[70:71], s[70:71], 11
	v_lshlrev_b64 v[54:55], 10, v[54:55]
	s_add_u32 s69, s54, s70
	v_lshl_add_u64 v[54:55], s[16:17], 0, v[54:55]
	s_addc_u32 s71, s55, s71
	v_lshl_add_u64 v[54:55], v[54:55], 0, s[74:75]
	s_add_u32 s70, s69, s76
	v_lshl_add_u64 v[54:55], v[54:55], 0, v[190:191]
	s_addc_u32 s71, s71, s77
	s_waitcnt lgkmcnt(0)
	global_store_dwordx4 v[54:55], v[50:53], off
	v_lshl_add_u64 v[54:55], s[70:71], 0, v[182:183]
	v_lshl_add_u64 v[54:55], v[54:55], 0, v[180:181]
	v_lshl_add_u64 v[58:59], s[70:71], 0, v[184:185]
	global_load_dwordx4 v[54:57], v[54:55], off nt
	v_lshl_add_u64 v[58:59], v[58:59], 0, v[180:181]
	global_load_dwordx4 v[50:53], v[192:193], off offset:3072 nt
	v_pk_mul_f32 v[42:43], v[42:43], s[40:41] op_sel_hi:[1,0]
	global_load_dwordx4 v[58:61], v[58:59], off nt
	v_exp_f32_e32 v42, v42
	v_exp_f32_e32 v43, v43
	v_pk_fma_f32 v[34:35], v[34:35], s[38:39], v[2:3] op_sel_hi:[1,0,1]
	v_pk_fma_f32 v[46:47], v[46:47], s[38:39], v[14:15] op_sel_hi:[1,0,1]
	v_pk_mul_f32 v[34:35], v[34:35], s[40:41] op_sel_hi:[1,0]
	v_pk_add_f32 v[42:43], v[42:43], 1.0 op_sel_hi:[1,0]
	v_pk_mul_f32 v[46:47], v[46:47], s[40:41] op_sel_hi:[1,0]
	v_rcp_f32_e32 v214, v42
	v_rcp_f32_e32 v215, v43
	v_pk_mul_f32 v[42:43], v[48:49], s[40:41] op_sel_hi:[1,0]
	v_exp_f32_e32 v34, v34
	v_exp_f32_e32 v42, v42
	v_exp_f32_e32 v43, v43
	v_exp_f32_e32 v35, v35
	s_waitcnt vmcnt(8)
	v_cvt_pk_f32_fp8_e32 v[200:201], v66
	v_cvt_pk_f32_fp8_e32 v[212:213], v67
	v_exp_f32_e32 v46, v46
	v_exp_f32_e32 v47, v47
	v_pk_fma_f32 v[44:45], v[44:45], s[38:39], v[12:13] op_sel_hi:[1,0,1]
	s_waitcnt vmcnt(7)
	ds_write_b128 v207, v[70:73]
	s_waitcnt vmcnt(6)
	ds_write_b128 v207, v[74:77] offset:1152
	v_pk_mul_f32 v[44:45], v[44:45], s[40:41] op_sel_hi:[1,0]
	v_pk_add_f32 v[42:43], v[42:43], 1.0 op_sel_hi:[1,0]
	v_pk_fma_f32 v[40:41], v[40:41], s[38:39], v[8:9] op_sel_hi:[1,0,1]
	v_pk_fma_f32 v[38:39], v[38:39], s[38:39], v[6:7] op_sel_hi:[1,0,1]
	v_pk_fma_f32 v[36:37], v[36:37], s[38:39], v[4:5] op_sel_hi:[1,0,1]
	v_pk_add_f32 v[34:35], v[34:35], 1.0 op_sel_hi:[1,0]
	ds_read_b128 v[70:73], v208
	ds_read_b128 v[74:77], v208 offset:64
	v_pk_add_f32 v[46:47], v[46:47], 1.0 op_sel_hi:[1,0]
	v_exp_f32_e32 v44, v44
	v_exp_f32_e32 v45, v45
	v_rcp_f32_e32 v48, v42
	v_rcp_f32_e32 v49, v43
	v_pk_mul_f32 v[42:43], v[200:201], s[42:43] op_sel_hi:[1,0]
	v_pk_mul_f32 v[200:201], v[212:213], s[42:43] op_sel_hi:[1,0]
	v_pk_mul_f32 v[38:39], v[38:39], s[40:41] op_sel_hi:[1,0]
	v_rcp_f32_e32 v212, v34
	v_rcp_f32_e32 v213, v35
	v_pk_mul_f32 v[34:35], v[40:41], s[40:41] op_sel_hi:[1,0]
	v_pk_mul_f32 v[36:37], v[36:37], s[40:41] op_sel_hi:[1,0]
	v_cvt_pk_f32_fp8_sdwa v[210:211], v66 src0_sel:WORD_1
	v_rcp_f32_e32 v46, v46
	v_rcp_f32_e32 v47, v47
	v_exp_f32_e32 v38, v38
	v_exp_f32_e32 v39, v39
	v_exp_f32_e32 v34, v34
	v_exp_f32_e32 v35, v35
	v_exp_f32_e32 v36, v36
	v_exp_f32_e32 v37, v37
	s_waitcnt lgkmcnt(1)
	v_lshlrev_b32_e32 v192, 16, v70
	v_and_b32_e32 v193, 0xffff0000, v70
	v_lshlrev_b32_e32 v198, 16, v72
	v_and_b32_e32 v199, 0xffff0000, v72
	v_cvt_pk_f32_fp8_sdwa v[66:67], v67 src0_sel:WORD_1
	v_pk_add_f32 v[44:45], v[44:45], 1.0 op_sel_hi:[1,0]
	v_pk_fma_f32 v[42:43], v[46:47], v[42:43], v[192:193]
	v_rcp_f32_e32 v216, v44
	v_rcp_f32_e32 v217, v45
	v_pk_mul_f32 v[44:45], v[210:211], s[42:43] op_sel_hi:[1,0]
	v_pk_fma_f32 v[46:47], v[214:215], v[200:201], v[198:199]
	v_cvt_pk_f32_fp8_e32 v[198:199], v68
	v_cvt_pk_f32_fp8_sdwa v[200:201], v68 src0_sel:WORD_1
	v_cvt_pk_f32_fp8_e32 v[210:211], v69
	v_cvt_pk_f32_fp8_sdwa v[68:69], v69 src0_sel:WORD_1
	v_pk_add_f32 v[38:39], v[38:39], 1.0 op_sel_hi:[1,0]
	v_pk_add_f32 v[34:35], v[34:35], 1.0 op_sel_hi:[1,0]
	v_pk_add_f32 v[36:37], v[36:37], 1.0 op_sel_hi:[1,0]
	v_rcp_f32_e32 v38, v38
	v_rcp_f32_e32 v39, v39
	v_rcp_f32_e32 v40, v34
	v_rcp_f32_e32 v41, v35
	v_rcp_f32_e32 v214, v36
	v_rcp_f32_e32 v215, v37
	s_or_b32 s70, s78, 32
	s_ashr_i32 s71, s70, 31
	v_lshlrev_b32_e32 v70, 16, v71
	v_and_b32_e32 v71, 0xffff0000, v71
	v_lshlrev_b32_e32 v72, 16, v73
	v_and_b32_e32 v73, 0xffff0000, v73
	v_pk_mul_f32 v[66:67], v[66:67], s[42:43] op_sel_hi:[1,0]
	s_lshl_b64 s[70:71], s[70:71], 11
	v_pk_fma_f32 v[44:45], v[48:49], v[44:45], v[70:71]
	v_pk_fma_f32 v[48:49], v[216:217], v[66:67], v[72:73]
	v_cvt_pk_bf16_f32 v70, v42, v43
	v_cvt_pk_bf16_f32 v71, v44, v45
	v_cvt_pk_bf16_f32 v72, v46, v47
	s_waitcnt lgkmcnt(0)
	v_lshlrev_b32_e32 v66, 16, v74
	v_cvt_pk_bf16_f32 v73, v48, v49
	v_and_b32_e32 v67, 0xffff0000, v74
	v_lshlrev_b32_e32 v74, 16, v75
	v_and_b32_e32 v75, 0xffff0000, v75
	v_lshlrev_b32_e32 v192, 16, v76
	v_and_b32_e32 v193, 0xffff0000, v76
	v_lshlrev_b32_e32 v76, 16, v77
	v_and_b32_e32 v77, 0xffff0000, v77
	v_pk_mul_f32 v[36:37], v[200:201], s[42:43] op_sel_hi:[1,0]
	v_pk_mul_f32 v[34:35], v[198:199], s[42:43] op_sel_hi:[1,0]
	v_pk_mul_f32 v[68:69], v[68:69], s[42:43] op_sel_hi:[1,0]
	v_pk_mul_f32 v[198:199], v[210:211], s[42:43] op_sel_hi:[1,0]
	s_add_u32 s69, s56, s70
	v_pk_fma_f32 v[34:35], v[38:39], v[34:35], v[66:67]
	v_pk_fma_f32 v[36:37], v[40:41], v[36:37], v[74:75]
	v_pk_fma_f32 v[38:39], v[212:213], v[198:199], v[192:193]
	v_pk_fma_f32 v[40:41], v[214:215], v[68:69], v[76:77]
	v_cvt_pk_bf16_f32 v66, v34, v35
	v_cvt_pk_bf16_f32 v67, v36, v37
	v_cvt_pk_bf16_f32 v68, v38, v39
	s_addc_u32 s71, s57, s71
	v_cvt_pk_bf16_f32 v69, v40, v41
	ds_write_b128 v208, v[70:73]
	ds_write_b128 v208, v[66:69] offset:64
	s_add_u32 s70, s69, s76
	ds_read_b128 v[66:69], v207
	ds_read_b128 v[70:73], v207 offset:1152
	s_addc_u32 s71, s71, s77
	v_lshl_add_u64 v[74:75], s[70:71], 0, v[182:183]
	v_lshl_add_u64 v[74:75], v[74:75], 0, v[180:181]
	s_waitcnt lgkmcnt(1)
	global_store_dwordx4 v[74:75], v[66:69], off
	v_pk_fma_f32 v[10:11], v[26:27], s[38:39], v[10:11] op_sel_hi:[1,0,1]
	v_pk_fma_f32 v[16:17], v[32:33], s[38:39], v[16:17] op_sel_hi:[1,0,1]
	v_lshl_add_u64 v[66:67], s[70:71], 0, v[184:185]
	v_lshl_add_u64 v[66:67], v[66:67], 0, v[180:181]
	s_waitcnt lgkmcnt(0)
	global_store_dwordx4 v[66:67], v[70:73], off
	v_mov_b32_e32 v67, v175
	v_mov_b32_e32 v66, v175
	v_mov_b32_e32 v69, v175
	v_mov_b32_e32 v68, v175
	v_cvt_pk_fp8_f32 v67, v38, v39
	v_cvt_pk_fp8_f32 v66, v34, v35
	v_cvt_pk_fp8_f32 v69, v46, v47
	v_cvt_pk_fp8_f32 v68, v42, v43
	v_cvt_pk_fp8_f32 v67, v40, v41 op_sel:[0,0,1]
	v_cvt_pk_fp8_f32 v66, v36, v37 op_sel:[0,0,1]
	v_cvt_pk_fp8_f32 v69, v48, v49 op_sel:[0,0,1]
	v_cvt_pk_fp8_f32 v68, v44, v45 op_sel:[0,0,1]
	v_pk_mul_f32 v[10:11], v[10:11], s[40:41] op_sel_hi:[1,0]
	v_or_b32_e32 v70, s47, v195
	v_exp_f32_e32 v10, v10
	v_exp_f32_e32 v11, v11
	ds_write2_b64 v194, v[68:69], v[66:67] offset1:4
	v_add_u32_e32 v70, s10, v70
	ds_read_b128 v[66:69], v196
	v_ashrrev_i32_e32 v71, 31, v70
	v_lshlrev_b64 v[70:71], 10, v[70:71]
	v_pk_fma_f32 v[14:15], v[30:31], s[38:39], v[14:15] op_sel_hi:[1,0,1]
	v_pk_fma_f32 v[12:13], v[28:29], s[38:39], v[12:13] op_sel_hi:[1,0,1]
	v_pk_add_f32 v[10:11], v[10:11], 1.0 op_sel_hi:[1,0]
	v_lshl_add_u64 v[70:71], s[16:17], 0, v[70:71]
	v_pk_mul_f32 v[14:15], v[14:15], s[40:41] op_sel_hi:[1,0]
	v_rcp_f32_e32 v26, v10
	v_rcp_f32_e32 v27, v11
	v_pk_mul_f32 v[10:11], v[16:17], s[40:41] op_sel_hi:[1,0]
	v_pk_mul_f32 v[12:13], v[12:13], s[40:41] op_sel_hi:[1,0]
	v_lshl_add_u64 v[70:71], v[70:71], 0, s[74:75]
	v_exp_f32_e32 v14, v14
	v_exp_f32_e32 v15, v15
	v_exp_f32_e32 v10, v10
	v_exp_f32_e32 v11, v11
	v_exp_f32_e32 v12, v12
	v_exp_f32_e32 v13, v13
	v_lshl_add_u64 v[70:71], v[70:71], 0, v[190:191]
	s_waitcnt lgkmcnt(0)
	global_store_dwordx4 v[70:71], v[66:69], off
	s_waitcnt vmcnt(5)
	ds_write_b128 v207, v[54:57]
	s_waitcnt vmcnt(3)
	ds_write_b128 v207, v[58:61] offset:1152
	v_pk_fma_f32 v[8:9], v[24:25], s[38:39], v[8:9] op_sel_hi:[1,0,1]
	v_pk_fma_f32 v[6:7], v[22:23], s[38:39], v[6:7] op_sel_hi:[1,0,1]
	v_pk_fma_f32 v[4:5], v[20:21], s[38:39], v[4:5] op_sel_hi:[1,0,1]
	v_pk_fma_f32 v[2:3], v[18:19], s[38:39], v[2:3] op_sel_hi:[1,0,1]
	ds_read_b128 v[54:57], v208
	ds_read_b128 v[58:61], v208 offset:64
	v_cvt_pk_f32_fp8_e32 v[70:71], v50
	v_cvt_pk_f32_fp8_sdwa v[72:73], v50 src0_sel:WORD_1
	v_cvt_pk_f32_fp8_e32 v[74:75], v51
	v_cvt_pk_f32_fp8_sdwa v[50:51], v51 src0_sel:WORD_1
	v_pk_add_f32 v[14:15], v[14:15], 1.0 op_sel_hi:[1,0]
	v_pk_add_f32 v[10:11], v[10:11], 1.0 op_sel_hi:[1,0]
	v_pk_add_f32 v[12:13], v[12:13], 1.0 op_sel_hi:[1,0]
	v_pk_mul_f32 v[6:7], v[6:7], s[40:41] op_sel_hi:[1,0]
	v_pk_mul_f32 v[2:3], v[2:3], s[40:41] op_sel_hi:[1,0]
	v_pk_mul_f32 v[8:9], v[8:9], s[40:41] op_sel_hi:[1,0]
	v_pk_mul_f32 v[4:5], v[4:5], s[40:41] op_sel_hi:[1,0]
	v_rcp_f32_e32 v14, v14
	v_rcp_f32_e32 v15, v15
	v_rcp_f32_e32 v16, v10
	v_rcp_f32_e32 v17, v11
	v_rcp_f32_e32 v28, v12
	v_rcp_f32_e32 v29, v13
	v_exp_f32_e32 v6, v6
	v_exp_f32_e32 v7, v7
	v_exp_f32_e32 v2, v2
	v_exp_f32_e32 v3, v3
	v_exp_f32_e32 v8, v8
	v_exp_f32_e32 v9, v9
	v_exp_f32_e32 v4, v4
	v_exp_f32_e32 v5, v5
	s_waitcnt lgkmcnt(1)
	v_lshlrev_b32_e32 v66, 16, v54
	v_and_b32_e32 v67, 0xffff0000, v54
	v_lshlrev_b32_e32 v54, 16, v55
	v_and_b32_e32 v55, 0xffff0000, v55
	v_lshlrev_b32_e32 v68, 16, v56
	v_and_b32_e32 v69, 0xffff0000, v56
	v_lshlrev_b32_e32 v56, 16, v57
	v_and_b32_e32 v57, 0xffff0000, v57
	v_pk_mul_f32 v[12:13], v[72:73], s[42:43] op_sel_hi:[1,0]
	v_pk_mul_f32 v[10:11], v[70:71], s[42:43] op_sel_hi:[1,0]
	v_pk_mul_f32 v[30:31], v[50:51], s[42:43] op_sel_hi:[1,0]
	v_pk_mul_f32 v[32:33], v[74:75], s[42:43] op_sel_hi:[1,0]
	v_pk_fma_f32 v[10:11], v[14:15], v[10:11], v[66:67]
	v_pk_fma_f32 v[12:13], v[16:17], v[12:13], v[54:55]
	v_pk_fma_f32 v[14:15], v[26:27], v[32:33], v[68:69]
	v_pk_fma_f32 v[16:17], v[28:29], v[30:31], v[56:57]
	s_waitcnt lgkmcnt(0)
	v_lshlrev_b32_e32 v30, 16, v58
	v_and_b32_e32 v31, 0xffff0000, v58
	v_lshlrev_b32_e32 v32, 16, v59
	v_and_b32_e32 v33, 0xffff0000, v59
	v_lshlrev_b32_e32 v50, 16, v60
	v_and_b32_e32 v51, 0xffff0000, v60
	v_lshlrev_b32_e32 v54, 16, v61
	v_and_b32_e32 v55, 0xffff0000, v61
	v_cvt_pk_f32_fp8_e32 v[56:57], v52
	v_cvt_pk_f32_fp8_sdwa v[58:59], v52 src0_sel:WORD_1
	v_cvt_pk_f32_fp8_e32 v[60:61], v53
	v_cvt_pk_f32_fp8_sdwa v[52:53], v53 src0_sel:WORD_1
	v_pk_add_f32 v[6:7], v[6:7], 1.0 op_sel_hi:[1,0]
	v_pk_add_f32 v[2:3], v[2:3], 1.0 op_sel_hi:[1,0]
	v_pk_add_f32 v[8:9], v[8:9], 1.0 op_sel_hi:[1,0]
	v_pk_add_f32 v[4:5], v[4:5], 1.0 op_sel_hi:[1,0]
	v_rcp_f32_e32 v6, v6
	v_rcp_f32_e32 v7, v7
	v_rcp_f32_e32 v2, v2
	v_rcp_f32_e32 v3, v3
	v_rcp_f32_e32 v8, v8
	v_rcp_f32_e32 v9, v9
	v_rcp_f32_e32 v4, v4
	v_rcp_f32_e32 v5, v5
	s_or_b32 s70, s78, 48
	s_ashr_i32 s71, s70, 31
	s_lshl_b64 s[70:71], s[70:71], 11
	v_cvt_pk_bf16_f32 v26, v10, v11
	v_cvt_pk_bf16_f32 v27, v12, v13
	v_cvt_pk_bf16_f32 v28, v14, v15
	v_cvt_pk_bf16_f32 v29, v16, v17
	v_pk_mul_f32 v[18:19], v[58:59], s[42:43] op_sel_hi:[1,0]
	v_pk_mul_f32 v[20:21], v[56:57], s[42:43] op_sel_hi:[1,0]
	v_pk_mul_f32 v[22:23], v[52:53], s[42:43] op_sel_hi:[1,0]
	v_pk_mul_f32 v[24:25], v[60:61], s[42:43] op_sel_hi:[1,0]
	s_add_u32 s47, s56, s70
	v_pk_fma_f32 v[20:21], v[6:7], v[20:21], v[30:31]
	v_pk_fma_f32 v[18:19], v[8:9], v[18:19], v[32:33]
	v_pk_fma_f32 v[24:25], v[2:3], v[24:25], v[50:51]
	v_pk_fma_f32 v[22:23], v[4:5], v[22:23], v[54:55]
	v_cvt_pk_bf16_f32 v2, v20, v21
	v_cvt_pk_bf16_f32 v3, v18, v19
	v_cvt_pk_bf16_f32 v4, v24, v25
	s_addc_u32 s69, s57, s71
	v_cvt_pk_bf16_f32 v5, v22, v23
	ds_write_b128 v208, v[26:29]
	ds_write_b128 v208, v[2:5] offset:64
	s_add_u32 s70, s47, s76
	ds_read_b128 v[2:5], v207
	ds_read_b128 v[6:9], v207 offset:1152
	s_addc_u32 s71, s69, s77
	v_lshl_add_u64 v[26:27], s[70:71], 0, v[182:183]
	v_lshl_add_u64 v[26:27], v[26:27], 0, v[180:181]
	s_waitcnt lgkmcnt(1)
	global_store_dwordx4 v[26:27], v[2:5], off
	s_lshl_b32 s47, s64, 2
	s_ashr_i32 s73, s72, 31
	v_lshl_add_u64 v[2:3], s[70:71], 0, v[184:185]
	v_lshl_add_u64 v[2:3], v[2:3], 0, v[180:181]
	s_waitcnt lgkmcnt(0)
	global_store_dwordx4 v[2:3], v[6:9], off
	v_mov_b32_e32 v3, v175
	v_mov_b32_e32 v2, v175
	v_mov_b32_e32 v5, v175
	v_mov_b32_e32 v4, v175
	v_cvt_pk_fp8_f32 v3, v24, v25
	v_cvt_pk_fp8_f32 v2, v20, v21
	v_cvt_pk_fp8_f32 v5, v14, v15
	v_cvt_pk_fp8_f32 v4, v10, v11
	v_cvt_pk_fp8_f32 v3, v22, v23 op_sel:[0,0,1]
	v_cvt_pk_fp8_f32 v2, v18, v19 op_sel:[0,0,1]
	v_cvt_pk_fp8_f32 v5, v16, v17 op_sel:[0,0,1]
	v_cvt_pk_fp8_f32 v4, v12, v13 op_sel:[0,0,1]
	v_or_b32_e32 v6, s68, v195
	v_add_u32_e32 v6, s10, v6
	v_ashrrev_i32_e32 v7, 31, v6
	ds_write2_b64 v194, v[4:5], v[2:3] offset1:4
	ds_read_b128 v[2:5], v196
	v_lshlrev_b64 v[6:7], 10, v[6:7]
	v_lshl_add_u64 v[6:7], s[16:17], 0, v[6:7]
	v_lshl_add_u64 v[6:7], v[6:7], 0, s[74:75]
	v_lshl_add_u64 v[6:7], v[6:7], 0, v[190:191]
	s_waitcnt lgkmcnt(0)
	global_store_dwordx4 v[6:7], v[2:5], off
	v_mul_f32_e32 v6, v37, v37
	v_fmac_f32_e32 v6, v36, v36
	v_mul_f32_e32 v2, v15, v15
	v_mul_f32_e32 v3, v17, v17
	v_fmac_f32_e32 v2, v14, v14
	v_fmac_f32_e32 v3, v16, v16
	v_add_f32_e32 v2, v2, v3
	v_mul_f32_e32 v3, v11, v11
	v_mul_f32_e32 v4, v13, v13
	v_fmac_f32_e32 v3, v10, v10
	v_fmac_f32_e32 v4, v12, v12
	v_add_f32_e32 v3, v3, v4
	v_add_f32_e32 v2, v3, v2
	v_mul_f32_e32 v3, v25, v25
	v_mul_f32_e32 v4, v23, v23
	v_fmac_f32_e32 v3, v24, v24
	v_fmac_f32_e32 v4, v22, v22
	v_add_f32_e32 v3, v3, v4
	v_mul_f32_e32 v4, v21, v21
	v_mul_f32_e32 v5, v19, v19
	v_fmac_f32_e32 v4, v20, v20
	v_fmac_f32_e32 v5, v18, v18
	v_add_f32_e32 v4, v4, v5
	v_add_f32_e32 v3, v4, v3
	v_add_f32_e32 v2, v2, v3
	v_mul_f32_e32 v3, v47, v47
	v_mul_f32_e32 v4, v49, v49
	v_fmac_f32_e32 v3, v46, v46
	v_fmac_f32_e32 v4, v48, v48
	v_add_f32_e32 v3, v3, v4
	v_mul_f32_e32 v4, v43, v43
	v_mul_f32_e32 v5, v45, v45
	v_fmac_f32_e32 v4, v42, v42
	v_fmac_f32_e32 v5, v44, v44
	v_add_f32_e32 v4, v4, v5
	v_add_f32_e32 v3, v4, v3
	v_mul_f32_e32 v4, v39, v39
	v_mul_f32_e32 v5, v41, v41
	v_fmac_f32_e32 v4, v38, v38
	v_fmac_f32_e32 v5, v40, v40
	v_add_f32_e32 v4, v4, v5
	v_mul_f32_e32 v5, v35, v35
	v_fmac_f32_e32 v5, v34, v34
	v_add_f32_e32 v5, v5, v6
	v_add_f32_e32 v4, v5, v4
	v_add_f32_e32 v3, v3, v4
	v_mul_f32_e32 v4, v83, v83
	v_mul_f32_e32 v5, v87, v87
	v_fmac_f32_e32 v4, v82, v82
	v_fmac_f32_e32 v5, v86, v86
	v_add_f32_e32 v4, v4, v5
	v_mul_f32_e32 v5, v63, v63
	v_mul_f32_e32 v6, v65, v65
	v_fmac_f32_e32 v5, v62, v62
	v_fmac_f32_e32 v6, v64, v64
	v_add_f32_e32 v5, v5, v6
	v_add_f32_e32 v4, v5, v4
	v_mul_f32_e32 v5, v91, v91
	v_mul_f32_e32 v6, v93, v93
	v_fmac_f32_e32 v5, v90, v90
	v_fmac_f32_e32 v6, v92, v92
	v_add_f32_e32 v5, v5, v6
	v_mul_f32_e32 v6, v85, v85
	v_mul_f32_e32 v7, v89, v89
	v_fmac_f32_e32 v6, v84, v84
	v_fmac_f32_e32 v7, v88, v88
	v_add_f32_e32 v6, v6, v7
	v_add_f32_e32 v5, v6, v5
	v_add_f32_e32 v4, v4, v5
	v_mul_f32_e32 v5, v99, v99
	v_mul_f32_e32 v6, v103, v103
	v_fmac_f32_e32 v5, v98, v98
	v_fmac_f32_e32 v6, v102, v102
	v_add_f32_e32 v5, v5, v6
	v_mul_f32_e32 v6, v79, v79
	v_mul_f32_e32 v7, v81, v81
	v_fmac_f32_e32 v6, v78, v78
	v_fmac_f32_e32 v7, v80, v80
	v_add_f32_e32 v6, v6, v7
	v_add_f32_e32 v5, v6, v5
	v_mul_f32_e32 v6, v107, v107
	v_mul_f32_e32 v7, v109, v109
	v_fmac_f32_e32 v6, v106, v106
	v_fmac_f32_e32 v7, v108, v108
	v_add_f32_e32 v6, v6, v7
	v_mul_f32_e32 v7, v101, v101
	v_mul_f32_e32 v8, v105, v105
	v_fmac_f32_e32 v7, v100, v100
	v_fmac_f32_e32 v8, v104, v104
	v_add_f32_e32 v7, v7, v8
	v_add_f32_e32 v6, v7, v6
	v_add_f32_e32 v5, v5, v6
	v_mul_f32_e32 v6, v119, v119
	v_mul_f32_e32 v7, v115, v115
	v_fmac_f32_e32 v6, v118, v118
	v_fmac_f32_e32 v7, v114, v114
	v_add_f32_e32 v6, v6, v7
	v_mul_f32_e32 v7, v97, v97
	v_mul_f32_e32 v8, v95, v95
	v_fmac_f32_e32 v7, v96, v96
	v_fmac_f32_e32 v8, v94, v94
	v_add_f32_e32 v7, v7, v8
	v_add_f32_e32 v6, v7, v6
	v_mul_f32_e32 v7, v125, v125
	v_mul_f32_e32 v8, v123, v123
	v_fmac_f32_e32 v7, v124, v124
	v_fmac_f32_e32 v8, v122, v122
	v_add_f32_e32 v7, v7, v8
	v_mul_f32_e32 v8, v121, v121
	v_mul_f32_e32 v9, v117, v117
	v_fmac_f32_e32 v8, v120, v120
	v_fmac_f32_e32 v9, v116, v116
	v_add_f32_e32 v8, v8, v9
	v_add_f32_e32 v7, v8, v7
	v_add_f32_e32 v6, v6, v7
	v_mul_f32_e32 v7, v135, v135
	v_mul_f32_e32 v8, v131, v131
	v_fmac_f32_e32 v7, v134, v134
	v_fmac_f32_e32 v8, v130, v130
	v_add_f32_e32 v7, v7, v8
	v_mul_f32_e32 v8, v113, v113
	v_mul_f32_e32 v9, v111, v111
	v_fmac_f32_e32 v8, v112, v112
	v_fmac_f32_e32 v9, v110, v110
	v_add_f32_e32 v8, v8, v9
	v_add_f32_e32 v7, v8, v7
	v_mul_f32_e32 v8, v141, v141
	v_mul_f32_e32 v9, v139, v139
	v_fmac_f32_e32 v8, v140, v140
	v_fmac_f32_e32 v9, v138, v138
	v_add_f32_e32 v8, v8, v9
	v_mul_f32_e32 v9, v137, v137
	v_mul_f32_e32 v10, v133, v133
	v_fmac_f32_e32 v9, v136, v136
	v_fmac_f32_e32 v10, v132, v132
	v_add_f32_e32 v9, v9, v10
	v_add_f32_e32 v8, v9, v8
	v_add_f32_e32 v7, v7, v8
	v_mul_f32_e32 v8, v151, v151
	v_mul_f32_e32 v9, v147, v147
	v_fmac_f32_e32 v8, v150, v150
	v_fmac_f32_e32 v9, v146, v146
	v_add_f32_e32 v8, v8, v9
	v_mul_f32_e32 v9, v129, v129
	v_mul_f32_e32 v10, v127, v127
	v_fmac_f32_e32 v9, v128, v128
	v_fmac_f32_e32 v10, v126, v126
	v_add_f32_e32 v9, v9, v10
	v_add_f32_e32 v8, v9, v8
	v_mul_f32_e32 v9, v157, v157
	v_mul_f32_e32 v10, v155, v155
	v_fmac_f32_e32 v9, v156, v156
	v_fmac_f32_e32 v10, v154, v154
	v_add_f32_e32 v9, v9, v10
	v_mul_f32_e32 v10, v153, v153
	v_mul_f32_e32 v11, v149, v149
	v_fmac_f32_e32 v10, v152, v152
	v_fmac_f32_e32 v11, v148, v148
	v_add_f32_e32 v10, v10, v11
	v_add_f32_e32 v9, v10, v9
	v_add_f32_e32 v8, v8, v9
	v_mul_f32_e32 v9, v187, v187
	v_mul_f32_e32 v10, v159, v159
	v_fmac_f32_e32 v9, v186, v186
	v_fmac_f32_e32 v10, v158, v158
	v_add_f32_e32 v9, v9, v10
	v_mul_f32_e32 v10, v145, v145
	v_mul_f32_e32 v11, v143, v143
	v_fmac_f32_e32 v10, v144, v144
	v_fmac_f32_e32 v11, v142, v142
	v_add_f32_e32 v10, v10, v11
	v_add_f32_e32 v9, v10, v9
	v_mul_f32_e32 v10, v189, v189
	v_mul_f32_e32 v11, v165, v165
	v_fmac_f32_e32 v10, v188, v188
	v_fmac_f32_e32 v11, v164, v164
	v_add_f32_e32 v10, v10, v11
	v_mul_f32_e32 v11, v163, v163
	v_mul_f32_e32 v12, v161, v161
	v_fmac_f32_e32 v11, v162, v162
	v_fmac_f32_e32 v12, v160, v160
	v_add_f32_e32 v11, v11, v12
	v_add_f32_e32 v10, v11, v10
	v_add_f32_e32 v9, v9, v10
	v_lshlrev_b32_e32 v10, 2, v206
	v_lshlrev_b32_e32 v11, 4, v205
	s_or_b32 s68, s45, s47
	v_add3_u32 v10, s11, v10, v11
	ds_write2st64_b32 v10, v9, v8 offset1:1
	ds_write2st64_b32 v10, v7, v6 offset0:2 offset1:3
	ds_write2st64_b32 v10, v5, v4 offset0:4 offset1:5
	ds_write2st64_b32 v10, v3, v2 offset0:6 offset1:7
	v_add_u32_e32 v6, s11, v174
	s_ashr_i32 s69, s68, 31
	s_ashr_i32 s11, s10, 31
	s_lshl_b64 s[68:69], s[68:69], 18
	ds_read_b128 v[2:5], v6
	s_add_u32 s45, s58, s68
	s_addc_u32 s47, s59, s69
	s_lshl_b64 s[68:69], s[72:73], 2
	s_add_u32 s45, s45, s68
	s_addc_u32 s47, s47, s69
	s_lshl_b64 s[10:11], s[10:11], 2
	s_add_u32 s10, s45, s10
	s_waitcnt lgkmcnt(0)
	v_add_f32_e32 v2, v2, v3
	v_add_f32_e32 v3, v4, v5
	s_addc_u32 s11, s47, s11
	v_lshlrev_b32_e32 v7, 2, v204
	v_add_f32_e32 v2, v2, v3
	global_store_dword v7, v2, s[10:11]
	ds_read_b128 v[2:5], v6 offset:1024
	s_and_b64 vcc, exec, s[8:9]
	s_waitcnt lgkmcnt(0)
	v_add_f32_e32 v2, v2, v3
	v_add_f32_e32 v3, v4, v5
	v_add_f32_e32 v2, v2, v3
	global_store_dword v7, v2, s[10:11] offset:512
	s_mov_b64 s[10:11], -1
	s_cbranch_vccnz .LBB0_1769
	v_mov_b32_e32 v2, v0
	s_nop 0
	v_readfirstlane_b32 s8, v2
	s_and_b32 s10, s8, 0xc0
	s_lshl_b32 s8, s44, 8
	s_ashr_i32 s9, s8, 31
	s_lshl_b64 s[8:9], s[8:9], 2
	s_add_u32 s8, s12, s8
	s_addc_u32 s9, s13, s9
	s_lshl_b32 s10, s10, 2
	s_add_u32 s8, s8, s10
	v_lshlrev_b32_e32 v2, 1, v2
	s_addc_u32 s9, s9, 0
	v_and_b32_e32 v6, 0x60, v2
	global_load_dwordx4 v[10:13], v6, s[8:9] offset:16 nt
	global_load_dwordx4 v[14:17], v6, s[8:9] nt
	global_load_dwordx4 v[2:5], v6, s[8:9] offset:144 nt
	s_nop 0
	global_load_dwordx4 v[6:9], v6, s[8:9] offset:128 nt
	s_andn2_b64 vcc, exec, s[14:15]
	s_cbranch_vccnz .LBB0_1768
	s_barrier
	s_branch .LBB0_1768

.LBB0_2302:
	v_mov_b32_e32 v186, v0
	s_lshl_b32 s46, s46, 8
	v_readfirstlane_b32 s8, v186
	s_ashr_i32 s39, s8, 6
	s_ashr_i32 s8, s8, 2
	s_andn2_b32 s8, s8, 63
	s_mul_i32 s9, s39, 0xb00
	s_and_b32 s39, s39, 3
	s_add_i32 s70, s8, s46
	s_add_i32 s9, s9, 0
	s_lshl_b32 s41, s14, 8
	s_lshl_b32 s47, s39, 6
	s_ashr_i32 s71, s70, 31
	s_add_i32 s9, s9, 0x20000
	s_or_b32 s48, s47, s41
	s_lshl_b64 s[72:73], s[70:71], 11
	s_add_u32 s41, s37, s72
	s_addc_u32 s47, s54, s73
	s_ashr_i32 s49, s48, 31
	s_lshl_b64 s[50:51], s[48:49], 1
	v_and_b32_e32 v164, 63, v186
	s_add_u32 s74, s41, s50
	v_bfe_u32 v156, v186, 3, 3
	s_addc_u32 s75, s47, s51
	v_lshlrev_b32_e32 v138, 11, v156
	v_lshlrev_b32_e32 v165, 4, v164
	v_lshl_add_u64 v[146:147], s[74:75], 0, v[138:139]
	v_and_b32_e32 v144, 0x70, v165
	v_mov_b32_e32 v145, v139
	v_lshl_add_u64 v[148:149], v[146:147], 0, v[144:145]
	v_or_b32_e32 v146, 0x4000, v138
	v_mov_b32_e32 v147, v139
	v_lshl_add_u64 v[150:151], s[74:75], 0, v[146:147]
	v_lshl_add_u64 v[152:153], v[150:151], 0, v[144:145]
	global_load_dwordx4 v[148:151], v[148:149], off nt
	s_nop 0
	global_load_dwordx4 v[152:155], v[152:153], off nt
	s_or_b32 s74, s70, 16
	s_ashr_i32 s75, s74, 31
	s_lshl_b64 s[78:79], s[74:75], 11
	s_add_u32 s41, s37, s78
	s_addc_u32 s47, s54, s79
	v_and_b32_e32 v166, 15, v186
	s_add_u32 s76, s41, s50
	v_and_b32_e32 v157, 48, v186
	v_mul_u32_u24_e32 v156, 0x90, v156
	v_mul_u32_u24_e32 v158, 0x90, v166
	s_addc_u32 s77, s47, s51
	v_add3_u32 v168, s9, v156, v144
	v_add3_u32 v169, s9, v158, v157
	v_lshl_add_u64 v[156:157], s[76:77], 0, v[138:139]
	v_lshl_add_u64 v[158:159], s[76:77], 0, v[146:147]
	v_lshl_add_u64 v[156:157], v[156:157], 0, v[144:145]
	v_lshl_add_u64 v[158:159], v[158:159], 0, v[144:145]
	v_mov_b32_e32 v174, v139
	v_mov_b32_e32 v175, v139
	s_add_u32 s41, s55, s72
	s_addc_u32 s47, s56, s73
	s_add_u32 s72, s41, s50
	s_addc_u32 s73, s47, s51
	v_bfe_u32 v167, v186, 4, 2
	s_waitcnt vmcnt(0)
	ds_write_b128 v168, v[148:151]
	ds_write_b128 v168, v[152:155] offset:1152
	ds_read_b128 v[148:151], v169
	global_load_dwordx4 v[152:155], v[156:157], off nt
	s_nop 0
	global_load_dwordx4 v[156:159], v[158:159], off nt
	ds_read_b128 v[170:173], v169 offset:64
	s_waitcnt lgkmcnt(0)
	v_lshlrev_b32_e32 v176, 16, v148
	v_and_b32_e32 v177, 0xffff0000, v148
	v_lshlrev_b32_e32 v178, 16, v150
	v_and_b32_e32 v179, 0xffff0000, v150
	v_lshlrev_b32_e32 v180, 16, v151
	v_and_b32_e32 v181, 0xffff0000, v151
	v_pk_fma_f32 v[150:151], v[118:119], s[36:37], v[176:177] op_sel_hi:[1,0,1]
	v_pk_fma_f32 v[122:123], v[122:123], s[36:37], v[178:179] op_sel_hi:[1,0,1]
	v_med3_f32 v176, v150, s69, v163
	v_med3_f32 v178, v151, s69, v163
	v_cvt_pk_fp8_f32 v174, v176, v178
	v_lshlrev_b32_e32 v148, 16, v149
	v_and_b32_e32 v149, 0xffff0000, v149
	v_lshlrev_b32_e32 v182, 16, v170
	v_and_b32_e32 v183, 0xffff0000, v170
	v_lshlrev_b32_e32 v170, 16, v171
	v_and_b32_e32 v171, 0xffff0000, v171
	v_lshlrev_b32_e32 v184, 16, v172
	v_and_b32_e32 v185, 0xffff0000, v172
	v_pk_fma_f32 v[148:149], v[120:121], s[36:37], v[148:149] op_sel_hi:[1,0,1]
	v_pk_fma_f32 v[126:127], v[126:127], s[36:37], v[182:183] op_sel_hi:[1,0,1]
	v_med3_f32 v177, v122, s69, v163
	v_med3_f32 v179, v123, s69, v163
	v_lshlrev_b32_e32 v172, 16, v173
	v_and_b32_e32 v173, 0xffff0000, v173
	v_pk_fma_f32 v[124:125], v[124:125], s[36:37], v[180:181] op_sel_hi:[1,0,1]
	v_pk_fma_f32 v[118:119], v[128:129], s[36:37], v[170:171] op_sel_hi:[1,0,1]
	v_pk_fma_f32 v[128:129], v[114:115], s[36:37], v[184:185] op_sel_hi:[1,0,1]
	v_med3_f32 v180, v148, s69, v163
	v_med3_f32 v182, v149, s69, v163
	v_cvt_pk_fp8_f32 v175, v177, v179
	v_med3_f32 v177, v126, s69, v163
	v_med3_f32 v179, v127, s69, v163
	v_mov_b32_e32 v176, v139
	v_pk_fma_f32 v[120:121], v[116:117], s[36:37], v[172:173] op_sel_hi:[1,0,1]
	v_cvt_pk_bf16_f32 v114, v150, v151
	v_cvt_pk_bf16_f32 v115, v148, v149
	v_cvt_pk_bf16_f32 v116, v122, v123
	v_cvt_pk_bf16_f32 v117, v124, v125
	v_med3_f32 v178, v128, s69, v163
	v_cvt_pk_fp8_f32 v174, v180, v182 op_sel:[0,0,1]
	v_med3_f32 v180, v129, s69, v163
	v_cvt_pk_fp8_f32 v176, v177, v179
	v_mov_b32_e32 v177, v139
	v_cvt_pk_bf16_f32 v170, v126, v127
	v_cvt_pk_bf16_f32 v171, v118, v119
	v_cvt_pk_bf16_f32 v172, v128, v129
	v_cvt_pk_bf16_f32 v173, v120, v121
	v_cvt_pk_fp8_f32 v177, v178, v180
	ds_write_b128 v169, v[114:117]
	ds_write_b128 v169, v[170:173] offset:64
	ds_read_b128 v[114:117], v168
	ds_read_b128 v[170:173], v168 offset:1152
	v_med3_f32 v181, v124, s69, v163
	v_med3_f32 v183, v125, s69, v163
	v_cvt_pk_fp8_f32 v175, v181, v183 op_sel:[0,0,1]
	v_med3_f32 v181, v118, s69, v163
	v_med3_f32 v182, v120, s69, v163
	v_med3_f32 v178, v119, s69, v163
	v_med3_f32 v179, v121, s69, v163
	v_cvt_pk_fp8_f32 v176, v181, v178 op_sel:[0,0,1]
	v_cvt_pk_fp8_f32 v177, v182, v179 op_sel:[0,0,1]
	v_lshl_add_u64 v[178:179], s[72:73], 0, v[138:139]
	v_lshl_add_u64 v[178:179], v[178:179], 0, v[144:145]
	s_waitcnt lgkmcnt(1)
	global_store_dwordx4 v[178:179], v[114:117], off
	s_nop 1
	v_lshl_add_u64 v[114:115], s[72:73], 0, v[146:147]
	v_lshl_add_u64 v[114:115], v[114:115], 0, v[144:145]
	s_lshl_b64 s[72:73], s[70:71], 10
	s_waitcnt lgkmcnt(0)
	global_store_dwordx4 v[114:115], v[170:173], off
	s_add_u32 s41, s60, s72
	v_mul_u32_u24_e32 v114, 0x50, v166
	v_lshlrev_b32_e32 v115, 3, v167
	s_addc_u32 s47, s61, s73
	v_add3_u32 v170, s9, v114, v115
	v_bfe_u32 v115, v186, 2, 4
	s_add_u32 s72, s41, s48
	v_mul_u32_u24_e32 v116, 0x50, v115
	v_and_b32_e32 v114, 48, v165
	s_addc_u32 s73, s47, s49
	v_add3_u32 v171, s9, v116, v114
	v_lshlrev_b32_e32 v116, 10, v115
	v_mov_b32_e32 v117, v139
	ds_write2_b64 v170, v[174:175], v[176:177] offset1:4
	v_lshl_add_u64 v[176:177], s[72:73], 0, v[116:117]
	s_or_b32 s72, s70, 32
	s_ashr_i32 s73, s72, 31
	ds_read_b128 v[172:175], v171
	s_lshl_b64 s[76:77], s[72:73], 11
	s_add_u32 s41, s37, s76
	s_addc_u32 s47, s54, s77
	v_mov_b32_e32 v115, v139
	s_add_u32 s80, s41, s50
	v_lshl_add_u64 v[176:177], v[176:177], 0, v[114:115]
	s_addc_u32 s81, s47, s51
	s_waitcnt lgkmcnt(0)
	global_store_dwordx4 v[176:177], v[172:175], off
	s_waitcnt vmcnt(4)
	ds_write_b128 v168, v[152:155]
	s_waitcnt vmcnt(3)
	ds_write_b128 v168, v[156:159] offset:1152
	v_lshl_add_u64 v[172:173], s[80:81], 0, v[138:139]
	v_lshl_add_u64 v[174:175], s[80:81], 0, v[146:147]
	v_lshl_add_u64 v[172:173], v[172:173], 0, v[144:145]
	v_lshl_add_u64 v[174:175], v[174:175], 0, v[144:145]
	ds_read_b128 v[152:155], v169
	global_load_dwordx4 v[156:159], v[172:173], off nt
	s_nop 0
	global_load_dwordx4 v[172:175], v[174:175], off nt
	ds_read_b128 v[176:179], v169 offset:64
	s_add_u32 s41, s55, s78
	s_addc_u32 s47, s56, s79
	s_waitcnt lgkmcnt(1)
	v_lshlrev_b32_e32 v180, 16, v152
	v_and_b32_e32 v181, 0xffff0000, v152
	v_lshlrev_b32_e32 v182, 16, v154
	v_and_b32_e32 v183, 0xffff0000, v154
	v_pk_fma_f32 v[110:111], v[110:111], s[36:37], v[180:181] op_sel_hi:[1,0,1]
	v_pk_fma_f32 v[106:107], v[106:107], s[36:37], v[182:183] op_sel_hi:[1,0,1]
	v_med3_f32 v181, v110, s69, v163
	v_med3_f32 v183, v111, s69, v163
	v_mov_b32_e32 v180, v139
	v_med3_f32 v182, v106, s69, v163
	v_med3_f32 v184, v107, s69, v163
	v_cvt_pk_fp8_f32 v180, v181, v183
	v_mov_b32_e32 v181, v139
	v_cvt_pk_fp8_f32 v181, v182, v184
	v_lshlrev_b32_e32 v152, 16, v153
	v_and_b32_e32 v153, 0xffff0000, v153
	v_lshlrev_b32_e32 v154, 16, v155
	v_and_b32_e32 v155, 0xffff0000, v155
	v_pk_fma_f32 v[112:113], v[112:113], s[36:37], v[152:153] op_sel_hi:[1,0,1]
	v_pk_fma_f32 v[108:109], v[108:109], s[36:37], v[154:155] op_sel_hi:[1,0,1]
	v_med3_f32 v185, v112, s69, v163
	v_med3_f32 v186, v108, s69, v163
	v_med3_f32 v182, v113, s69, v163
	v_med3_f32 v183, v109, s69, v163
	v_cvt_pk_fp8_f32 v180, v185, v182 op_sel:[0,0,1]
	v_cvt_pk_fp8_f32 v181, v186, v183 op_sel:[0,0,1]
	s_waitcnt lgkmcnt(0)
	v_lshlrev_b32_e32 v182, 16, v176
	v_and_b32_e32 v183, 0xffff0000, v176
	v_lshlrev_b32_e32 v184, 16, v178
	v_and_b32_e32 v185, 0xffff0000, v178
	v_pk_fma_f32 v[102:103], v[102:103], s[36:37], v[182:183] op_sel_hi:[1,0,1]
	v_pk_fma_f32 v[98:99], v[98:99], s[36:37], v[184:185] op_sel_hi:[1,0,1]
	v_med3_f32 v183, v102, s69, v163
	v_med3_f32 v185, v103, s69, v163
	v_mov_b32_e32 v182, v139
	v_cvt_pk_bf16_f32 v152, v110, v111
	v_cvt_pk_bf16_f32 v153, v112, v113
	v_cvt_pk_bf16_f32 v154, v106, v107
	v_cvt_pk_bf16_f32 v155, v108, v109
	v_lshlrev_b32_e32 v176, 16, v177
	v_and_b32_e32 v177, 0xffff0000, v177
	v_lshlrev_b32_e32 v178, 16, v179
	v_and_b32_e32 v179, 0xffff0000, v179
	v_med3_f32 v184, v98, s69, v163
	v_med3_f32 v186, v99, s69, v163
	v_cvt_pk_fp8_f32 v182, v183, v185
	v_mov_b32_e32 v183, v139
	v_pk_fma_f32 v[104:105], v[104:105], s[36:37], v[176:177] op_sel_hi:[1,0,1]
	v_pk_fma_f32 v[100:101], v[100:101], s[36:37], v[178:179] op_sel_hi:[1,0,1]
	v_cvt_pk_bf16_f32 v176, v102, v103
	v_cvt_pk_bf16_f32 v177, v104, v105
	v_cvt_pk_bf16_f32 v178, v98, v99
	v_cvt_pk_fp8_f32 v183, v184, v186
	v_cvt_pk_bf16_f32 v179, v100, v101
	ds_write_b128 v169, v[152:155]
	ds_write_b128 v169, v[176:179] offset:64
	ds_read_b128 v[152:155], v168
	ds_read_b128 v[176:179], v168 offset:1152
	s_add_u32 s78, s41, s50
	v_med3_f32 v187, v104, s69, v163
	v_med3_f32 v188, v100, s69, v163
	v_med3_f32 v184, v105, s69, v163
	v_med3_f32 v185, v101, s69, v163
	s_addc_u32 s79, s47, s51
	s_lshl_b64 s[74:75], s[74:75], 10
	v_cvt_pk_fp8_f32 v182, v187, v184 op_sel:[0,0,1]
	v_cvt_pk_fp8_f32 v183, v188, v185 op_sel:[0,0,1]
	v_lshl_add_u64 v[184:185], s[78:79], 0, v[138:139]
	s_add_u32 s41, s60, s74
	v_lshl_add_u64 v[184:185], v[184:185], 0, v[144:145]
	s_addc_u32 s47, s61, s75
	s_waitcnt lgkmcnt(1)
	global_store_dwordx4 v[184:185], v[152:155], off
	s_add_u32 s74, s41, s48
	s_addc_u32 s75, s47, s49
	v_lshl_add_u64 v[152:153], s[78:79], 0, v[146:147]
	v_lshl_add_u64 v[152:153], v[152:153], 0, v[144:145]
	s_waitcnt lgkmcnt(0)
	global_store_dwordx4 v[152:153], v[176:179], off
	ds_write2_b64 v170, v[180:181], v[182:183] offset1:4
	ds_read_b128 v[152:155], v171
	v_lshl_add_u64 v[176:177], s[74:75], 0, v[116:117]
	s_or_b32 s74, s70, 48
	s_ashr_i32 s75, s74, 31
	s_lshl_b64 s[78:79], s[74:75], 11
	s_add_u32 s41, s37, s78
	s_addc_u32 s47, s54, s79
	s_add_u32 s80, s41, s50
	v_lshl_add_u64 v[176:177], v[176:177], 0, v[114:115]
	s_addc_u32 s81, s47, s51
	s_waitcnt lgkmcnt(0)
	global_store_dwordx4 v[176:177], v[152:155], off
	v_lshl_add_u64 v[178:179], s[80:81], 0, v[146:147]
	s_waitcnt vmcnt(4)
	ds_write_b128 v168, v[156:159]
	s_waitcnt vmcnt(3)
	ds_write_b128 v168, v[172:175] offset:1152
	v_lshl_add_u64 v[152:153], s[80:81], 0, v[138:139]
	v_lshl_add_u64 v[176:177], v[152:153], 0, v[144:145]
	v_lshl_add_u64 v[172:173], v[178:179], 0, v[144:145]
	ds_read_b128 v[152:155], v169
	global_load_dwordx4 v[156:159], v[176:177], off nt
	s_nop 0
	global_load_dwordx4 v[172:175], v[172:173], off nt
	ds_read_b128 v[176:179], v169 offset:64
	s_add_u32 s41, s55, s76
	s_addc_u32 s47, s56, s77
	s_waitcnt lgkmcnt(1)
	v_lshlrev_b32_e32 v180, 16, v152
	v_and_b32_e32 v181, 0xffff0000, v152
	v_lshlrev_b32_e32 v182, 16, v154
	v_and_b32_e32 v183, 0xffff0000, v154
	v_pk_fma_f32 v[94:95], v[94:95], s[36:37], v[180:181] op_sel_hi:[1,0,1]
	v_pk_fma_f32 v[90:91], v[90:91], s[36:37], v[182:183] op_sel_hi:[1,0,1]
	v_med3_f32 v181, v94, s69, v163
	v_med3_f32 v183, v95, s69, v163
	v_mov_b32_e32 v180, v139
	v_med3_f32 v182, v90, s69, v163
	v_med3_f32 v184, v91, s69, v163
	v_cvt_pk_fp8_f32 v180, v181, v183
	v_mov_b32_e32 v181, v139
	v_cvt_pk_fp8_f32 v181, v182, v184
	v_lshlrev_b32_e32 v152, 16, v153
	v_and_b32_e32 v153, 0xffff0000, v153
	v_lshlrev_b32_e32 v154, 16, v155
	v_and_b32_e32 v155, 0xffff0000, v155
	v_pk_fma_f32 v[96:97], v[96:97], s[36:37], v[152:153] op_sel_hi:[1,0,1]
	v_pk_fma_f32 v[92:93], v[92:93], s[36:37], v[154:155] op_sel_hi:[1,0,1]
	v_med3_f32 v185, v96, s69, v163
	v_med3_f32 v186, v92, s69, v163
	v_med3_f32 v182, v97, s69, v163
	v_med3_f32 v183, v93, s69, v163
	v_cvt_pk_fp8_f32 v180, v185, v182 op_sel:[0,0,1]
	v_cvt_pk_fp8_f32 v181, v186, v183 op_sel:[0,0,1]
	s_waitcnt lgkmcnt(0)
	v_lshlrev_b32_e32 v182, 16, v176
	v_and_b32_e32 v183, 0xffff0000, v176
	v_lshlrev_b32_e32 v184, 16, v178
	v_and_b32_e32 v185, 0xffff0000, v178
	v_pk_fma_f32 v[86:87], v[86:87], s[36:37], v[182:183] op_sel_hi:[1,0,1]
	v_pk_fma_f32 v[82:83], v[82:83], s[36:37], v[184:185] op_sel_hi:[1,0,1]
	v_med3_f32 v183, v86, s69, v163
	v_med3_f32 v185, v87, s69, v163
	v_mov_b32_e32 v182, v139
	v_cvt_pk_bf16_f32 v152, v94, v95
	v_cvt_pk_bf16_f32 v153, v96, v97
	v_cvt_pk_bf16_f32 v154, v90, v91
	v_cvt_pk_bf16_f32 v155, v92, v93
	v_lshlrev_b32_e32 v176, 16, v177
	v_and_b32_e32 v177, 0xffff0000, v177
	v_lshlrev_b32_e32 v178, 16, v179
	v_and_b32_e32 v179, 0xffff0000, v179
	v_med3_f32 v184, v82, s69, v163
	v_med3_f32 v186, v83, s69, v163
	v_cvt_pk_fp8_f32 v182, v183, v185
	v_mov_b32_e32 v183, v139
	v_pk_fma_f32 v[88:89], v[88:89], s[36:37], v[176:177] op_sel_hi:[1,0,1]
	v_pk_fma_f32 v[84:85], v[84:85], s[36:37], v[178:179] op_sel_hi:[1,0,1]
	v_cvt_pk_bf16_f32 v176, v86, v87
	v_cvt_pk_bf16_f32 v177, v88, v89
	v_cvt_pk_bf16_f32 v178, v82, v83
	v_cvt_pk_fp8_f32 v183, v184, v186
	v_cvt_pk_bf16_f32 v179, v84, v85
	ds_write_b128 v169, v[152:155]
	ds_write_b128 v169, v[176:179] offset:64
	ds_read_b128 v[152:155], v168
	ds_read_b128 v[176:179], v168 offset:1152
	s_add_u32 s76, s41, s50
	v_med3_f32 v187, v88, s69, v163
	v_med3_f32 v188, v84, s69, v163
	v_med3_f32 v184, v89, s69, v163
	v_med3_f32 v185, v85, s69, v163
	s_addc_u32 s77, s47, s51
	s_lshl_b64 s[72:73], s[72:73], 10
	v_cvt_pk_fp8_f32 v182, v187, v184 op_sel:[0,0,1]
	v_cvt_pk_fp8_f32 v183, v188, v185 op_sel:[0,0,1]
	v_lshl_add_u64 v[184:185], s[76:77], 0, v[138:139]
	s_add_u32 s41, s60, s72
	v_lshl_add_u64 v[184:185], v[184:185], 0, v[144:145]
	s_addc_u32 s47, s61, s73
	s_waitcnt lgkmcnt(1)
	global_store_dwordx4 v[184:185], v[152:155], off
	s_add_u32 s72, s41, s48
	s_addc_u32 s73, s47, s49
	v_lshl_add_u64 v[152:153], s[76:77], 0, v[146:147]
	v_lshl_add_u64 v[152:153], v[152:153], 0, v[144:145]
	s_waitcnt lgkmcnt(0)
	global_store_dwordx4 v[152:153], v[176:179], off
	ds_write2_b64 v170, v[180:181], v[182:183] offset1:4
	ds_read_b128 v[152:155], v171
	v_lshl_add_u64 v[176:177], s[72:73], 0, v[116:117]
	s_add_i32 s72, s70, 0x80
	s_ashr_i32 s73, s72, 31
	s_lshl_b64 s[76:77], s[72:73], 11
	s_add_u32 s41, s37, s76
	s_addc_u32 s47, s54, s77
	s_add_u32 s80, s41, s50
	v_lshl_add_u64 v[176:177], v[176:177], 0, v[114:115]
	s_addc_u32 s81, s47, s51
	s_waitcnt lgkmcnt(0)
	global_store_dwordx4 v[176:177], v[152:155], off
	v_lshl_add_u64 v[178:179], s[80:81], 0, v[146:147]
	s_waitcnt vmcnt(4)
	ds_write_b128 v168, v[156:159]
	s_waitcnt vmcnt(3)
	ds_write_b128 v168, v[172:175] offset:1152
	v_lshl_add_u64 v[152:153], s[80:81], 0, v[138:139]
	v_lshl_add_u64 v[176:177], v[152:153], 0, v[144:145]
	v_lshl_add_u64 v[172:173], v[178:179], 0, v[144:145]
	ds_read_b128 v[152:155], v169
	global_load_dwordx4 v[156:159], v[176:177], off nt
	s_nop 0
	global_load_dwordx4 v[172:175], v[172:173], off nt
	ds_read_b128 v[176:179], v169 offset:64
	s_add_u32 s41, s55, s78
	s_addc_u32 s47, s56, s79
	s_waitcnt lgkmcnt(1)
	v_lshlrev_b32_e32 v180, 16, v152
	v_and_b32_e32 v181, 0xffff0000, v152
	v_lshlrev_b32_e32 v182, 16, v154
	v_and_b32_e32 v183, 0xffff0000, v154
	v_pk_fma_f32 v[78:79], v[78:79], s[36:37], v[180:181] op_sel_hi:[1,0,1]
	v_pk_fma_f32 v[74:75], v[74:75], s[36:37], v[182:183] op_sel_hi:[1,0,1]
	v_med3_f32 v181, v78, s69, v163
	v_med3_f32 v183, v79, s69, v163
	v_mov_b32_e32 v180, v139
	v_med3_f32 v182, v74, s69, v163
	v_med3_f32 v184, v75, s69, v163
	v_cvt_pk_fp8_f32 v180, v181, v183
	v_mov_b32_e32 v181, v139
	v_cvt_pk_fp8_f32 v181, v182, v184
	v_lshlrev_b32_e32 v152, 16, v153
	v_and_b32_e32 v153, 0xffff0000, v153
	v_lshlrev_b32_e32 v154, 16, v155
	v_and_b32_e32 v155, 0xffff0000, v155
	v_pk_fma_f32 v[80:81], v[80:81], s[36:37], v[152:153] op_sel_hi:[1,0,1]
	v_pk_fma_f32 v[76:77], v[76:77], s[36:37], v[154:155] op_sel_hi:[1,0,1]
	v_med3_f32 v185, v80, s69, v163
	v_med3_f32 v186, v76, s69, v163
	v_med3_f32 v182, v81, s69, v163
	v_med3_f32 v183, v77, s69, v163
	v_cvt_pk_fp8_f32 v180, v185, v182 op_sel:[0,0,1]
	v_cvt_pk_fp8_f32 v181, v186, v183 op_sel:[0,0,1]
	s_waitcnt lgkmcnt(0)
	v_lshlrev_b32_e32 v182, 16, v176
	v_and_b32_e32 v183, 0xffff0000, v176
	v_lshlrev_b32_e32 v184, 16, v178
	v_and_b32_e32 v185, 0xffff0000, v178
	v_pk_fma_f32 v[70:71], v[70:71], s[36:37], v[182:183] op_sel_hi:[1,0,1]
	v_pk_fma_f32 v[66:67], v[66:67], s[36:37], v[184:185] op_sel_hi:[1,0,1]
	v_med3_f32 v183, v70, s69, v163
	v_med3_f32 v185, v71, s69, v163
	v_mov_b32_e32 v182, v139
	v_cvt_pk_bf16_f32 v152, v78, v79
	v_cvt_pk_bf16_f32 v153, v80, v81
	v_cvt_pk_bf16_f32 v154, v74, v75
	v_cvt_pk_bf16_f32 v155, v76, v77
	v_lshlrev_b32_e32 v176, 16, v177
	v_and_b32_e32 v177, 0xffff0000, v177
	v_lshlrev_b32_e32 v178, 16, v179
	v_and_b32_e32 v179, 0xffff0000, v179
	v_med3_f32 v184, v66, s69, v163
	v_med3_f32 v186, v67, s69, v163
	v_cvt_pk_fp8_f32 v182, v183, v185
	v_mov_b32_e32 v183, v139
	v_pk_fma_f32 v[72:73], v[72:73], s[36:37], v[176:177] op_sel_hi:[1,0,1]
	v_pk_fma_f32 v[68:69], v[68:69], s[36:37], v[178:179] op_sel_hi:[1,0,1]
	v_cvt_pk_bf16_f32 v176, v70, v71
	v_cvt_pk_bf16_f32 v177, v72, v73
	v_cvt_pk_bf16_f32 v178, v66, v67
	v_cvt_pk_fp8_f32 v183, v184, v186
	v_cvt_pk_bf16_f32 v179, v68, v69
	ds_write_b128 v169, v[152:155]
	ds_write_b128 v169, v[176:179] offset:64
	ds_read_b128 v[152:155], v168
	ds_read_b128 v[176:179], v168 offset:1152
	s_add_u32 s78, s41, s50
	v_med3_f32 v187, v72, s69, v163
	v_med3_f32 v188, v68, s69, v163
	v_med3_f32 v184, v73, s69, v163
	v_med3_f32 v185, v69, s69, v163
	s_addc_u32 s79, s47, s51
	s_lshl_b64 s[74:75], s[74:75], 10
	v_cvt_pk_fp8_f32 v182, v187, v184 op_sel:[0,0,1]
	v_cvt_pk_fp8_f32 v183, v188, v185 op_sel:[0,0,1]
	v_lshl_add_u64 v[184:185], s[78:79], 0, v[138:139]
	s_add_u32 s41, s60, s74
	v_lshl_add_u64 v[184:185], v[184:185], 0, v[144:145]
	s_addc_u32 s47, s61, s75
	s_waitcnt lgkmcnt(1)
	global_store_dwordx4 v[184:185], v[152:155], off
	s_add_u32 s74, s41, s48
	s_addc_u32 s75, s47, s49
	v_lshl_add_u64 v[152:153], s[78:79], 0, v[146:147]
	v_lshl_add_u64 v[152:153], v[152:153], 0, v[144:145]
	s_waitcnt lgkmcnt(0)
	global_store_dwordx4 v[152:153], v[176:179], off
	ds_write2_b64 v170, v[180:181], v[182:183] offset1:4
	ds_read_b128 v[152:155], v171
	v_lshl_add_u64 v[176:177], s[74:75], 0, v[116:117]
	s_add_i32 s74, s70, 0x90
	s_ashr_i32 s75, s74, 31
	s_lshl_b64 s[78:79], s[74:75], 11
	s_add_u32 s41, s37, s78
	s_addc_u32 s47, s54, s79
	s_add_u32 s80, s41, s50
	v_lshl_add_u64 v[176:177], v[176:177], 0, v[114:115]
	s_addc_u32 s81, s47, s51
	s_waitcnt lgkmcnt(0)
	global_store_dwordx4 v[176:177], v[152:155], off
	v_lshl_add_u64 v[178:179], s[80:81], 0, v[146:147]
	s_waitcnt vmcnt(4)
	ds_write_b128 v168, v[156:159]
	s_waitcnt vmcnt(3)
	ds_write_b128 v168, v[172:175] offset:1152
	v_lshl_add_u64 v[152:153], s[80:81], 0, v[138:139]
	v_lshl_add_u64 v[176:177], v[152:153], 0, v[144:145]
	v_lshl_add_u64 v[172:173], v[178:179], 0, v[144:145]
	ds_read_b128 v[152:155], v169
	global_load_dwordx4 v[156:159], v[176:177], off nt
	s_nop 0
	global_load_dwordx4 v[172:175], v[172:173], off nt
	ds_read_b128 v[176:179], v169 offset:64
	s_add_u32 s41, s55, s76
	s_addc_u32 s47, s56, s77
	s_waitcnt lgkmcnt(1)
	v_lshlrev_b32_e32 v180, 16, v152
	v_and_b32_e32 v181, 0xffff0000, v152
	v_lshlrev_b32_e32 v182, 16, v154
	v_and_b32_e32 v183, 0xffff0000, v154
	v_pk_fma_f32 v[62:63], v[62:63], s[36:37], v[180:181] op_sel_hi:[1,0,1]
	v_pk_fma_f32 v[58:59], v[58:59], s[36:37], v[182:183] op_sel_hi:[1,0,1]
	v_med3_f32 v181, v62, s69, v163
	v_med3_f32 v183, v63, s69, v163
	v_mov_b32_e32 v180, v139
	v_med3_f32 v182, v58, s69, v163
	v_med3_f32 v184, v59, s69, v163
	v_cvt_pk_fp8_f32 v180, v181, v183
	v_mov_b32_e32 v181, v139
	v_cvt_pk_fp8_f32 v181, v182, v184
	v_lshlrev_b32_e32 v152, 16, v153
	v_and_b32_e32 v153, 0xffff0000, v153
	v_lshlrev_b32_e32 v154, 16, v155
	v_and_b32_e32 v155, 0xffff0000, v155
	v_pk_fma_f32 v[64:65], v[64:65], s[36:37], v[152:153] op_sel_hi:[1,0,1]
	v_pk_fma_f32 v[60:61], v[60:61], s[36:37], v[154:155] op_sel_hi:[1,0,1]
	v_med3_f32 v185, v64, s69, v163
	v_med3_f32 v186, v60, s69, v163
	v_med3_f32 v182, v65, s69, v163
	v_med3_f32 v183, v61, s69, v163
	v_cvt_pk_fp8_f32 v180, v185, v182 op_sel:[0,0,1]
	v_cvt_pk_fp8_f32 v181, v186, v183 op_sel:[0,0,1]
	s_waitcnt lgkmcnt(0)
	v_lshlrev_b32_e32 v182, 16, v176
	v_and_b32_e32 v183, 0xffff0000, v176
	v_lshlrev_b32_e32 v184, 16, v178
	v_and_b32_e32 v185, 0xffff0000, v178
	v_pk_fma_f32 v[54:55], v[54:55], s[36:37], v[182:183] op_sel_hi:[1,0,1]
	v_pk_fma_f32 v[50:51], v[50:51], s[36:37], v[184:185] op_sel_hi:[1,0,1]
	v_med3_f32 v183, v54, s69, v163
	v_med3_f32 v185, v55, s69, v163
	v_mov_b32_e32 v182, v139
	v_med3_f32 v184, v50, s69, v163
	v_med3_f32 v186, v51, s69, v163
	v_cvt_pk_fp8_f32 v182, v183, v185
	v_mov_b32_e32 v183, v139
	v_cvt_pk_bf16_f32 v152, v62, v63
	v_cvt_pk_bf16_f32 v153, v64, v65
	v_cvt_pk_bf16_f32 v154, v58, v59
	v_cvt_pk_bf16_f32 v155, v60, v61
	v_lshlrev_b32_e32 v176, 16, v177
	v_and_b32_e32 v177, 0xffff0000, v177
	v_lshlrev_b32_e32 v178, 16, v179
	v_and_b32_e32 v179, 0xffff0000, v179
	v_cvt_pk_fp8_f32 v183, v184, v186
	v_pk_fma_f32 v[56:57], v[56:57], s[36:37], v[176:177] op_sel_hi:[1,0,1]
	v_pk_fma_f32 v[52:53], v[52:53], s[36:37], v[178:179] op_sel_hi:[1,0,1]
	v_cvt_pk_bf16_f32 v176, v54, v55
	v_cvt_pk_bf16_f32 v177, v56, v57
	v_cvt_pk_bf16_f32 v178, v50, v51
	s_add_u32 s76, s41, s50
	v_cvt_pk_bf16_f32 v179, v52, v53
	ds_write_b128 v169, v[152:155]
	ds_write_b128 v169, v[176:179] offset:64
	ds_read_b128 v[152:155], v168
	ds_read_b128 v[176:179], v168 offset:1152
	v_med3_f32 v187, v56, s69, v163
	v_med3_f32 v188, v52, s69, v163
	v_med3_f32 v184, v57, s69, v163
	v_med3_f32 v185, v53, s69, v163
	s_addc_u32 s77, s47, s51
	s_lshl_b64 s[72:73], s[72:73], 10
	v_cvt_pk_fp8_f32 v182, v187, v184 op_sel:[0,0,1]
	v_cvt_pk_fp8_f32 v183, v188, v185 op_sel:[0,0,1]
	s_add_u32 s41, s60, s72
	v_lshl_add_u64 v[184:185], s[76:77], 0, v[138:139]
	s_addc_u32 s47, s61, s73
	v_lshl_add_u64 v[184:185], v[184:185], 0, v[144:145]
	s_add_u32 s72, s41, s48
	s_waitcnt lgkmcnt(1)
	global_store_dwordx4 v[184:185], v[152:155], off
	s_addc_u32 s73, s47, s49
	ds_write2_b64 v170, v[180:181], v[182:183] offset1:4
	v_lshl_add_u64 v[152:153], s[76:77], 0, v[146:147]
	s_add_i32 s76, s70, 0xa0
	v_lshl_add_u64 v[152:153], v[152:153], 0, v[144:145]
	s_ashr_i32 s77, s76, 31
	s_waitcnt lgkmcnt(1)
	global_store_dwordx4 v[152:153], v[176:179], off
	ds_read_b128 v[152:155], v171
	s_lshl_b64 s[80:81], s[76:77], 11
	s_add_u32 s41, s37, s80
	s_addc_u32 s47, s54, s81
	v_lshl_add_u64 v[176:177], s[72:73], 0, v[116:117]
	s_add_u32 s72, s41, s50
	v_lshl_add_u64 v[176:177], v[176:177], 0, v[114:115]
	s_addc_u32 s73, s47, s51
	s_waitcnt lgkmcnt(0)
	global_store_dwordx4 v[176:177], v[152:155], off
	v_lshl_add_u64 v[178:179], s[72:73], 0, v[146:147]
	s_waitcnt vmcnt(4)
	ds_write_b128 v168, v[156:159]
	s_waitcnt vmcnt(3)
	ds_write_b128 v168, v[172:175] offset:1152
	v_lshl_add_u64 v[152:153], s[72:73], 0, v[138:139]
	v_lshl_add_u64 v[176:177], v[152:153], 0, v[144:145]
	ds_read_b128 v[152:155], v169
	v_lshl_add_u64 v[156:157], v[178:179], 0, v[144:145]
	global_load_dwordx4 v[172:175], v[176:177], off nt
	s_nop 0
	global_load_dwordx4 v[176:179], v[156:157], off nt
	ds_read_b128 v[156:159], v169 offset:64
	v_mov_b32_e32 v184, v139
	s_waitcnt lgkmcnt(1)
	v_lshlrev_b32_e32 v180, 16, v152
	v_and_b32_e32 v181, 0xffff0000, v152
	v_lshlrev_b32_e32 v182, 16, v154
	v_and_b32_e32 v183, 0xffff0000, v154
	v_lshlrev_b32_e32 v152, 16, v153
	v_and_b32_e32 v153, 0xffff0000, v153
	v_lshlrev_b32_e32 v154, 16, v155
	v_and_b32_e32 v155, 0xffff0000, v155
	v_pk_fma_f32 v[46:47], v[46:47], s[36:37], v[180:181] op_sel_hi:[1,0,1]
	v_pk_fma_f32 v[42:43], v[42:43], s[36:37], v[182:183] op_sel_hi:[1,0,1]
	v_pk_fma_f32 v[48:49], v[48:49], s[36:37], v[152:153] op_sel_hi:[1,0,1]
	v_pk_fma_f32 v[44:45], v[44:45], s[36:37], v[154:155] op_sel_hi:[1,0,1]
	v_med3_f32 v152, v46, s69, v163
	v_med3_f32 v153, v42, s69, v163
	v_med3_f32 v154, v47, s69, v163
	v_med3_f32 v155, v43, s69, v163
	v_mov_b32_e32 v185, v139
	v_cvt_pk_fp8_f32 v184, v152, v154
	v_cvt_pk_fp8_f32 v185, v153, v155
	v_med3_f32 v186, v48, s69, v163
	v_med3_f32 v187, v44, s69, v163
	v_med3_f32 v152, v49, s69, v163
	v_med3_f32 v153, v45, s69, v163
	v_cvt_pk_fp8_f32 v184, v186, v152 op_sel:[0,0,1]
	v_cvt_pk_fp8_f32 v185, v187, v153 op_sel:[0,0,1]
	s_waitcnt lgkmcnt(0)
	v_lshlrev_b32_e32 v154, 16, v156
	v_and_b32_e32 v155, 0xffff0000, v156
	v_lshlrev_b32_e32 v186, 16, v158
	v_and_b32_e32 v187, 0xffff0000, v158
	v_lshlrev_b32_e32 v158, 16, v159
	v_and_b32_e32 v159, 0xffff0000, v159
	v_lshlrev_b32_e32 v152, 16, v157
	v_and_b32_e32 v153, 0xffff0000, v157
	v_pk_fma_f32 v[156:157], v[38:39], s[36:37], v[154:155] op_sel_hi:[1,0,1]
	v_pk_fma_f32 v[154:155], v[36:37], s[36:37], v[158:159] op_sel_hi:[1,0,1]
	v_pk_fma_f32 v[158:159], v[34:35], s[36:37], v[186:187] op_sel_hi:[1,0,1]
	v_pk_fma_f32 v[152:153], v[40:41], s[36:37], v[152:153] op_sel_hi:[1,0,1]
	v_med3_f32 v38, v156, s69, v163
	v_med3_f32 v39, v158, s69, v163
	v_med3_f32 v40, v157, s69, v163
	v_med3_f32 v41, v159, s69, v163
	v_mov_b32_e32 v186, v139
	v_mov_b32_e32 v187, v139
	v_cvt_pk_bf16_f32 v180, v46, v47
	v_cvt_pk_bf16_f32 v181, v48, v49
	v_cvt_pk_bf16_f32 v182, v42, v43
	v_cvt_pk_bf16_f32 v183, v44, v45
	v_cvt_pk_fp8_f32 v186, v38, v40
	v_cvt_pk_fp8_f32 v187, v39, v41
	v_cvt_pk_bf16_f32 v34, v156, v157
	v_cvt_pk_bf16_f32 v35, v152, v153
	v_cvt_pk_bf16_f32 v36, v158, v159
	v_cvt_pk_bf16_f32 v37, v154, v155
	s_add_u32 s41, s55, s78
	ds_write_b128 v169, v[180:183]
	ds_write_b128 v169, v[34:37] offset:64
	s_addc_u32 s47, s56, s79
	ds_read_b128 v[34:37], v168
	v_med3_f32 v188, v152, s69, v163
	v_med3_f32 v189, v154, s69, v163
	v_med3_f32 v38, v153, s69, v163
	v_med3_f32 v39, v155, s69, v163
	s_add_u32 s72, s41, s50
	v_cvt_pk_fp8_f32 v186, v188, v38 op_sel:[0,0,1]
	v_cvt_pk_fp8_f32 v187, v189, v39 op_sel:[0,0,1]
	s_addc_u32 s73, s47, s51
	ds_read_b128 v[38:41], v168 offset:1152
	v_lshl_add_u64 v[180:181], s[72:73], 0, v[138:139]
	v_lshl_add_u64 v[180:181], v[180:181], 0, v[144:145]
	s_waitcnt lgkmcnt(1)
	global_store_dwordx4 v[180:181], v[34:37], off
	ds_write2_b64 v170, v[184:185], v[186:187] offset1:4
	v_mov_b32_e32 v187, v139
	v_lshl_add_u64 v[34:35], s[72:73], 0, v[146:147]
	s_lshl_b64 s[72:73], s[74:75], 10
	v_lshl_add_u64 v[34:35], v[34:35], 0, v[144:145]
	s_add_u32 s41, s60, s72
	s_waitcnt lgkmcnt(1)
	global_store_dwordx4 v[34:35], v[38:41], off
	s_addc_u32 s47, s61, s73
	ds_read_b128 v[34:37], v171
	s_add_u32 s72, s41, s48
	s_addc_u32 s73, s47, s49
	v_lshl_add_u64 v[38:39], s[72:73], 0, v[116:117]
	v_lshl_add_u64 v[38:39], v[38:39], 0, v[114:115]
	s_waitcnt lgkmcnt(0)
	global_store_dwordx4 v[38:39], v[34:37], off
	s_addk_i32 s70, 0xb0
	s_waitcnt vmcnt(4)
	ds_write_b128 v168, v[172:175]
	s_waitcnt vmcnt(3)
	ds_write_b128 v168, v[176:179] offset:1152
	s_ashr_i32 s71, s70, 31
	ds_read_b128 v[172:175], v169
	s_lshl_b64 s[72:73], s[70:71], 11
	s_add_u32 s41, s37, s72
	s_addc_u32 s47, s54, s73
	s_add_u32 s74, s41, s50
	s_addc_u32 s75, s47, s51
	s_waitcnt lgkmcnt(0)
	v_lshlrev_b32_e32 v180, 16, v172
	v_and_b32_e32 v181, 0xffff0000, v172
	v_lshl_add_u64 v[34:35], s[74:75], 0, v[138:139]
	v_lshl_add_u64 v[36:37], s[74:75], 0, v[146:147]
	v_lshlrev_b32_e32 v172, 16, v173
	v_and_b32_e32 v173, 0xffff0000, v173
	v_lshlrev_b32_e32 v182, 16, v174
	v_and_b32_e32 v183, 0xffff0000, v174
	v_lshlrev_b32_e32 v174, 16, v175
	v_and_b32_e32 v175, 0xffff0000, v175
	v_pk_fma_f32 v[30:31], v[30:31], s[36:37], v[180:181] op_sel_hi:[1,0,1]
	v_lshl_add_u64 v[34:35], v[34:35], 0, v[144:145]
	v_lshl_add_u64 v[38:39], v[36:37], 0, v[144:145]
	v_pk_fma_f32 v[32:33], v[32:33], s[36:37], v[172:173] op_sel_hi:[1,0,1]
	v_pk_fma_f32 v[172:173], v[28:29], s[36:37], v[174:175] op_sel_hi:[1,0,1]
	v_pk_fma_f32 v[174:175], v[26:27], s[36:37], v[182:183] op_sel_hi:[1,0,1]
	v_med3_f32 v181, v30, s69, v163
	v_med3_f32 v183, v31, s69, v163
	v_mov_b32_e32 v180, v139
	global_load_dwordx4 v[34:37], v[34:35], off nt
	s_nop 0
	global_load_dwordx4 v[38:41], v[38:39], off nt
	ds_read_b128 v[176:179], v169 offset:64
	v_med3_f32 v182, v174, s69, v163
	v_med3_f32 v184, v175, s69, v163
	v_cvt_pk_fp8_f32 v180, v181, v183
	v_mov_b32_e32 v181, v139
	v_cvt_pk_fp8_f32 v181, v182, v184
	v_med3_f32 v185, v32, s69, v163
	v_med3_f32 v186, v172, s69, v163
	v_med3_f32 v182, v33, s69, v163
	v_med3_f32 v183, v173, s69, v163
	v_cvt_pk_fp8_f32 v180, v185, v182 op_sel:[0,0,1]
	v_cvt_pk_fp8_f32 v181, v186, v183 op_sel:[0,0,1]
	s_waitcnt lgkmcnt(0)
	v_lshlrev_b32_e32 v182, 16, v176
	v_and_b32_e32 v183, 0xffff0000, v176
	v_lshlrev_b32_e32 v184, 16, v178
	v_and_b32_e32 v185, 0xffff0000, v178
	v_lshlrev_b32_e32 v176, 16, v177
	v_and_b32_e32 v177, 0xffff0000, v177
	v_pk_fma_f32 v[182:183], v[22:23], s[36:37], v[182:183] op_sel_hi:[1,0,1]
	v_pk_fma_f32 v[184:185], v[18:19], s[36:37], v[184:185] op_sel_hi:[1,0,1]
	v_pk_fma_f32 v[176:177], v[24:25], s[36:37], v[176:177] op_sel_hi:[1,0,1]
	v_med3_f32 v22, v182, s69, v163
	v_med3_f32 v23, v184, s69, v163
	v_med3_f32 v24, v183, s69, v163
	v_med3_f32 v25, v185, s69, v163
	v_mov_b32_e32 v186, v139
	v_cvt_pk_bf16_f32 v26, v30, v31
	v_cvt_pk_bf16_f32 v27, v32, v33
	v_cvt_pk_bf16_f32 v28, v174, v175
	v_cvt_pk_bf16_f32 v29, v172, v173
	v_lshlrev_b32_e32 v178, 16, v179
	v_and_b32_e32 v179, 0xffff0000, v179
	v_cvt_pk_fp8_f32 v186, v22, v24
	v_cvt_pk_fp8_f32 v187, v23, v25
	v_pk_fma_f32 v[178:179], v[20:21], s[36:37], v[178:179] op_sel_hi:[1,0,1]
	v_cvt_pk_bf16_f32 v18, v182, v183
	v_cvt_pk_bf16_f32 v19, v176, v177
	v_cvt_pk_bf16_f32 v20, v184, v185
	s_add_u32 s41, s55, s80
	v_cvt_pk_bf16_f32 v21, v178, v179
	ds_write_b128 v169, v[26:29]
	ds_write_b128 v169, v[18:21] offset:64
	s_addc_u32 s47, s56, s81
	ds_read_b128 v[18:21], v168
	v_med3_f32 v188, v176, s69, v163
	v_med3_f32 v189, v178, s69, v163
	v_med3_f32 v22, v177, s69, v163
	v_med3_f32 v23, v179, s69, v163
	s_add_u32 s74, s41, s50
	v_cvt_pk_fp8_f32 v186, v188, v22 op_sel:[0,0,1]
	v_cvt_pk_fp8_f32 v187, v189, v23 op_sel:[0,0,1]
	s_addc_u32 s75, s47, s51
	ds_read_b128 v[22:25], v168 offset:1152
	v_lshl_add_u64 v[26:27], s[74:75], 0, v[138:139]
	v_lshl_add_u64 v[26:27], v[26:27], 0, v[144:145]
	s_waitcnt lgkmcnt(1)
	global_store_dwordx4 v[26:27], v[18:21], off
	ds_write2_b64 v170, v[180:181], v[186:187] offset1:4
	s_nop 0
	v_lshl_add_u64 v[18:19], s[74:75], 0, v[146:147]
	s_lshl_b64 s[74:75], s[76:77], 10
	v_lshl_add_u64 v[18:19], v[18:19], 0, v[144:145]
	s_add_u32 s41, s60, s74
	s_waitcnt lgkmcnt(1)
	global_store_dwordx4 v[18:19], v[22:25], off
	s_addc_u32 s47, s61, s75
	ds_read_b128 v[18:21], v171
	s_add_u32 s74, s41, s48
	s_addc_u32 s75, s47, s49
	v_lshl_add_u64 v[22:23], s[74:75], 0, v[116:117]
	v_lshl_add_u64 v[22:23], v[22:23], 0, v[114:115]
	s_waitcnt lgkmcnt(0)
	global_store_dwordx4 v[22:23], v[18:21], off
	s_waitcnt vmcnt(4)
	ds_write_b128 v168, v[34:37]
	s_waitcnt vmcnt(3)
	ds_write_b128 v168, v[38:41] offset:1152
	v_mul_f32_e32 v18, v31, v31
	v_mul_f32_e32 v19, v33, v33
	v_fmac_f32_e32 v18, v30, v30
	v_fmac_f32_e32 v19, v32, v32
	v_add_f32_e32 v18, v18, v19
	v_mul_f32_e32 v19, v175, v175
	v_mul_f32_e32 v20, v173, v173
	v_fmac_f32_e32 v19, v174, v174
	v_fmac_f32_e32 v20, v172, v172
	v_add_f32_e32 v19, v19, v20
	v_add_f32_e32 v18, v18, v19
	v_mul_f32_e32 v19, v183, v183
	v_mul_f32_e32 v20, v177, v177
	v_fmac_f32_e32 v19, v182, v182
	v_fmac_f32_e32 v20, v176, v176
	v_add_f32_e32 v19, v19, v20
	v_mul_f32_e32 v20, v185, v185
	v_mul_f32_e32 v21, v179, v179
	v_fmac_f32_e32 v20, v184, v184
	v_fmac_f32_e32 v21, v178, v178
	v_add_f32_e32 v20, v20, v21
	v_add_f32_e32 v19, v19, v20
	v_add_f32_e32 v30, v18, v19
	v_mul_f32_e32 v18, v47, v47
	v_mul_f32_e32 v19, v49, v49
	v_fmac_f32_e32 v18, v46, v46
	v_fmac_f32_e32 v19, v48, v48
	v_add_f32_e32 v18, v18, v19
	v_mul_f32_e32 v19, v43, v43
	v_mul_f32_e32 v20, v45, v45
	v_fmac_f32_e32 v19, v42, v42
	v_fmac_f32_e32 v20, v44, v44
	v_add_f32_e32 v19, v19, v20
	v_add_f32_e32 v18, v18, v19
	v_mul_f32_e32 v19, v157, v157
	v_mul_f32_e32 v20, v153, v153
	v_fmac_f32_e32 v19, v156, v156
	v_fmac_f32_e32 v20, v152, v152
	v_add_f32_e32 v19, v19, v20
	v_mul_f32_e32 v20, v159, v159
	v_mul_f32_e32 v21, v155, v155
	v_fmac_f32_e32 v20, v158, v158
	v_fmac_f32_e32 v21, v154, v154
	v_add_f32_e32 v20, v20, v21
	v_add_f32_e32 v19, v19, v20
	v_add_f32_e32 v31, v18, v19
	v_mul_f32_e32 v18, v63, v63
	v_mul_f32_e32 v19, v65, v65
	v_fmac_f32_e32 v18, v62, v62
	v_fmac_f32_e32 v19, v64, v64
	v_add_f32_e32 v18, v18, v19
	v_mul_f32_e32 v19, v59, v59
	v_mul_f32_e32 v20, v61, v61
	v_fmac_f32_e32 v19, v58, v58
	v_fmac_f32_e32 v20, v60, v60
	v_add_f32_e32 v19, v19, v20
	v_add_f32_e32 v18, v18, v19
	v_mul_f32_e32 v19, v55, v55
	v_mul_f32_e32 v20, v57, v57
	v_fmac_f32_e32 v19, v54, v54
	v_fmac_f32_e32 v20, v56, v56
	v_add_f32_e32 v19, v19, v20
	v_mul_f32_e32 v20, v51, v51
	v_mul_f32_e32 v21, v53, v53
	v_fmac_f32_e32 v20, v50, v50
	v_fmac_f32_e32 v21, v52, v52
	v_add_f32_e32 v20, v20, v21
	v_add_f32_e32 v19, v19, v20
	v_add_f32_e32 v32, v18, v19
	v_mul_f32_e32 v18, v79, v79
	v_mul_f32_e32 v19, v81, v81
	v_fmac_f32_e32 v18, v78, v78
	v_fmac_f32_e32 v19, v80, v80
	v_add_f32_e32 v18, v18, v19
	v_mul_f32_e32 v19, v75, v75
	v_mul_f32_e32 v20, v77, v77
	v_fmac_f32_e32 v19, v74, v74
	v_fmac_f32_e32 v20, v76, v76
	v_add_f32_e32 v19, v19, v20
	v_add_f32_e32 v18, v18, v19
	v_mul_f32_e32 v19, v71, v71
	v_mul_f32_e32 v20, v73, v73
	v_fmac_f32_e32 v19, v70, v70
	v_fmac_f32_e32 v20, v72, v72
	v_add_f32_e32 v19, v19, v20
	v_mul_f32_e32 v20, v67, v67
	v_mul_f32_e32 v21, v69, v69
	v_fmac_f32_e32 v20, v66, v66
	v_fmac_f32_e32 v21, v68, v68
	v_add_f32_e32 v20, v20, v21
	v_add_f32_e32 v19, v19, v20
	v_add_f32_e32 v33, v18, v19
	v_mul_f32_e32 v18, v95, v95
	v_mul_f32_e32 v19, v97, v97
	v_fmac_f32_e32 v18, v94, v94
	v_fmac_f32_e32 v19, v96, v96
	v_add_f32_e32 v18, v18, v19
	v_mul_f32_e32 v19, v91, v91
	v_mul_f32_e32 v20, v93, v93
	v_fmac_f32_e32 v19, v90, v90
	v_fmac_f32_e32 v20, v92, v92
	v_add_f32_e32 v19, v19, v20
	v_add_f32_e32 v18, v18, v19
	v_mul_f32_e32 v19, v87, v87
	v_mul_f32_e32 v20, v89, v89
	v_fmac_f32_e32 v19, v86, v86
	v_fmac_f32_e32 v20, v88, v88
	v_add_f32_e32 v19, v19, v20
	v_mul_f32_e32 v20, v83, v83
	v_mul_f32_e32 v21, v85, v85
	v_fmac_f32_e32 v20, v82, v82
	v_fmac_f32_e32 v21, v84, v84
	v_add_f32_e32 v20, v20, v21
	v_add_f32_e32 v19, v19, v20
	v_add_f32_e32 v42, v18, v19
	v_mul_f32_e32 v18, v111, v111
	v_mul_f32_e32 v19, v113, v113
	v_fmac_f32_e32 v18, v110, v110
	v_fmac_f32_e32 v19, v112, v112
	v_add_f32_e32 v18, v18, v19
	v_mul_f32_e32 v19, v107, v107
	v_mul_f32_e32 v20, v109, v109
	v_fmac_f32_e32 v19, v106, v106
	v_fmac_f32_e32 v20, v108, v108
	v_add_f32_e32 v19, v19, v20
	v_add_f32_e32 v18, v18, v19
	v_mul_f32_e32 v19, v103, v103
	v_mul_f32_e32 v20, v105, v105
	v_fmac_f32_e32 v19, v102, v102
	v_fmac_f32_e32 v20, v104, v104
	v_add_f32_e32 v19, v19, v20
	v_mul_f32_e32 v20, v99, v99
	v_mul_f32_e32 v21, v101, v101
	v_fmac_f32_e32 v20, v98, v98
	v_fmac_f32_e32 v21, v100, v100
	v_add_f32_e32 v20, v20, v21
	v_add_f32_e32 v19, v19, v20
	v_add_f32_e32 v43, v18, v19
	v_mul_f32_e32 v18, v151, v151
	v_mul_f32_e32 v19, v149, v149
	v_fmac_f32_e32 v18, v150, v150
	v_fmac_f32_e32 v19, v148, v148
	v_add_f32_e32 v18, v18, v19
	v_mul_f32_e32 v19, v123, v123
	v_mul_f32_e32 v20, v125, v125
	v_fmac_f32_e32 v19, v122, v122
	v_fmac_f32_e32 v20, v124, v124
	v_add_f32_e32 v19, v19, v20
	v_add_f32_e32 v22, v18, v19
	v_mul_f32_e32 v18, v127, v127
	v_mul_f32_e32 v19, v119, v119
	v_fmac_f32_e32 v18, v126, v126
	v_fmac_f32_e32 v19, v118, v118
	v_add_f32_e32 v23, v18, v19
	ds_read_b128 v[18:21], v169
	v_mul_f32_e32 v24, v129, v129
	v_mul_f32_e32 v25, v121, v121
	v_fmac_f32_e32 v24, v128, v128
	v_fmac_f32_e32 v25, v120, v120
	v_add_f32_e32 v24, v24, v25
	v_add_f32_e32 v23, v23, v24
	v_add_f32_e32 v34, v22, v23
	ds_read_b128 v[22:25], v169 offset:64
	s_waitcnt lgkmcnt(1)
	v_lshlrev_b32_e32 v26, 16, v18
	v_and_b32_e32 v27, 0xffff0000, v18
	v_lshlrev_b32_e32 v18, 16, v19
	v_and_b32_e32 v19, 0xffff0000, v19
	v_lshlrev_b32_e32 v28, 16, v20
	v_and_b32_e32 v29, 0xffff0000, v20
	v_lshlrev_b32_e32 v20, 16, v21
	v_and_b32_e32 v21, 0xffff0000, v21
	v_pk_fma_f32 v[16:17], v[16:17], s[36:37], v[18:19] op_sel_hi:[1,0,1]
	v_pk_fma_f32 v[14:15], v[14:15], s[36:37], v[26:27] op_sel_hi:[1,0,1]
	v_pk_fma_f32 v[18:19], v[12:13], s[36:37], v[20:21] op_sel_hi:[1,0,1]
	v_pk_fma_f32 v[20:21], v[10:11], s[36:37], v[28:29] op_sel_hi:[1,0,1]
	v_mul_f32_e32 v10, v15, v15
	v_mul_f32_e32 v11, v17, v17
	v_fmac_f32_e32 v10, v14, v14
	v_fmac_f32_e32 v11, v16, v16
	v_add_f32_e32 v10, v10, v11
	v_mul_f32_e32 v11, v21, v21
	v_mul_f32_e32 v12, v19, v19
	v_fmac_f32_e32 v11, v20, v20
	v_fmac_f32_e32 v12, v18, v18
	v_add_f32_e32 v11, v11, v12
	v_add_f32_e32 v26, v10, v11
	v_cvt_pk_bf16_f32 v10, v14, v15
	v_med3_f32 v27, v14, s69, v163
	v_med3_f32 v15, v15, s69, v163
	v_mov_b32_e32 v14, v139
	v_cvt_pk_bf16_f32 v11, v16, v17
	v_cvt_pk_bf16_f32 v12, v20, v21
	v_med3_f32 v20, v20, s69, v163
	v_med3_f32 v21, v21, s69, v163
	v_cvt_pk_fp8_f32 v14, v27, v15
	v_mov_b32_e32 v15, v139
	v_cvt_pk_fp8_f32 v15, v20, v21
	v_cvt_pk_bf16_f32 v13, v18, v19
	v_med3_f32 v16, v16, s69, v163
	v_med3_f32 v18, v18, s69, v163
	v_med3_f32 v17, v17, s69, v163
	v_med3_f32 v19, v19, s69, v163
	v_cvt_pk_fp8_f32 v14, v16, v17 op_sel:[0,0,1]
	v_cvt_pk_fp8_f32 v15, v18, v19 op_sel:[0,0,1]
	s_waitcnt lgkmcnt(0)
	v_lshlrev_b32_e32 v16, 16, v22
	v_and_b32_e32 v17, 0xffff0000, v22
	v_lshlrev_b32_e32 v18, 16, v23
	v_and_b32_e32 v19, 0xffff0000, v23
	v_lshlrev_b32_e32 v20, 16, v24
	v_and_b32_e32 v21, 0xffff0000, v24
	v_pk_fma_f32 v[8:9], v[8:9], s[36:37], v[18:19] op_sel_hi:[1,0,1]
	v_pk_fma_f32 v[6:7], v[6:7], s[36:37], v[16:17] op_sel_hi:[1,0,1]
	v_lshlrev_b32_e32 v22, 16, v25
	v_and_b32_e32 v23, 0xffff0000, v25
	v_pk_fma_f32 v[18:19], v[2:3], s[36:37], v[20:21] op_sel_hi:[1,0,1]
	v_mul_f32_e32 v2, v7, v7
	v_mul_f32_e32 v3, v9, v9
	v_pk_fma_f32 v[16:17], v[4:5], s[36:37], v[22:23] op_sel_hi:[1,0,1]
	v_fmac_f32_e32 v2, v6, v6
	v_fmac_f32_e32 v3, v8, v8
	v_add_f32_e32 v2, v2, v3
	v_mul_f32_e32 v3, v19, v19
	v_mul_f32_e32 v4, v17, v17
	v_fmac_f32_e32 v3, v18, v18
	v_fmac_f32_e32 v4, v16, v16
	v_add_f32_e32 v3, v3, v4
	v_add_f32_e32 v2, v2, v3
	v_add_f32_e32 v20, v26, v2
	v_cvt_pk_bf16_f32 v2, v6, v7
	v_cvt_pk_bf16_f32 v3, v8, v9
	v_cvt_pk_bf16_f32 v4, v18, v19
	v_med3_f32 v6, v6, s69, v163
	v_med3_f32 v21, v18, s69, v163
	v_med3_f32 v7, v7, s69, v163
	v_med3_f32 v22, v19, s69, v163
	v_mov_b32_e32 v18, v139
	v_mov_b32_e32 v19, v139
	v_cvt_pk_fp8_f32 v18, v6, v7
	v_cvt_pk_fp8_f32 v19, v21, v22
	v_cvt_pk_bf16_f32 v5, v16, v17
	s_add_u32 s41, s55, s72
	ds_write_b128 v169, v[10:13]
	ds_write_b128 v169, v[2:5] offset:64
	s_addc_u32 s47, s56, s73
	ds_read_b128 v[2:5], v168
	v_med3_f32 v8, v8, s69, v163
	v_med3_f32 v16, v16, s69, v163
	v_med3_f32 v6, v9, s69, v163
	v_med3_f32 v7, v17, s69, v163
	s_add_u32 s50, s41, s50
	v_cvt_pk_fp8_f32 v18, v8, v6 op_sel:[0,0,1]
	v_cvt_pk_fp8_f32 v19, v16, v7 op_sel:[0,0,1]
	s_addc_u32 s51, s47, s51
	ds_read_b128 v[6:9], v168 offset:1152
	v_lshl_add_u64 v[10:11], s[50:51], 0, v[138:139]
	v_lshl_add_u64 v[10:11], v[10:11], 0, v[144:145]
	s_waitcnt lgkmcnt(1)
	global_store_dwordx4 v[10:11], v[2:5], off
	ds_write2_b64 v170, v[14:15], v[18:19] offset1:4
	v_lshlrev_b32_e32 v10, 2, v164
	v_lshl_add_u64 v[2:3], s[50:51], 0, v[146:147]
	s_lshl_b64 s[50:51], s[70:71], 10
	v_lshl_add_u64 v[2:3], v[2:3], 0, v[144:145]
	s_add_u32 s41, s60, s50
	s_waitcnt lgkmcnt(1)
	global_store_dwordx4 v[2:3], v[6:9], off
	s_addc_u32 s47, s61, s51
	ds_read_b128 v[2:5], v171
	s_add_u32 s48, s41, s48
	s_addc_u32 s49, s47, s49
	v_lshl_add_u64 v[6:7], s[48:49], 0, v[116:117]
	v_lshl_add_u64 v[6:7], v[6:7], 0, v[114:115]
	s_waitcnt lgkmcnt(0)
	global_store_dwordx4 v[6:7], v[2:5], off
	s_lshl_b32 s14, s14, 2
	s_or_b32 s48, s39, s14
	v_lshlrev_b32_e32 v2, 2, v167
	v_lshlrev_b32_e32 v3, 4, v166
	v_add3_u32 v2, s9, v2, v3
	ds_write2st64_b32 v2, v34, v43 offset1:1
	ds_write2st64_b32 v2, v42, v33 offset0:2 offset1:3
	ds_write2st64_b32 v2, v32, v31 offset0:4 offset1:5
	ds_write2st64_b32 v2, v30, v20 offset0:6 offset1:7
	v_add_u32_e32 v6, s9, v165
	s_ashr_i32 s49, s48, 31
	s_ashr_i32 s47, s46, 31
	s_ashr_i32 s9, s8, 31
	s_lshl_b64 s[48:49], s[48:49], 18
	ds_read_b128 v[2:5], v6
	s_add_u32 s14, s58, s48
	s_addc_u32 s39, s59, s49
	s_lshl_b64 s[46:47], s[46:47], 2
	ds_read_b128 v[6:9], v6 offset:1024
	s_add_u32 s14, s14, s46
	s_addc_u32 s39, s39, s47
	s_lshl_b64 s[8:9], s[8:9], 2
	s_add_u32 s8, s14, s8
	s_waitcnt lgkmcnt(1)
	v_add_f32_e32 v2, v2, v3
	v_add_f32_e32 v3, v4, v5
	s_addc_u32 s9, s39, s9
	v_add_f32_e32 v2, v2, v3
	global_store_dword v10, v2, s[8:9]
	s_waitcnt lgkmcnt(0)
	v_add_f32_e32 v2, v6, v7
	v_add_f32_e32 v3, v8, v9
	v_add_f32_e32 v2, v2, v3
	global_store_dword v10, v2, s[8:9] offset:512
	s_and_b64 vcc, exec, s[10:11]
	s_mov_b64 s[8:9], -1
	s_cbranch_vccnz .LBB0_2291
	v_mov_b32_e32 v2, v0
	s_andn2_b64 vcc, exec, s[12:13]
	s_cbranch_vccnz .LBB0_2290
	s_barrier
	s_branch .LBB0_2290

.LBB0_3582:
	v_mov_b32_e32 v178, v0
	s_lshl_b32 s41, s70, 8
	v_readfirstlane_b32 s8, v178
	s_ashr_i32 s39, s8, 6
	s_mul_i32 s9, s39, 0xb00
	s_and_b32 s39, s39, 3
	s_lshl_b32 s47, s39, 6
	s_ashr_i32 s8, s8, 8
	s_or_b32 s48, s47, s41
	s_lshl_b32 s41, s46, 2
	s_add_i32 s50, s41, s70
	s_lshl_b32 s41, s8, 2
	s_or_b32 s58, s41, s39
	s_add_i32 s9, s9, 0
	s_ashr_i32 s51, s50, 31
	s_ashr_i32 s59, s58, 31
	s_add_i32 s9, s9, 0x20000
	s_lshl_b64 s[50:51], s[50:51], 16
	s_lshl_b64 s[58:59], s[58:59], 13
	s_add_u32 s41, s56, s50
	s_addc_u32 s47, s57, s51
	s_add_u32 s58, s41, s58
	s_addc_u32 s59, s47, s59
	s_lshl_b32 s46, s46, 8
	s_lshl_b32 s8, s8, 6
	s_add_i32 s50, s8, s46
	s_ashr_i32 s51, s50, 31
	s_ashr_i32 s49, s48, 31
	s_lshl_b64 s[60:61], s[50:51], 11
	s_add_u32 s41, s64, s60
	s_addc_u32 s47, s65, s61
	s_lshl_b64 s[48:49], s[48:49], 1
	v_and_b32_e32 v177, 63, v178
	s_add_u32 s62, s41, s48
	v_bfe_u32 v180, v178, 3, 3
	v_lshlrev_b32_e32 v154, 4, v177
	s_addc_u32 s63, s47, s49
	v_lshlrev_b32_e32 v166, 11, v180
	v_mov_b32_e32 v167, v155
	v_lshl_add_u64 v[160:161], s[62:63], 0, v[166:167]
	v_and_b32_e32 v164, 0x70, v154
	v_mov_b32_e32 v165, v155
	v_or_b32_e32 v168, 0x4000, v166
	v_mov_b32_e32 v169, v155
	v_lshl_add_u64 v[160:161], v[160:161], 0, v[164:165]
	v_lshl_add_u64 v[162:163], s[62:63], 0, v[168:169]
	global_load_dwordx4 v[170:173], v154, s[58:59] nt
	v_lshl_add_u64 v[174:175], v[162:163], 0, v[164:165]
	global_load_dwordx4 v[160:163], v[160:161], off nt
	s_nop 0
	global_load_dwordx4 v[182:185], v[174:175], off nt
	s_or_b32 s62, s50, 16
	v_pk_fma_f32 v[142:143], v[142:143], s[30:31], v[14:15] op_sel_hi:[1,0,1]
	s_ashr_i32 s63, s62, 31
	v_pk_mul_f32 v[142:143], v[142:143], s[34:35] op_sel_hi:[1,0]
	s_lshl_b64 s[62:63], s[62:63], 11
	v_pk_fma_f32 v[138:139], v[138:139], s[30:31], v[10:11] op_sel_hi:[1,0,1]
	v_exp_f32_e32 v142, v142
	v_exp_f32_e32 v143, v143
	s_add_u32 s41, s64, s62
	v_pk_mul_f32 v[138:139], v[138:139], s[34:35] op_sel_hi:[1,0]
	s_addc_u32 s47, s65, s63
	v_pk_fma_f32 v[144:145], v[144:145], s[30:31], v[16:17] op_sel_hi:[1,0,1]
	v_pk_fma_f32 v[140:141], v[140:141], s[30:31], v[12:13] op_sel_hi:[1,0,1]
	v_exp_f32_e32 v138, v138
	v_exp_f32_e32 v139, v139
	s_add_u32 s80, s41, s48
	v_pk_mul_f32 v[144:145], v[144:145], s[34:35] op_sel_hi:[1,0]
	v_pk_mul_f32 v[140:141], v[140:141], s[34:35] op_sel_hi:[1,0]
	v_and_b32_e32 v179, 15, v178
	s_addc_u32 s81, s47, s49
	v_and_b32_e32 v174, 48, v178
	v_exp_f32_e32 v194, v144
	v_exp_f32_e32 v195, v145
	v_exp_f32_e32 v196, v140
	v_exp_f32_e32 v197, v141
	v_mul_u32_u24_e32 v144, 0x90, v180
	v_mul_u32_u24_e32 v145, 0x90, v179
	v_pk_add_f32 v[140:141], v[142:143], 1.0 op_sel_hi:[1,0]
	v_lshl_add_u64 v[142:143], s[80:81], 0, v[166:167]
	v_add3_u32 v180, s9, v144, v164
	v_add3_u32 v181, s9, v145, v174
	v_lshl_add_u64 v[144:145], s[80:81], 0, v[168:169]
	v_lshl_add_u64 v[142:143], v[142:143], 0, v[164:165]
	v_pk_add_f32 v[198:199], v[138:139], 1.0 op_sel_hi:[1,0]
	v_rcp_f32_e32 v200, v140
	v_rcp_f32_e32 v201, v141
	global_load_dwordx4 v[138:141], v154, s[58:59] offset:1024 nt
	v_lshl_add_u64 v[144:145], v[144:145], 0, v[164:165]
	global_load_dwordx4 v[186:189], v[142:143], off nt
	global_load_dwordx4 v[190:193], v[144:145], off nt
	v_pk_fma_f32 v[134:135], v[134:135], s[30:31], v[2:3] op_sel_hi:[1,0,1]
	s_waitcnt vmcnt(0)
	v_pk_fma_f32 v[130:131], v[130:131], s[30:31], v[6:7] op_sel_hi:[1,0,1]
	v_pk_mul_f32 v[134:135], v[134:135], s[34:35] op_sel_hi:[1,0]
	v_pk_fma_f32 v[132:133], v[132:133], s[30:31], v[8:9] op_sel_hi:[1,0,1]
	v_pk_fma_f32 v[136:137], v[136:137], s[30:31], v[4:5] op_sel_hi:[1,0,1]
	v_pk_mul_f32 v[130:131], v[130:131], s[34:35] op_sel_hi:[1,0]
	v_exp_f32_e32 v134, v134
	v_exp_f32_e32 v135, v135
	v_pk_mul_f32 v[132:133], v[132:133], s[34:35] op_sel_hi:[1,0]
	v_pk_mul_f32 v[136:137], v[136:137], s[34:35] op_sel_hi:[1,0]
	v_rcp_f32_e32 v198, v198
	v_rcp_f32_e32 v199, v199
	v_exp_f32_e32 v130, v130
	v_exp_f32_e32 v131, v131
	s_waitcnt vmcnt(0)
	ds_write_b128 v180, v[160:163]
	ds_write_b128 v180, v[182:185] offset:1152
	ds_read_b128 v[142:145], v181
	ds_read_b128 v[182:185], v181 offset:64
	v_cvt_pk_f32_fp8_e32 v[202:203], v170
	v_cvt_pk_f32_fp8_sdwa v[160:161], v170 src0_sel:WORD_1
	v_cvt_pk_f32_fp8_e32 v[162:163], v171
	s_waitcnt lgkmcnt(0)
	v_lshlrev_b32_e32 v206, 16, v144
	v_and_b32_e32 v207, 0xffff0000, v144
	v_lshlrev_b32_e32 v208, 16, v145
	v_and_b32_e32 v209, 0xffff0000, v145
	v_pk_add_f32 v[144:145], v[194:195], 1.0 op_sel_hi:[1,0]
	v_cvt_pk_f32_fp8_sdwa v[170:171], v171 src0_sel:WORD_1
	v_pk_add_f32 v[194:195], v[196:197], 1.0 op_sel_hi:[1,0]
	v_rcp_f32_e32 v144, v144
	v_rcp_f32_e32 v145, v145
	v_exp_f32_e32 v132, v132
	v_exp_f32_e32 v133, v133
	v_exp_f32_e32 v136, v136
	v_exp_f32_e32 v137, v137
	v_rcp_f32_e32 v194, v194
	v_rcp_f32_e32 v195, v195
	v_lshlrev_b32_e32 v204, 16, v142
	v_and_b32_e32 v205, 0xffff0000, v142
	v_lshlrev_b32_e32 v142, 16, v143
	v_and_b32_e32 v143, 0xffff0000, v143
	v_pk_mul_f32 v[196:197], v[202:203], s[36:37] op_sel_hi:[1,0]
	v_pk_mul_f32 v[160:161], v[160:161], s[36:37] op_sel_hi:[1,0]
	v_pk_mul_f32 v[162:163], v[162:163], s[36:37] op_sel_hi:[1,0]
	v_pk_add_f32 v[134:135], v[134:135], 1.0 op_sel_hi:[1,0]
	v_pk_mul_f32 v[170:171], v[170:171], s[36:37] op_sel_hi:[1,0]
	v_pk_fma_f32 v[142:143], v[144:145], v[160:161], v[142:143]
	v_pk_fma_f32 v[144:145], v[200:201], v[196:197], v[204:205]
	v_pk_fma_f32 v[162:163], v[198:199], v[162:163], v[206:207]
	v_cvt_pk_f32_fp8_e32 v[200:201], v172
	v_cvt_pk_f32_fp8_sdwa v[202:203], v172 src0_sel:WORD_1
	v_cvt_pk_f32_fp8_e32 v[204:205], v173
	v_cvt_pk_f32_fp8_sdwa v[172:173], v173 src0_sel:WORD_1
	v_pk_add_f32 v[130:131], v[130:131], 1.0 op_sel_hi:[1,0]
	v_rcp_f32_e32 v206, v134
	v_rcp_f32_e32 v207, v135
	v_pk_add_f32 v[132:133], v[132:133], 1.0 op_sel_hi:[1,0]
	v_pk_add_f32 v[134:135], v[136:137], 1.0 op_sel_hi:[1,0]
	v_pk_fma_f32 v[160:161], v[194:195], v[170:171], v[208:209]
	v_rcp_f32_e32 v130, v130
	v_rcp_f32_e32 v131, v131
	v_rcp_f32_e32 v132, v132
	v_rcp_f32_e32 v133, v133
	v_rcp_f32_e32 v208, v134
	v_rcp_f32_e32 v209, v135
	v_cvt_pk_bf16_f32 v194, v144, v145
	v_cvt_pk_bf16_f32 v195, v142, v143
	v_cvt_pk_bf16_f32 v196, v162, v163
	v_cvt_pk_bf16_f32 v197, v160, v161
	v_lshlrev_b32_e32 v170, 16, v182
	v_and_b32_e32 v171, 0xffff0000, v182
	v_lshlrev_b32_e32 v182, 16, v183
	v_and_b32_e32 v183, 0xffff0000, v183
	v_lshlrev_b32_e32 v198, 16, v184
	v_and_b32_e32 v199, 0xffff0000, v184
	v_lshlrev_b32_e32 v184, 16, v185
	v_and_b32_e32 v185, 0xffff0000, v185
	v_pk_mul_f32 v[136:137], v[200:201], s[36:37] op_sel_hi:[1,0]
	v_pk_mul_f32 v[134:135], v[202:203], s[36:37] op_sel_hi:[1,0]
	v_pk_mul_f32 v[200:201], v[204:205], s[36:37] op_sel_hi:[1,0]
	v_pk_mul_f32 v[172:173], v[172:173], s[36:37] op_sel_hi:[1,0]
	v_pk_fma_f32 v[134:135], v[132:133], v[134:135], v[182:183]
	v_pk_fma_f32 v[136:137], v[130:131], v[136:137], v[170:171]
	v_pk_fma_f32 v[170:171], v[208:209], v[172:173], v[184:185]
	v_pk_fma_f32 v[172:173], v[206:207], v[200:201], v[198:199]
	v_cvt_pk_bf16_f32 v130, v136, v137
	v_cvt_pk_bf16_f32 v131, v134, v135
	s_add_u32 s41, s66, s60
	v_cvt_pk_bf16_f32 v132, v172, v173
	v_cvt_pk_bf16_f32 v133, v170, v171
	ds_write_b128 v181, v[194:197]
	ds_write_b128 v181, v[130:133] offset:64
	s_addc_u32 s47, s67, s61
	ds_read_b128 v[130:133], v180
	ds_read_b128 v[182:185], v180 offset:1152
	s_add_u32 s60, s41, s48
	s_addc_u32 s61, s47, s49
	v_lshl_add_u64 v[194:195], s[60:61], 0, v[166:167]
	v_lshl_add_u64 v[194:195], v[194:195], 0, v[164:165]
	s_waitcnt lgkmcnt(1)
	global_store_dwordx4 v[194:195], v[130:133], off
	v_pk_fma_f32 v[122:123], v[122:123], s[30:31], v[14:15] op_sel_hi:[1,0,1]
	v_pk_fma_f32 v[126:127], v[126:127], s[30:31], v[10:11] op_sel_hi:[1,0,1]
	v_lshl_add_u64 v[130:131], s[60:61], 0, v[168:169]
	s_or_b32 s60, s50, 32
	s_ashr_i32 s61, s60, 31
	s_lshl_b64 s[60:61], s[60:61], 11
	s_add_u32 s41, s64, s60
	s_addc_u32 s47, s65, s61
	v_lshl_add_u64 v[130:131], v[130:131], 0, v[164:165]
	s_add_u32 s80, s41, s48
	s_waitcnt lgkmcnt(0)
	global_store_dwordx4 v[130:131], v[182:185], off
	s_addc_u32 s81, s47, s49
	v_lshl_add_u64 v[196:197], s[80:81], 0, v[168:169]
	v_lshl_add_u64 v[182:183], s[80:81], 0, v[166:167]
	global_load_dwordx4 v[130:133], v154, s[58:59] offset:2048 nt
	v_lshl_add_u64 v[194:195], v[182:183], 0, v[164:165]
	ds_write_b128 v180, v[186:189]
	ds_write_b128 v180, v[190:193] offset:1152
	v_lshl_add_u64 v[190:191], v[196:197], 0, v[164:165]
	ds_read_b128 v[182:185], v181
	global_load_dwordx4 v[186:189], v[194:195], off nt
	s_nop 0
	global_load_dwordx4 v[190:193], v[190:191], off nt
	v_pk_mul_f32 v[122:123], v[122:123], s[34:35] op_sel_hi:[1,0]
	v_pk_fma_f32 v[124:125], v[124:125], s[30:31], v[16:17] op_sel_hi:[1,0,1]
	v_exp_f32_e32 v122, v122
	v_exp_f32_e32 v123, v123
	v_pk_mul_f32 v[126:127], v[126:127], s[34:35] op_sel_hi:[1,0]
	v_pk_fma_f32 v[128:129], v[128:129], s[30:31], v[12:13] op_sel_hi:[1,0,1]
	v_exp_f32_e32 v126, v126
	v_pk_add_f32 v[122:123], v[122:123], 1.0 op_sel_hi:[1,0]
	v_exp_f32_e32 v127, v127
	v_rcp_f32_e32 v208, v122
	v_rcp_f32_e32 v209, v123
	v_pk_mul_f32 v[122:123], v[124:125], s[34:35] op_sel_hi:[1,0]
	v_pk_mul_f32 v[124:125], v[128:129], s[34:35] op_sel_hi:[1,0]
	v_exp_f32_e32 v122, v122
	v_exp_f32_e32 v123, v123
	v_pk_fma_f32 v[118:119], v[118:119], s[30:31], v[2:3] op_sel_hi:[1,0,1]
	v_exp_f32_e32 v124, v124
	v_exp_f32_e32 v125, v125
	v_pk_fma_f32 v[114:115], v[114:115], s[30:31], v[6:7] op_sel_hi:[1,0,1]
	v_pk_mul_f32 v[118:119], v[118:119], s[34:35] op_sel_hi:[1,0]
	v_pk_fma_f32 v[116:117], v[116:117], s[30:31], v[8:9] op_sel_hi:[1,0,1]
	v_pk_fma_f32 v[120:121], v[120:121], s[30:31], v[4:5] op_sel_hi:[1,0,1]
	v_cvt_pk_f32_fp8_e32 v[202:203], v138
	v_cvt_pk_f32_fp8_sdwa v[204:205], v138 src0_sel:WORD_1
	v_cvt_pk_f32_fp8_e32 v[206:207], v139
	v_pk_add_f32 v[126:127], v[126:127], 1.0 op_sel_hi:[1,0]
	v_pk_add_f32 v[122:123], v[122:123], 1.0 op_sel_hi:[1,0]
	v_pk_mul_f32 v[114:115], v[114:115], s[34:35] op_sel_hi:[1,0]
	v_exp_f32_e32 v118, v118
	v_exp_f32_e32 v119, v119
	v_pk_mul_f32 v[116:117], v[116:117], s[34:35] op_sel_hi:[1,0]
	v_pk_mul_f32 v[120:121], v[120:121], s[34:35] op_sel_hi:[1,0]
	v_rcp_f32_e32 v128, v126
	v_rcp_f32_e32 v129, v127
	v_rcp_f32_e32 v122, v122
	v_rcp_f32_e32 v123, v123
	v_exp_f32_e32 v114, v114
	v_exp_f32_e32 v115, v115
	v_exp_f32_e32 v116, v116
	v_exp_f32_e32 v117, v117
	v_exp_f32_e32 v120, v120
	v_exp_f32_e32 v121, v121
	v_pk_add_f32 v[124:125], v[124:125], 1.0 op_sel_hi:[1,0]
	ds_read_b128 v[194:197], v181 offset:64
	s_waitcnt lgkmcnt(1)
	v_lshlrev_b32_e32 v198, 16, v182
	v_and_b32_e32 v199, 0xffff0000, v182
	v_lshlrev_b32_e32 v182, 16, v183
	v_and_b32_e32 v183, 0xffff0000, v183
	v_lshlrev_b32_e32 v200, 16, v184
	v_and_b32_e32 v201, 0xffff0000, v184
	v_cvt_pk_f32_fp8_sdwa v[138:139], v139 src0_sel:WORD_1
	v_rcp_f32_e32 v126, v124
	v_rcp_f32_e32 v127, v125
	v_pk_mul_f32 v[124:125], v[202:203], s[36:37] op_sel_hi:[1,0]
	v_pk_mul_f32 v[202:203], v[204:205], s[36:37] op_sel_hi:[1,0]
	v_pk_mul_f32 v[204:205], v[206:207], s[36:37] op_sel_hi:[1,0]
	v_pk_add_f32 v[118:119], v[118:119], 1.0 op_sel_hi:[1,0]
	v_pk_fma_f32 v[122:123], v[122:123], v[202:203], v[182:183]
	v_pk_fma_f32 v[128:129], v[128:129], v[204:205], v[200:201]
	v_cvt_pk_f32_fp8_e32 v[200:201], v140
	v_cvt_pk_f32_fp8_sdwa v[202:203], v140 src0_sel:WORD_1
	v_cvt_pk_f32_fp8_e32 v[204:205], v141
	v_cvt_pk_f32_fp8_sdwa v[140:141], v141 src0_sel:WORD_1
	v_pk_add_f32 v[114:115], v[114:115], 1.0 op_sel_hi:[1,0]
	v_rcp_f32_e32 v206, v118
	v_rcp_f32_e32 v207, v119
	v_pk_add_f32 v[116:117], v[116:117], 1.0 op_sel_hi:[1,0]
	v_pk_add_f32 v[118:119], v[120:121], 1.0 op_sel_hi:[1,0]
	v_pk_fma_f32 v[124:125], v[208:209], v[124:125], v[198:199]
	v_rcp_f32_e32 v114, v114
	v_rcp_f32_e32 v115, v115
	v_rcp_f32_e32 v116, v116
	v_rcp_f32_e32 v117, v117
	v_rcp_f32_e32 v208, v118
	v_rcp_f32_e32 v209, v119
	v_lshlrev_b32_e32 v184, 16, v185
	v_and_b32_e32 v185, 0xffff0000, v185
	v_pk_mul_f32 v[138:139], v[138:139], s[36:37] op_sel_hi:[1,0]
	v_cvt_pk_bf16_f32 v182, v124, v125
	v_cvt_pk_bf16_f32 v183, v122, v123
	s_waitcnt lgkmcnt(0)
	v_lshlrev_b32_e32 v198, 16, v196
	v_pk_fma_f32 v[126:127], v[126:127], v[138:139], v[184:185]
	v_cvt_pk_bf16_f32 v184, v128, v129
	v_lshlrev_b32_e32 v138, 16, v194
	v_cvt_pk_bf16_f32 v185, v126, v127
	v_and_b32_e32 v139, 0xffff0000, v194
	v_lshlrev_b32_e32 v194, 16, v195
	v_and_b32_e32 v195, 0xffff0000, v195
	v_and_b32_e32 v199, 0xffff0000, v196
	v_lshlrev_b32_e32 v196, 16, v197
	v_and_b32_e32 v197, 0xffff0000, v197
	v_pk_mul_f32 v[120:121], v[200:201], s[36:37] op_sel_hi:[1,0]
	v_pk_mul_f32 v[118:119], v[202:203], s[36:37] op_sel_hi:[1,0]
	v_pk_mul_f32 v[200:201], v[204:205], s[36:37] op_sel_hi:[1,0]
	v_pk_mul_f32 v[140:141], v[140:141], s[36:37] op_sel_hi:[1,0]
	v_pk_fma_f32 v[118:119], v[116:117], v[118:119], v[194:195]
	v_pk_fma_f32 v[120:121], v[114:115], v[120:121], v[138:139]
	v_pk_fma_f32 v[138:139], v[208:209], v[140:141], v[196:197]
	v_pk_fma_f32 v[140:141], v[206:207], v[200:201], v[198:199]
	v_cvt_pk_bf16_f32 v114, v120, v121
	v_cvt_pk_bf16_f32 v115, v118, v119
	s_add_u32 s41, s66, s62
	v_cvt_pk_bf16_f32 v116, v140, v141
	v_cvt_pk_bf16_f32 v117, v138, v139
	ds_write_b128 v181, v[182:185]
	ds_write_b128 v181, v[114:117] offset:64
	s_addc_u32 s47, s67, s63
	ds_read_b128 v[114:117], v180
	ds_read_b128 v[182:185], v180 offset:1152
	s_add_u32 s62, s41, s48
	s_addc_u32 s63, s47, s49
	v_lshl_add_u64 v[194:195], s[62:63], 0, v[166:167]
	v_lshl_add_u64 v[194:195], v[194:195], 0, v[164:165]
	s_waitcnt lgkmcnt(1)
	global_store_dwordx4 v[194:195], v[114:117], off
	v_lshl_add_u64 v[174:175], s[58:59], 0, v[154:155]
	v_pk_fma_f32 v[106:107], v[106:107], s[30:31], v[14:15] op_sel_hi:[1,0,1]
	v_lshl_add_u64 v[114:115], s[62:63], 0, v[168:169]
	v_lshl_add_u64 v[114:115], v[114:115], 0, v[164:165]
	s_waitcnt lgkmcnt(0)
	global_store_dwordx4 v[114:115], v[182:185], off
	global_load_dwordx4 v[114:117], v154, s[58:59] offset:3072 nt
	s_or_b32 s58, s50, 48
	s_ashr_i32 s59, s58, 31
	s_lshl_b64 s[58:59], s[58:59], 11
	s_add_u32 s41, s64, s58
	s_addc_u32 s47, s65, s59
	s_add_u32 s62, s41, s48
	s_addc_u32 s63, s47, s49
	v_lshl_add_u64 v[182:183], s[62:63], 0, v[166:167]
	v_lshl_add_u64 v[196:197], s[62:63], 0, v[168:169]
	v_lshl_add_u64 v[194:195], v[182:183], 0, v[164:165]
	s_waitcnt vmcnt(4)
	ds_write_b128 v180, v[186:189]
	s_waitcnt vmcnt(3)
	ds_write_b128 v180, v[190:193] offset:1152
	v_lshl_add_u64 v[190:191], v[196:197], 0, v[164:165]
	ds_read_b128 v[182:185], v181
	global_load_dwordx4 v[186:189], v[194:195], off nt
	s_nop 0
	global_load_dwordx4 v[190:193], v[190:191], off nt
	v_pk_mul_f32 v[106:107], v[106:107], s[34:35] op_sel_hi:[1,0]
	v_pk_fma_f32 v[110:111], v[110:111], s[30:31], v[10:11] op_sel_hi:[1,0,1]
	v_exp_f32_e32 v106, v106
	v_exp_f32_e32 v107, v107
	v_pk_fma_f32 v[108:109], v[108:109], s[30:31], v[16:17] op_sel_hi:[1,0,1]
	v_pk_mul_f32 v[110:111], v[110:111], s[34:35] op_sel_hi:[1,0]
	v_pk_fma_f32 v[112:113], v[112:113], s[30:31], v[12:13] op_sel_hi:[1,0,1]
	v_pk_add_f32 v[106:107], v[106:107], 1.0 op_sel_hi:[1,0]
	v_exp_f32_e32 v110, v110
	v_rcp_f32_e32 v208, v106
	v_rcp_f32_e32 v209, v107
	v_pk_mul_f32 v[106:107], v[108:109], s[34:35] op_sel_hi:[1,0]
	v_exp_f32_e32 v111, v111
	v_exp_f32_e32 v106, v106
	v_exp_f32_e32 v107, v107
	v_pk_mul_f32 v[108:109], v[112:113], s[34:35] op_sel_hi:[1,0]
	v_pk_fma_f32 v[102:103], v[102:103], s[30:31], v[2:3] op_sel_hi:[1,0,1]
	v_exp_f32_e32 v108, v108
	v_exp_f32_e32 v109, v109
	v_pk_fma_f32 v[98:99], v[98:99], s[30:31], v[6:7] op_sel_hi:[1,0,1]
	v_pk_mul_f32 v[102:103], v[102:103], s[34:35] op_sel_hi:[1,0]
	v_pk_fma_f32 v[100:101], v[100:101], s[30:31], v[8:9] op_sel_hi:[1,0,1]
	v_pk_fma_f32 v[104:105], v[104:105], s[30:31], v[4:5] op_sel_hi:[1,0,1]
	v_cvt_pk_f32_fp8_e32 v[202:203], v130
	v_cvt_pk_f32_fp8_sdwa v[204:205], v130 src0_sel:WORD_1
	v_cvt_pk_f32_fp8_e32 v[206:207], v131
	v_pk_add_f32 v[110:111], v[110:111], 1.0 op_sel_hi:[1,0]
	v_pk_add_f32 v[106:107], v[106:107], 1.0 op_sel_hi:[1,0]
	v_pk_mul_f32 v[98:99], v[98:99], s[34:35] op_sel_hi:[1,0]
	v_exp_f32_e32 v102, v102
	v_exp_f32_e32 v103, v103
	v_pk_mul_f32 v[100:101], v[100:101], s[34:35] op_sel_hi:[1,0]
	v_pk_mul_f32 v[104:105], v[104:105], s[34:35] op_sel_hi:[1,0]
	v_rcp_f32_e32 v112, v110
	v_rcp_f32_e32 v113, v111
	v_rcp_f32_e32 v106, v106
	v_rcp_f32_e32 v107, v107
	v_exp_f32_e32 v98, v98
	v_exp_f32_e32 v99, v99
	v_exp_f32_e32 v100, v100
	v_exp_f32_e32 v101, v101
	v_exp_f32_e32 v104, v104
	v_exp_f32_e32 v105, v105
	v_pk_add_f32 v[108:109], v[108:109], 1.0 op_sel_hi:[1,0]
	ds_read_b128 v[194:197], v181 offset:64
	s_waitcnt lgkmcnt(1)
	v_lshlrev_b32_e32 v198, 16, v182
	v_and_b32_e32 v199, 0xffff0000, v182
	v_lshlrev_b32_e32 v182, 16, v183
	v_and_b32_e32 v183, 0xffff0000, v183
	v_lshlrev_b32_e32 v200, 16, v184
	v_and_b32_e32 v201, 0xffff0000, v184
	v_cvt_pk_f32_fp8_sdwa v[130:131], v131 src0_sel:WORD_1
	v_rcp_f32_e32 v110, v108
	v_rcp_f32_e32 v111, v109
	v_pk_mul_f32 v[108:109], v[202:203], s[36:37] op_sel_hi:[1,0]
	v_pk_mul_f32 v[202:203], v[204:205], s[36:37] op_sel_hi:[1,0]
	v_pk_mul_f32 v[204:205], v[206:207], s[36:37] op_sel_hi:[1,0]
	v_pk_add_f32 v[102:103], v[102:103], 1.0 op_sel_hi:[1,0]
	v_pk_fma_f32 v[106:107], v[106:107], v[202:203], v[182:183]
	v_pk_fma_f32 v[112:113], v[112:113], v[204:205], v[200:201]
	v_cvt_pk_f32_fp8_e32 v[200:201], v132
	v_cvt_pk_f32_fp8_sdwa v[202:203], v132 src0_sel:WORD_1
	v_cvt_pk_f32_fp8_e32 v[204:205], v133
	v_cvt_pk_f32_fp8_sdwa v[132:133], v133 src0_sel:WORD_1
	v_pk_add_f32 v[98:99], v[98:99], 1.0 op_sel_hi:[1,0]
	v_rcp_f32_e32 v206, v102
	v_rcp_f32_e32 v207, v103
	v_pk_add_f32 v[100:101], v[100:101], 1.0 op_sel_hi:[1,0]
	v_pk_add_f32 v[102:103], v[104:105], 1.0 op_sel_hi:[1,0]
	v_pk_fma_f32 v[108:109], v[208:209], v[108:109], v[198:199]
	v_rcp_f32_e32 v98, v98
	v_rcp_f32_e32 v99, v99
	v_rcp_f32_e32 v100, v100
	v_rcp_f32_e32 v101, v101
	v_rcp_f32_e32 v208, v102
	v_rcp_f32_e32 v209, v103
	v_lshlrev_b32_e32 v184, 16, v185
	v_and_b32_e32 v185, 0xffff0000, v185
	v_pk_mul_f32 v[130:131], v[130:131], s[36:37] op_sel_hi:[1,0]
	v_cvt_pk_bf16_f32 v182, v108, v109
	v_cvt_pk_bf16_f32 v183, v106, v107
	s_waitcnt lgkmcnt(0)
	v_lshlrev_b32_e32 v198, 16, v196
	v_pk_fma_f32 v[110:111], v[110:111], v[130:131], v[184:185]
	v_cvt_pk_bf16_f32 v184, v112, v113
	v_lshlrev_b32_e32 v130, 16, v194
	v_cvt_pk_bf16_f32 v185, v110, v111
	v_and_b32_e32 v131, 0xffff0000, v194
	v_lshlrev_b32_e32 v194, 16, v195
	v_and_b32_e32 v195, 0xffff0000, v195
	v_and_b32_e32 v199, 0xffff0000, v196
	v_lshlrev_b32_e32 v196, 16, v197
	v_and_b32_e32 v197, 0xffff0000, v197
	v_pk_mul_f32 v[104:105], v[200:201], s[36:37] op_sel_hi:[1,0]
	v_pk_mul_f32 v[102:103], v[202:203], s[36:37] op_sel_hi:[1,0]
	v_pk_mul_f32 v[200:201], v[204:205], s[36:37] op_sel_hi:[1,0]
	v_pk_mul_f32 v[132:133], v[132:133], s[36:37] op_sel_hi:[1,0]
	v_pk_fma_f32 v[102:103], v[100:101], v[102:103], v[194:195]
	v_pk_fma_f32 v[104:105], v[98:99], v[104:105], v[130:131]
	v_pk_fma_f32 v[130:131], v[208:209], v[132:133], v[196:197]
	v_pk_fma_f32 v[132:133], v[206:207], v[200:201], v[198:199]
	v_cvt_pk_bf16_f32 v98, v104, v105
	v_cvt_pk_bf16_f32 v99, v102, v103
	s_add_u32 s41, s66, s60
	v_cvt_pk_bf16_f32 v100, v132, v133
	v_cvt_pk_bf16_f32 v101, v130, v131
	ds_write_b128 v181, v[182:185]
	ds_write_b128 v181, v[98:101] offset:64
	s_addc_u32 s47, s67, s61
	ds_read_b128 v[98:101], v180
	ds_read_b128 v[182:185], v180 offset:1152
	s_add_u32 s60, s41, s48
	s_addc_u32 s61, s47, s49
	v_lshl_add_u64 v[194:195], s[60:61], 0, v[166:167]
	v_lshl_add_u64 v[194:195], v[194:195], 0, v[164:165]
	s_waitcnt lgkmcnt(1)
	global_store_dwordx4 v[194:195], v[98:101], off
	v_add_co_u32_e32 v174, vcc, s78, v174
	s_nop 0
	v_lshl_add_u64 v[98:99], s[60:61], 0, v[168:169]
	s_add_i32 s60, s50, 0x80
	s_ashr_i32 s61, s60, 31
	s_lshl_b64 s[60:61], s[60:61], 11
	s_add_u32 s41, s64, s60
	s_addc_u32 s47, s65, s61
	s_add_u32 s62, s41, s48
	v_lshl_add_u64 v[98:99], v[98:99], 0, v[164:165]
	s_addc_u32 s63, s47, s49
	s_waitcnt lgkmcnt(0)
	global_store_dwordx4 v[98:99], v[182:185], off
	v_lshl_add_u64 v[98:99], s[62:63], 0, v[166:167]
	v_addc_co_u32_e32 v175, vcc, 0, v175, vcc
	v_lshl_add_u64 v[182:183], v[98:99], 0, v[164:165]
	global_load_dwordx4 v[98:101], v[174:175], off nt
	s_nop 0
	global_load_dwordx4 v[182:185], v[182:183], off nt
	s_waitcnt vmcnt(5)
	ds_write_b128 v180, v[186:189]
	s_waitcnt vmcnt(4)
	ds_write_b128 v180, v[190:193] offset:1152
	v_lshl_add_u64 v[190:191], s[62:63], 0, v[168:169]
	v_lshl_add_u64 v[190:191], v[190:191], 0, v[164:165]
	global_load_dwordx4 v[190:193], v[190:191], off nt
	v_pk_fma_f32 v[90:91], v[90:91], s[30:31], v[14:15] op_sel_hi:[1,0,1]
	v_pk_fma_f32 v[94:95], v[94:95], s[30:31], v[10:11] op_sel_hi:[1,0,1]
	v_pk_mul_f32 v[90:91], v[90:91], s[34:35] op_sel_hi:[1,0]
	v_pk_fma_f32 v[92:93], v[92:93], s[30:31], v[16:17] op_sel_hi:[1,0,1]
	v_exp_f32_e32 v90, v90
	v_exp_f32_e32 v91, v91
	v_pk_mul_f32 v[94:95], v[94:95], s[34:35] op_sel_hi:[1,0]
	v_pk_fma_f32 v[96:97], v[96:97], s[30:31], v[12:13] op_sel_hi:[1,0,1]
	v_exp_f32_e32 v94, v94
	v_pk_add_f32 v[90:91], v[90:91], 1.0 op_sel_hi:[1,0]
	v_exp_f32_e32 v95, v95
	v_rcp_f32_e32 v208, v90
	v_rcp_f32_e32 v209, v91
	v_pk_mul_f32 v[90:91], v[92:93], s[34:35] op_sel_hi:[1,0]
	v_pk_mul_f32 v[92:93], v[96:97], s[34:35] op_sel_hi:[1,0]
	v_exp_f32_e32 v90, v90
	v_exp_f32_e32 v91, v91
	v_pk_fma_f32 v[86:87], v[86:87], s[30:31], v[2:3] op_sel_hi:[1,0,1]
	ds_read_b128 v[186:189], v181
	ds_read_b128 v[194:197], v181 offset:64
	v_exp_f32_e32 v92, v92
	v_exp_f32_e32 v93, v93
	v_pk_fma_f32 v[82:83], v[82:83], s[30:31], v[6:7] op_sel_hi:[1,0,1]
	v_pk_mul_f32 v[86:87], v[86:87], s[34:35] op_sel_hi:[1,0]
	v_pk_fma_f32 v[84:85], v[84:85], s[30:31], v[8:9] op_sel_hi:[1,0,1]
	v_pk_fma_f32 v[88:89], v[88:89], s[30:31], v[4:5] op_sel_hi:[1,0,1]
	v_cvt_pk_f32_fp8_e32 v[202:203], v114
	v_cvt_pk_f32_fp8_sdwa v[204:205], v114 src0_sel:WORD_1
	v_cvt_pk_f32_fp8_e32 v[206:207], v115
	v_pk_add_f32 v[94:95], v[94:95], 1.0 op_sel_hi:[1,0]
	v_pk_add_f32 v[90:91], v[90:91], 1.0 op_sel_hi:[1,0]
	v_pk_mul_f32 v[82:83], v[82:83], s[34:35] op_sel_hi:[1,0]
	v_exp_f32_e32 v86, v86
	v_exp_f32_e32 v87, v87
	v_pk_mul_f32 v[84:85], v[84:85], s[34:35] op_sel_hi:[1,0]
	v_pk_mul_f32 v[88:89], v[88:89], s[34:35] op_sel_hi:[1,0]
	v_rcp_f32_e32 v96, v94
	v_rcp_f32_e32 v97, v95
	v_rcp_f32_e32 v90, v90
	v_rcp_f32_e32 v91, v91
	v_exp_f32_e32 v82, v82
	v_exp_f32_e32 v83, v83
	v_exp_f32_e32 v84, v84
	v_exp_f32_e32 v85, v85
	v_exp_f32_e32 v88, v88
	v_exp_f32_e32 v89, v89
	v_pk_add_f32 v[92:93], v[92:93], 1.0 op_sel_hi:[1,0]
	s_waitcnt lgkmcnt(1)
	v_lshlrev_b32_e32 v198, 16, v186
	v_and_b32_e32 v199, 0xffff0000, v186
	v_lshlrev_b32_e32 v186, 16, v187
	v_and_b32_e32 v187, 0xffff0000, v187
	v_lshlrev_b32_e32 v200, 16, v188
	v_and_b32_e32 v201, 0xffff0000, v188
	v_cvt_pk_f32_fp8_sdwa v[114:115], v115 src0_sel:WORD_1
	v_rcp_f32_e32 v94, v92
	v_rcp_f32_e32 v95, v93
	v_pk_mul_f32 v[92:93], v[202:203], s[36:37] op_sel_hi:[1,0]
	v_pk_mul_f32 v[202:203], v[204:205], s[36:37] op_sel_hi:[1,0]
	v_pk_mul_f32 v[204:205], v[206:207], s[36:37] op_sel_hi:[1,0]
	v_pk_add_f32 v[86:87], v[86:87], 1.0 op_sel_hi:[1,0]
	v_pk_fma_f32 v[90:91], v[90:91], v[202:203], v[186:187]
	v_pk_fma_f32 v[96:97], v[96:97], v[204:205], v[200:201]
	v_cvt_pk_f32_fp8_e32 v[200:201], v116
	v_cvt_pk_f32_fp8_sdwa v[202:203], v116 src0_sel:WORD_1
	v_cvt_pk_f32_fp8_e32 v[204:205], v117
	v_cvt_pk_f32_fp8_sdwa v[116:117], v117 src0_sel:WORD_1
	v_pk_add_f32 v[82:83], v[82:83], 1.0 op_sel_hi:[1,0]
	v_rcp_f32_e32 v206, v86
	v_rcp_f32_e32 v207, v87
	v_pk_add_f32 v[84:85], v[84:85], 1.0 op_sel_hi:[1,0]
	v_pk_add_f32 v[86:87], v[88:89], 1.0 op_sel_hi:[1,0]
	v_pk_fma_f32 v[92:93], v[208:209], v[92:93], v[198:199]
	v_rcp_f32_e32 v82, v82
	v_rcp_f32_e32 v83, v83
	v_rcp_f32_e32 v84, v84
	v_rcp_f32_e32 v85, v85
	v_rcp_f32_e32 v208, v86
	v_rcp_f32_e32 v209, v87
	v_lshlrev_b32_e32 v188, 16, v189
	v_and_b32_e32 v189, 0xffff0000, v189
	v_pk_mul_f32 v[114:115], v[114:115], s[36:37] op_sel_hi:[1,0]
	v_cvt_pk_bf16_f32 v186, v92, v93
	v_cvt_pk_bf16_f32 v187, v90, v91
	s_waitcnt lgkmcnt(0)
	v_lshlrev_b32_e32 v198, 16, v196
	v_pk_fma_f32 v[94:95], v[94:95], v[114:115], v[188:189]
	v_cvt_pk_bf16_f32 v188, v96, v97
	v_lshlrev_b32_e32 v114, 16, v194
	v_cvt_pk_bf16_f32 v189, v94, v95
	v_and_b32_e32 v115, 0xffff0000, v194
	v_lshlrev_b32_e32 v194, 16, v195
	v_and_b32_e32 v195, 0xffff0000, v195
	v_and_b32_e32 v199, 0xffff0000, v196
	v_lshlrev_b32_e32 v196, 16, v197
	v_and_b32_e32 v197, 0xffff0000, v197
	v_pk_mul_f32 v[88:89], v[200:201], s[36:37] op_sel_hi:[1,0]
	v_pk_mul_f32 v[86:87], v[202:203], s[36:37] op_sel_hi:[1,0]
	v_pk_mul_f32 v[200:201], v[204:205], s[36:37] op_sel_hi:[1,0]
	v_pk_mul_f32 v[116:117], v[116:117], s[36:37] op_sel_hi:[1,0]
	v_pk_fma_f32 v[86:87], v[84:85], v[86:87], v[194:195]
	v_pk_fma_f32 v[88:89], v[82:83], v[88:89], v[114:115]
	v_pk_fma_f32 v[114:115], v[208:209], v[116:117], v[196:197]
	v_pk_fma_f32 v[116:117], v[206:207], v[200:201], v[198:199]
	v_cvt_pk_bf16_f32 v82, v88, v89
	v_cvt_pk_bf16_f32 v83, v86, v87
	s_add_u32 s41, s66, s58
	v_cvt_pk_bf16_f32 v84, v116, v117
	v_cvt_pk_bf16_f32 v85, v114, v115
	ds_write_b128 v181, v[186:189]
	ds_write_b128 v181, v[82:85] offset:64
	s_addc_u32 s47, s67, s59
	ds_read_b128 v[82:85], v180
	ds_read_b128 v[186:189], v180 offset:1152
	s_add_u32 s58, s41, s48
	s_addc_u32 s59, s47, s49
	v_lshl_add_u64 v[194:195], s[58:59], 0, v[166:167]
	v_lshl_add_u64 v[194:195], v[194:195], 0, v[164:165]
	s_waitcnt lgkmcnt(1)
	global_store_dwordx4 v[194:195], v[82:85], off
	v_pk_fma_f32 v[74:75], v[74:75], s[30:31], v[14:15] op_sel_hi:[1,0,1]
	v_pk_fma_f32 v[78:79], v[78:79], s[30:31], v[10:11] op_sel_hi:[1,0,1]
	v_lshl_add_u64 v[82:83], s[58:59], 0, v[168:169]
	s_add_i32 s58, s50, 0x90
	s_ashr_i32 s59, s58, 31
	s_lshl_b64 s[58:59], s[58:59], 11
	s_add_u32 s41, s64, s58
	s_addc_u32 s47, s65, s59
	s_add_u32 s62, s41, s48
	v_lshl_add_u64 v[82:83], v[82:83], 0, v[164:165]
	s_addc_u32 s63, s47, s49
	s_waitcnt lgkmcnt(0)
	global_store_dwordx4 v[82:83], v[186:189], off
	v_lshl_add_u64 v[82:83], s[62:63], 0, v[166:167]
	v_pk_fma_f32 v[76:77], v[76:77], s[30:31], v[16:17] op_sel_hi:[1,0,1]
	v_lshl_add_u64 v[186:187], v[82:83], 0, v[164:165]
	global_load_dwordx4 v[82:85], v[174:175], off offset:1024 nt
	s_nop 0
	global_load_dwordx4 v[186:189], v[186:187], off nt
	s_waitcnt vmcnt(5)
	ds_write_b128 v180, v[182:185]
	s_waitcnt vmcnt(4)
	ds_write_b128 v180, v[190:193] offset:1152
	v_lshl_add_u64 v[190:191], s[62:63], 0, v[168:169]
	v_lshl_add_u64 v[190:191], v[190:191], 0, v[164:165]
	global_load_dwordx4 v[190:193], v[190:191], off nt
	v_pk_mul_f32 v[74:75], v[74:75], s[34:35] op_sel_hi:[1,0]
	v_pk_mul_f32 v[78:79], v[78:79], s[34:35] op_sel_hi:[1,0]
	v_pk_mul_f32 v[76:77], v[76:77], s[34:35] op_sel_hi:[1,0]
	v_exp_f32_e32 v74, v74
	v_exp_f32_e32 v75, v75
	v_exp_f32_e32 v78, v78
	v_exp_f32_e32 v79, v79
	v_exp_f32_e32 v76, v76
	v_exp_f32_e32 v77, v77
	v_pk_fma_f32 v[80:81], v[80:81], s[30:31], v[12:13] op_sel_hi:[1,0,1]
	v_pk_fma_f32 v[70:71], v[70:71], s[30:31], v[2:3] op_sel_hi:[1,0,1]
	ds_read_b128 v[182:185], v181
	ds_read_b128 v[194:197], v181 offset:64
	v_pk_mul_f32 v[80:81], v[80:81], s[34:35] op_sel_hi:[1,0]
	v_pk_fma_f32 v[66:67], v[66:67], s[30:31], v[6:7] op_sel_hi:[1,0,1]
	v_pk_mul_f32 v[70:71], v[70:71], s[34:35] op_sel_hi:[1,0]
	v_pk_fma_f32 v[68:69], v[68:69], s[30:31], v[8:9] op_sel_hi:[1,0,1]
	v_pk_fma_f32 v[72:73], v[72:73], s[30:31], v[4:5] op_sel_hi:[1,0,1]
	v_cvt_pk_f32_fp8_e32 v[202:203], v98
	v_cvt_pk_f32_fp8_sdwa v[204:205], v98 src0_sel:WORD_1
	v_cvt_pk_f32_fp8_e32 v[206:207], v99
	v_pk_add_f32 v[74:75], v[74:75], 1.0 op_sel_hi:[1,0]
	v_pk_add_f32 v[78:79], v[78:79], 1.0 op_sel_hi:[1,0]
	v_exp_f32_e32 v80, v80
	v_exp_f32_e32 v81, v81
	v_pk_add_f32 v[76:77], v[76:77], 1.0 op_sel_hi:[1,0]
	v_pk_mul_f32 v[66:67], v[66:67], s[34:35] op_sel_hi:[1,0]
	v_exp_f32_e32 v70, v70
	v_exp_f32_e32 v71, v71
	v_pk_mul_f32 v[68:69], v[68:69], s[34:35] op_sel_hi:[1,0]
	v_pk_mul_f32 v[72:73], v[72:73], s[34:35] op_sel_hi:[1,0]
	v_rcp_f32_e32 v74, v74
	v_rcp_f32_e32 v75, v75
	v_rcp_f32_e32 v78, v78
	v_rcp_f32_e32 v79, v79
	v_rcp_f32_e32 v76, v76
	v_rcp_f32_e32 v77, v77
	v_exp_f32_e32 v66, v66
	v_exp_f32_e32 v67, v67
	v_exp_f32_e32 v68, v68
	v_exp_f32_e32 v69, v69
	v_exp_f32_e32 v72, v72
	v_exp_f32_e32 v73, v73
	s_waitcnt lgkmcnt(1)
	v_lshlrev_b32_e32 v198, 16, v182
	v_and_b32_e32 v199, 0xffff0000, v182
	v_lshlrev_b32_e32 v182, 16, v183
	v_and_b32_e32 v183, 0xffff0000, v183
	v_lshlrev_b32_e32 v200, 16, v184
	v_and_b32_e32 v201, 0xffff0000, v184
	v_cvt_pk_f32_fp8_sdwa v[98:99], v99 src0_sel:WORD_1
	v_pk_add_f32 v[80:81], v[80:81], 1.0 op_sel_hi:[1,0]
	v_pk_mul_f32 v[204:205], v[204:205], s[36:37] op_sel_hi:[1,0]
	v_pk_mul_f32 v[202:203], v[202:203], s[36:37] op_sel_hi:[1,0]
	v_pk_mul_f32 v[206:207], v[206:207], s[36:37] op_sel_hi:[1,0]
	v_pk_add_f32 v[70:71], v[70:71], 1.0 op_sel_hi:[1,0]
	v_rcp_f32_e32 v80, v80
	v_rcp_f32_e32 v81, v81
	v_pk_fma_f32 v[74:75], v[74:75], v[202:203], v[198:199]
	v_pk_fma_f32 v[76:77], v[76:77], v[204:205], v[182:183]
	v_pk_fma_f32 v[78:79], v[78:79], v[206:207], v[200:201]
	v_cvt_pk_f32_fp8_e32 v[200:201], v100
	v_cvt_pk_f32_fp8_sdwa v[202:203], v100 src0_sel:WORD_1
	v_cvt_pk_f32_fp8_e32 v[204:205], v101
	v_cvt_pk_f32_fp8_sdwa v[100:101], v101 src0_sel:WORD_1
	v_pk_add_f32 v[66:67], v[66:67], 1.0 op_sel_hi:[1,0]
	v_rcp_f32_e32 v206, v70
	v_rcp_f32_e32 v207, v71
	v_pk_add_f32 v[68:69], v[68:69], 1.0 op_sel_hi:[1,0]
	v_pk_add_f32 v[70:71], v[72:73], 1.0 op_sel_hi:[1,0]
	v_rcp_f32_e32 v66, v66
	v_rcp_f32_e32 v67, v67
	v_rcp_f32_e32 v68, v68
	v_rcp_f32_e32 v69, v69
	v_rcp_f32_e32 v208, v70
	v_rcp_f32_e32 v209, v71
	v_lshlrev_b32_e32 v184, 16, v185
	v_and_b32_e32 v185, 0xffff0000, v185
	v_pk_mul_f32 v[98:99], v[98:99], s[36:37] op_sel_hi:[1,0]
	v_cvt_pk_bf16_f32 v182, v74, v75
	v_cvt_pk_bf16_f32 v183, v76, v77
	s_waitcnt lgkmcnt(0)
	v_lshlrev_b32_e32 v198, 16, v196
	v_pk_fma_f32 v[80:81], v[80:81], v[98:99], v[184:185]
	v_cvt_pk_bf16_f32 v184, v78, v79
	v_lshlrev_b32_e32 v98, 16, v194
	v_cvt_pk_bf16_f32 v185, v80, v81
	v_and_b32_e32 v99, 0xffff0000, v194
	v_lshlrev_b32_e32 v194, 16, v195
	v_and_b32_e32 v195, 0xffff0000, v195
	v_and_b32_e32 v199, 0xffff0000, v196
	v_lshlrev_b32_e32 v196, 16, v197
	v_and_b32_e32 v197, 0xffff0000, v197
	v_pk_mul_f32 v[72:73], v[202:203], s[36:37] op_sel_hi:[1,0]
	v_pk_mul_f32 v[70:71], v[200:201], s[36:37] op_sel_hi:[1,0]
	v_pk_mul_f32 v[100:101], v[100:101], s[36:37] op_sel_hi:[1,0]
	v_pk_mul_f32 v[200:201], v[204:205], s[36:37] op_sel_hi:[1,0]
	v_pk_fma_f32 v[70:71], v[66:67], v[70:71], v[98:99]
	v_pk_fma_f32 v[72:73], v[68:69], v[72:73], v[194:195]
	v_pk_fma_f32 v[98:99], v[206:207], v[200:201], v[198:199]
	v_pk_fma_f32 v[100:101], v[208:209], v[100:101], v[196:197]
	v_cvt_pk_bf16_f32 v66, v70, v71
	v_cvt_pk_bf16_f32 v67, v72, v73
	v_cvt_pk_bf16_f32 v68, v98, v99
	s_add_u32 s41, s66, s60
	v_cvt_pk_bf16_f32 v69, v100, v101
	ds_write_b128 v181, v[182:185]
	ds_write_b128 v181, v[66:69] offset:64
	s_addc_u32 s47, s67, s61
	ds_read_b128 v[66:69], v180
	ds_read_b128 v[182:185], v180 offset:1152
	s_add_u32 s60, s41, s48
	s_addc_u32 s61, s47, s49
	v_lshl_add_u64 v[194:195], s[60:61], 0, v[166:167]
	v_lshl_add_u64 v[194:195], v[194:195], 0, v[164:165]
	s_waitcnt lgkmcnt(1)
	global_store_dwordx4 v[194:195], v[66:69], off
	v_pk_fma_f32 v[58:59], v[58:59], s[30:31], v[14:15] op_sel_hi:[1,0,1]
	v_pk_fma_f32 v[62:63], v[62:63], s[30:31], v[10:11] op_sel_hi:[1,0,1]
	v_lshl_add_u64 v[66:67], s[60:61], 0, v[168:169]
	s_add_i32 s60, s50, 0xa0
	s_ashr_i32 s61, s60, 31
	s_lshl_b64 s[60:61], s[60:61], 11
	s_add_u32 s41, s64, s60
	s_addc_u32 s47, s65, s61
	s_add_u32 s62, s41, s48
	v_lshl_add_u64 v[66:67], v[66:67], 0, v[164:165]
	s_addc_u32 s63, s47, s49
	s_waitcnt lgkmcnt(0)
	global_store_dwordx4 v[66:67], v[182:185], off
	v_lshl_add_u64 v[66:67], s[62:63], 0, v[166:167]
	v_pk_fma_f32 v[60:61], v[60:61], s[30:31], v[16:17] op_sel_hi:[1,0,1]
	v_lshl_add_u64 v[182:183], v[66:67], 0, v[164:165]
	global_load_dwordx4 v[66:69], v[174:175], off offset:2048 nt
	s_nop 0
	global_load_dwordx4 v[182:185], v[182:183], off nt
	s_waitcnt vmcnt(5)
	ds_write_b128 v180, v[186:189]
	s_waitcnt vmcnt(4)
	ds_write_b128 v180, v[190:193] offset:1152
	v_lshl_add_u64 v[190:191], s[62:63], 0, v[168:169]
	v_lshl_add_u64 v[190:191], v[190:191], 0, v[164:165]
	global_load_dwordx4 v[190:193], v[190:191], off nt
	v_pk_mul_f32 v[58:59], v[58:59], s[34:35] op_sel_hi:[1,0]
	v_pk_mul_f32 v[62:63], v[62:63], s[34:35] op_sel_hi:[1,0]
	v_pk_mul_f32 v[60:61], v[60:61], s[34:35] op_sel_hi:[1,0]
	v_exp_f32_e32 v58, v58
	v_exp_f32_e32 v59, v59
	v_exp_f32_e32 v62, v62
	v_exp_f32_e32 v63, v63
	v_exp_f32_e32 v60, v60
	v_exp_f32_e32 v61, v61
	v_pk_fma_f32 v[64:65], v[64:65], s[30:31], v[12:13] op_sel_hi:[1,0,1]
	v_pk_fma_f32 v[54:55], v[54:55], s[30:31], v[2:3] op_sel_hi:[1,0,1]
	ds_read_b128 v[186:189], v181
	ds_read_b128 v[194:197], v181 offset:64
	v_pk_mul_f32 v[64:65], v[64:65], s[34:35] op_sel_hi:[1,0]
	v_pk_fma_f32 v[50:51], v[50:51], s[30:31], v[6:7] op_sel_hi:[1,0,1]
	v_pk_mul_f32 v[54:55], v[54:55], s[34:35] op_sel_hi:[1,0]
	v_pk_fma_f32 v[52:53], v[52:53], s[30:31], v[8:9] op_sel_hi:[1,0,1]
	v_pk_fma_f32 v[56:57], v[56:57], s[30:31], v[4:5] op_sel_hi:[1,0,1]
	v_cvt_pk_f32_fp8_e32 v[202:203], v82
	v_cvt_pk_f32_fp8_sdwa v[204:205], v82 src0_sel:WORD_1
	v_cvt_pk_f32_fp8_e32 v[206:207], v83
	v_pk_add_f32 v[58:59], v[58:59], 1.0 op_sel_hi:[1,0]
	v_pk_add_f32 v[62:63], v[62:63], 1.0 op_sel_hi:[1,0]
	v_exp_f32_e32 v64, v64
	v_exp_f32_e32 v65, v65
	v_pk_add_f32 v[60:61], v[60:61], 1.0 op_sel_hi:[1,0]
	v_pk_mul_f32 v[50:51], v[50:51], s[34:35] op_sel_hi:[1,0]
	v_exp_f32_e32 v54, v54
	v_exp_f32_e32 v55, v55
	v_pk_mul_f32 v[52:53], v[52:53], s[34:35] op_sel_hi:[1,0]
	v_pk_mul_f32 v[56:57], v[56:57], s[34:35] op_sel_hi:[1,0]
	v_rcp_f32_e32 v58, v58
	v_rcp_f32_e32 v59, v59
	v_rcp_f32_e32 v62, v62
	v_rcp_f32_e32 v63, v63
	v_rcp_f32_e32 v60, v60
	v_rcp_f32_e32 v61, v61
	v_exp_f32_e32 v50, v50
	v_exp_f32_e32 v51, v51
	v_exp_f32_e32 v52, v52
	v_exp_f32_e32 v53, v53
	v_exp_f32_e32 v56, v56
	v_exp_f32_e32 v57, v57
	s_waitcnt lgkmcnt(1)
	v_lshlrev_b32_e32 v198, 16, v186
	v_and_b32_e32 v199, 0xffff0000, v186
	v_lshlrev_b32_e32 v186, 16, v187
	v_and_b32_e32 v187, 0xffff0000, v187
	v_lshlrev_b32_e32 v200, 16, v188
	v_and_b32_e32 v201, 0xffff0000, v188
	v_cvt_pk_f32_fp8_sdwa v[82:83], v83 src0_sel:WORD_1
	v_pk_add_f32 v[64:65], v[64:65], 1.0 op_sel_hi:[1,0]
	v_pk_mul_f32 v[204:205], v[204:205], s[36:37] op_sel_hi:[1,0]
	v_pk_mul_f32 v[202:203], v[202:203], s[36:37] op_sel_hi:[1,0]
	v_pk_mul_f32 v[206:207], v[206:207], s[36:37] op_sel_hi:[1,0]
	v_pk_add_f32 v[54:55], v[54:55], 1.0 op_sel_hi:[1,0]
	v_rcp_f32_e32 v64, v64
	v_rcp_f32_e32 v65, v65
	v_pk_fma_f32 v[58:59], v[58:59], v[202:203], v[198:199]
	v_pk_fma_f32 v[60:61], v[60:61], v[204:205], v[186:187]
	v_pk_fma_f32 v[62:63], v[62:63], v[206:207], v[200:201]
	v_cvt_pk_f32_fp8_e32 v[200:201], v84
	v_cvt_pk_f32_fp8_sdwa v[202:203], v84 src0_sel:WORD_1
	v_cvt_pk_f32_fp8_e32 v[204:205], v85
	v_cvt_pk_f32_fp8_sdwa v[84:85], v85 src0_sel:WORD_1
	v_pk_add_f32 v[50:51], v[50:51], 1.0 op_sel_hi:[1,0]
	v_rcp_f32_e32 v206, v54
	v_rcp_f32_e32 v207, v55
	v_pk_add_f32 v[52:53], v[52:53], 1.0 op_sel_hi:[1,0]
	v_pk_add_f32 v[54:55], v[56:57], 1.0 op_sel_hi:[1,0]
	v_rcp_f32_e32 v50, v50
	v_rcp_f32_e32 v51, v51
	v_rcp_f32_e32 v52, v52
	v_rcp_f32_e32 v53, v53
	v_rcp_f32_e32 v208, v54
	v_rcp_f32_e32 v209, v55
	v_lshlrev_b32_e32 v188, 16, v189
	v_and_b32_e32 v189, 0xffff0000, v189
	v_pk_mul_f32 v[82:83], v[82:83], s[36:37] op_sel_hi:[1,0]
	s_add_u32 s41, s66, s58
	v_pk_fma_f32 v[64:65], v[64:65], v[82:83], v[188:189]
	v_cvt_pk_bf16_f32 v186, v58, v59
	v_cvt_pk_bf16_f32 v187, v60, v61
	v_cvt_pk_bf16_f32 v188, v62, v63
	s_waitcnt lgkmcnt(0)
	v_lshlrev_b32_e32 v82, 16, v194
	v_cvt_pk_bf16_f32 v189, v64, v65
	v_and_b32_e32 v83, 0xffff0000, v194
	v_lshlrev_b32_e32 v194, 16, v195
	v_and_b32_e32 v195, 0xffff0000, v195
	v_lshlrev_b32_e32 v198, 16, v196
	v_and_b32_e32 v199, 0xffff0000, v196
	v_lshlrev_b32_e32 v196, 16, v197
	v_and_b32_e32 v197, 0xffff0000, v197
	v_pk_mul_f32 v[56:57], v[202:203], s[36:37] op_sel_hi:[1,0]
	v_pk_mul_f32 v[54:55], v[200:201], s[36:37] op_sel_hi:[1,0]
	v_pk_mul_f32 v[84:85], v[84:85], s[36:37] op_sel_hi:[1,0]
	v_pk_mul_f32 v[200:201], v[204:205], s[36:37] op_sel_hi:[1,0]
	s_addc_u32 s47, s67, s59
	v_pk_fma_f32 v[54:55], v[50:51], v[54:55], v[82:83]
	v_pk_fma_f32 v[56:57], v[52:53], v[56:57], v[194:195]
	v_pk_fma_f32 v[82:83], v[206:207], v[200:201], v[198:199]
	v_pk_fma_f32 v[84:85], v[208:209], v[84:85], v[196:197]
	v_cvt_pk_bf16_f32 v50, v54, v55
	v_cvt_pk_bf16_f32 v51, v56, v57
	v_cvt_pk_bf16_f32 v52, v82, v83
	s_add_u32 s58, s41, s48
	v_cvt_pk_bf16_f32 v53, v84, v85
	ds_write_b128 v181, v[186:189]
	ds_write_b128 v181, v[50:53] offset:64
	ds_read_b128 v[50:53], v180
	ds_read_b128 v[186:189], v180 offset:1152
	s_addc_u32 s59, s47, s49
	s_addk_i32 s50, 0xb0
	s_ashr_i32 s51, s50, 31
	s_lshl_b64 s[50:51], s[50:51], 11
	v_lshl_add_u64 v[194:195], s[58:59], 0, v[166:167]
	s_add_u32 s41, s64, s50
	v_lshl_add_u64 v[194:195], v[194:195], 0, v[164:165]
	s_addc_u32 s47, s65, s51
	s_waitcnt lgkmcnt(1)
	global_store_dwordx4 v[194:195], v[50:53], off
	v_pk_fma_f32 v[42:43], v[42:43], s[30:31], v[14:15] op_sel_hi:[1,0,1]
	v_pk_fma_f32 v[46:47], v[46:47], s[30:31], v[10:11] op_sel_hi:[1,0,1]
	v_lshl_add_u64 v[50:51], s[58:59], 0, v[168:169]
	s_add_u32 s58, s41, s48
	v_lshl_add_u64 v[50:51], v[50:51], 0, v[164:165]
	s_addc_u32 s59, s47, s49
	s_waitcnt lgkmcnt(0)
	global_store_dwordx4 v[50:51], v[186:189], off
	v_lshl_add_u64 v[50:51], s[58:59], 0, v[166:167]
	v_pk_fma_f32 v[44:45], v[44:45], s[30:31], v[16:17] op_sel_hi:[1,0,1]
	v_lshl_add_u64 v[186:187], v[50:51], 0, v[164:165]
	global_load_dwordx4 v[50:53], v[174:175], off offset:3072 nt
	s_nop 0
	global_load_dwordx4 v[186:189], v[186:187], off nt
	v_lshl_add_u64 v[174:175], s[58:59], 0, v[168:169]
	s_waitcnt vmcnt(5)
	ds_write_b128 v180, v[182:185]
	s_waitcnt vmcnt(4)
	ds_write_b128 v180, v[190:193] offset:1152
	v_lshl_add_u64 v[174:175], v[174:175], 0, v[164:165]
	global_load_dwordx4 v[190:193], v[174:175], off nt
	v_pk_mul_f32 v[42:43], v[42:43], s[34:35] op_sel_hi:[1,0]
	v_pk_mul_f32 v[46:47], v[46:47], s[34:35] op_sel_hi:[1,0]
	v_pk_mul_f32 v[44:45], v[44:45], s[34:35] op_sel_hi:[1,0]
	v_exp_f32_e32 v42, v42
	v_exp_f32_e32 v43, v43
	v_exp_f32_e32 v46, v46
	v_exp_f32_e32 v47, v47
	v_exp_f32_e32 v44, v44
	v_exp_f32_e32 v45, v45
	v_pk_fma_f32 v[48:49], v[48:49], s[30:31], v[12:13] op_sel_hi:[1,0,1]
	ds_read_b128 v[182:185], v181
	ds_read_b128 v[194:197], v181 offset:64
	v_pk_mul_f32 v[48:49], v[48:49], s[34:35] op_sel_hi:[1,0]
	v_pk_fma_f32 v[34:35], v[34:35], s[30:31], v[6:7] op_sel_hi:[1,0,1]
	v_pk_fma_f32 v[38:39], v[38:39], s[30:31], v[2:3] op_sel_hi:[1,0,1]
	v_pk_fma_f32 v[36:37], v[36:37], s[30:31], v[8:9] op_sel_hi:[1,0,1]
	v_pk_fma_f32 v[40:41], v[40:41], s[30:31], v[4:5] op_sel_hi:[1,0,1]
	v_cvt_pk_f32_fp8_e32 v[200:201], v66
	v_cvt_pk_f32_fp8_sdwa v[202:203], v66 src0_sel:WORD_1
	v_cvt_pk_f32_fp8_e32 v[204:205], v67
	v_pk_add_f32 v[42:43], v[42:43], 1.0 op_sel_hi:[1,0]
	v_pk_add_f32 v[46:47], v[46:47], 1.0 op_sel_hi:[1,0]
	v_exp_f32_e32 v48, v48
	v_exp_f32_e32 v49, v49
	v_pk_add_f32 v[44:45], v[44:45], 1.0 op_sel_hi:[1,0]
	v_pk_mul_f32 v[34:35], v[34:35], s[34:35] op_sel_hi:[1,0]
	v_pk_mul_f32 v[38:39], v[38:39], s[34:35] op_sel_hi:[1,0]
	v_pk_mul_f32 v[36:37], v[36:37], s[34:35] op_sel_hi:[1,0]
	v_pk_mul_f32 v[40:41], v[40:41], s[34:35] op_sel_hi:[1,0]
	v_rcp_f32_e32 v42, v42
	v_rcp_f32_e32 v43, v43
	v_rcp_f32_e32 v46, v46
	v_rcp_f32_e32 v47, v47
	v_rcp_f32_e32 v44, v44
	v_rcp_f32_e32 v45, v45
	v_exp_f32_e32 v34, v34
	v_exp_f32_e32 v35, v35
	v_exp_f32_e32 v38, v38
	v_exp_f32_e32 v39, v39
	v_exp_f32_e32 v36, v36
	v_exp_f32_e32 v37, v37
	v_exp_f32_e32 v40, v40
	v_exp_f32_e32 v41, v41
	s_waitcnt lgkmcnt(1)
	v_lshlrev_b32_e32 v174, 16, v182
	v_and_b32_e32 v175, 0xffff0000, v182
	v_lshlrev_b32_e32 v182, 16, v183
	v_and_b32_e32 v183, 0xffff0000, v183
	v_lshlrev_b32_e32 v198, 16, v184
	v_and_b32_e32 v199, 0xffff0000, v184
	v_cvt_pk_f32_fp8_sdwa v[66:67], v67 src0_sel:WORD_1
	v_pk_add_f32 v[48:49], v[48:49], 1.0 op_sel_hi:[1,0]
	v_pk_mul_f32 v[202:203], v[202:203], s[36:37] op_sel_hi:[1,0]
	v_pk_mul_f32 v[200:201], v[200:201], s[36:37] op_sel_hi:[1,0]
	v_pk_mul_f32 v[204:205], v[204:205], s[36:37] op_sel_hi:[1,0]
	v_rcp_f32_e32 v48, v48
	v_rcp_f32_e32 v49, v49
	v_pk_fma_f32 v[42:43], v[42:43], v[200:201], v[174:175]
	v_pk_fma_f32 v[44:45], v[44:45], v[202:203], v[182:183]
	v_pk_fma_f32 v[46:47], v[46:47], v[204:205], v[198:199]
	v_cvt_pk_f32_fp8_e32 v[198:199], v68
	v_cvt_pk_f32_fp8_sdwa v[200:201], v68 src0_sel:WORD_1
	v_cvt_pk_f32_fp8_e32 v[202:203], v69
	v_cvt_pk_f32_fp8_sdwa v[68:69], v69 src0_sel:WORD_1
	v_pk_add_f32 v[34:35], v[34:35], 1.0 op_sel_hi:[1,0]
	v_pk_add_f32 v[38:39], v[38:39], 1.0 op_sel_hi:[1,0]
	v_pk_add_f32 v[36:37], v[36:37], 1.0 op_sel_hi:[1,0]
	v_pk_add_f32 v[40:41], v[40:41], 1.0 op_sel_hi:[1,0]
	v_rcp_f32_e32 v34, v34
	v_rcp_f32_e32 v35, v35
	v_rcp_f32_e32 v38, v38
	v_rcp_f32_e32 v39, v39
	v_rcp_f32_e32 v36, v36
	v_rcp_f32_e32 v37, v37
	v_rcp_f32_e32 v40, v40
	v_rcp_f32_e32 v41, v41
	v_lshlrev_b32_e32 v184, 16, v185
	v_and_b32_e32 v185, 0xffff0000, v185
	v_pk_mul_f32 v[66:67], v[66:67], s[36:37] op_sel_hi:[1,0]
	v_cvt_pk_bf16_f32 v182, v42, v43
	v_cvt_pk_bf16_f32 v183, v44, v45
	s_waitcnt lgkmcnt(0)
	v_lshlrev_b32_e32 v174, 16, v195
	v_pk_fma_f32 v[48:49], v[48:49], v[66:67], v[184:185]
	v_cvt_pk_bf16_f32 v184, v46, v47
	v_lshlrev_b32_e32 v66, 16, v194
	v_cvt_pk_bf16_f32 v185, v48, v49
	v_and_b32_e32 v67, 0xffff0000, v194
	v_and_b32_e32 v175, 0xffff0000, v195
	v_lshlrev_b32_e32 v194, 16, v196
	v_and_b32_e32 v195, 0xffff0000, v196
	v_lshlrev_b32_e32 v196, 16, v197
	v_and_b32_e32 v197, 0xffff0000, v197
	v_pk_mul_f32 v[200:201], v[200:201], s[36:37] op_sel_hi:[1,0]
	v_pk_mul_f32 v[198:199], v[198:199], s[36:37] op_sel_hi:[1,0]
	v_pk_mul_f32 v[68:69], v[68:69], s[36:37] op_sel_hi:[1,0]
	v_pk_mul_f32 v[202:203], v[202:203], s[36:37] op_sel_hi:[1,0]
	v_pk_fma_f32 v[34:35], v[34:35], v[198:199], v[66:67]
	v_pk_fma_f32 v[36:37], v[36:37], v[200:201], v[174:175]
	v_pk_fma_f32 v[38:39], v[38:39], v[202:203], v[194:195]
	v_pk_fma_f32 v[40:41], v[40:41], v[68:69], v[196:197]
	v_cvt_pk_bf16_f32 v66, v34, v35
	v_cvt_pk_bf16_f32 v67, v36, v37
	v_cvt_pk_bf16_f32 v68, v38, v39
	s_add_u32 s41, s66, s60
	v_cvt_pk_bf16_f32 v69, v40, v41
	ds_write_b128 v181, v[182:185]
	ds_write_b128 v181, v[66:69] offset:64
	s_addc_u32 s47, s67, s61
	ds_read_b128 v[66:69], v180
	ds_read_b128 v[182:185], v180 offset:1152
	s_add_u32 s58, s41, s48
	s_addc_u32 s59, s47, s49
	v_lshl_add_u64 v[174:175], s[58:59], 0, v[166:167]
	v_pk_fma_f32 v[14:15], v[26:27], s[30:31], v[14:15] op_sel_hi:[1,0,1]
	v_pk_fma_f32 v[10:11], v[30:31], s[30:31], v[10:11] op_sel_hi:[1,0,1]
	v_pk_fma_f32 v[16:17], v[28:29], s[30:31], v[16:17] op_sel_hi:[1,0,1]
	v_pk_fma_f32 v[12:13], v[32:33], s[30:31], v[12:13] op_sel_hi:[1,0,1]
	v_lshl_add_u64 v[174:175], v[174:175], 0, v[164:165]
	v_pk_mul_f32 v[14:15], v[14:15], s[34:35] op_sel_hi:[1,0]
	v_pk_mul_f32 v[10:11], v[10:11], s[34:35] op_sel_hi:[1,0]
	v_pk_mul_f32 v[16:17], v[16:17], s[34:35] op_sel_hi:[1,0]
	v_pk_mul_f32 v[12:13], v[12:13], s[34:35] op_sel_hi:[1,0]
	s_waitcnt lgkmcnt(1)
	global_store_dwordx4 v[174:175], v[66:69], off
	v_exp_f32_e32 v14, v14
	v_exp_f32_e32 v15, v15
	v_lshl_add_u64 v[66:67], s[58:59], 0, v[168:169]
	v_exp_f32_e32 v10, v10
	v_exp_f32_e32 v11, v11
	v_exp_f32_e32 v16, v16
	v_exp_f32_e32 v17, v17
	v_exp_f32_e32 v12, v12
	v_exp_f32_e32 v13, v13
	v_lshl_add_u64 v[66:67], v[66:67], 0, v[164:165]
	s_waitcnt lgkmcnt(0)
	global_store_dwordx4 v[66:67], v[182:185], off
	s_waitcnt vmcnt(3)
	ds_write_b128 v180, v[186:189]
	s_waitcnt vmcnt(2)
	ds_write_b128 v180, v[190:193] offset:1152
	v_pk_fma_f32 v[6:7], v[18:19], s[30:31], v[6:7] op_sel_hi:[1,0,1]
	v_pk_fma_f32 v[2:3], v[22:23], s[30:31], v[2:3] op_sel_hi:[1,0,1]
	v_pk_fma_f32 v[8:9], v[20:21], s[30:31], v[8:9] op_sel_hi:[1,0,1]
	v_pk_fma_f32 v[4:5], v[24:25], s[30:31], v[4:5] op_sel_hi:[1,0,1]
	ds_read_b128 v[66:69], v181
	ds_read_b128 v[182:185], v181 offset:64
	v_cvt_pk_f32_fp8_e32 v[188:189], v50
	v_cvt_pk_f32_fp8_sdwa v[190:191], v50 src0_sel:WORD_1
	v_cvt_pk_f32_fp8_e32 v[192:193], v51
	v_cvt_pk_f32_fp8_sdwa v[50:51], v51 src0_sel:WORD_1
	v_pk_add_f32 v[14:15], v[14:15], 1.0 op_sel_hi:[1,0]
	v_pk_add_f32 v[10:11], v[10:11], 1.0 op_sel_hi:[1,0]
	v_pk_add_f32 v[16:17], v[16:17], 1.0 op_sel_hi:[1,0]
	v_pk_add_f32 v[12:13], v[12:13], 1.0 op_sel_hi:[1,0]
	v_pk_mul_f32 v[6:7], v[6:7], s[34:35] op_sel_hi:[1,0]
	v_pk_mul_f32 v[2:3], v[2:3], s[34:35] op_sel_hi:[1,0]
	v_pk_mul_f32 v[8:9], v[8:9], s[34:35] op_sel_hi:[1,0]
	v_pk_mul_f32 v[4:5], v[4:5], s[34:35] op_sel_hi:[1,0]
	v_rcp_f32_e32 v14, v14
	v_rcp_f32_e32 v15, v15
	v_rcp_f32_e32 v10, v10
	v_rcp_f32_e32 v11, v11
	v_rcp_f32_e32 v16, v16
	v_rcp_f32_e32 v17, v17
	v_rcp_f32_e32 v12, v12
	v_rcp_f32_e32 v13, v13
	v_exp_f32_e32 v6, v6
	v_exp_f32_e32 v7, v7
	v_exp_f32_e32 v2, v2
	v_exp_f32_e32 v3, v3
	v_exp_f32_e32 v8, v8
	v_exp_f32_e32 v9, v9
	v_exp_f32_e32 v4, v4
	v_exp_f32_e32 v5, v5
	s_waitcnt lgkmcnt(1)
	v_lshlrev_b32_e32 v174, 16, v66
	v_and_b32_e32 v175, 0xffff0000, v66
	v_lshlrev_b32_e32 v66, 16, v67
	v_and_b32_e32 v67, 0xffff0000, v67
	v_lshlrev_b32_e32 v186, 16, v68
	v_and_b32_e32 v187, 0xffff0000, v68
	v_lshlrev_b32_e32 v68, 16, v69
	v_and_b32_e32 v69, 0xffff0000, v69
	v_pk_mul_f32 v[26:27], v[190:191], s[36:37] op_sel_hi:[1,0]
	v_pk_mul_f32 v[28:29], v[188:189], s[36:37] op_sel_hi:[1,0]
	v_pk_mul_f32 v[30:31], v[50:51], s[36:37] op_sel_hi:[1,0]
	v_pk_mul_f32 v[32:33], v[192:193], s[36:37] op_sel_hi:[1,0]
	v_pk_fma_f32 v[14:15], v[14:15], v[28:29], v[174:175]
	v_pk_fma_f32 v[16:17], v[16:17], v[26:27], v[66:67]
	v_pk_fma_f32 v[26:27], v[10:11], v[32:33], v[186:187]
	v_pk_fma_f32 v[28:29], v[12:13], v[30:31], v[68:69]
	s_waitcnt lgkmcnt(0)
	v_lshlrev_b32_e32 v30, 16, v182
	v_and_b32_e32 v31, 0xffff0000, v182
	v_lshlrev_b32_e32 v32, 16, v183
	v_and_b32_e32 v33, 0xffff0000, v183
	v_cvt_pk_f32_fp8_e32 v[68:69], v52
	v_cvt_pk_f32_fp8_sdwa v[174:175], v52 src0_sel:WORD_1
	v_cvt_pk_f32_fp8_e32 v[182:183], v53
	v_cvt_pk_f32_fp8_sdwa v[52:53], v53 src0_sel:WORD_1
	v_pk_add_f32 v[6:7], v[6:7], 1.0 op_sel_hi:[1,0]
	v_pk_add_f32 v[2:3], v[2:3], 1.0 op_sel_hi:[1,0]
	v_pk_add_f32 v[8:9], v[8:9], 1.0 op_sel_hi:[1,0]
	v_pk_add_f32 v[4:5], v[4:5], 1.0 op_sel_hi:[1,0]
	v_rcp_f32_e32 v6, v6
	v_rcp_f32_e32 v7, v7
	v_rcp_f32_e32 v2, v2
	v_rcp_f32_e32 v3, v3
	v_rcp_f32_e32 v8, v8
	v_rcp_f32_e32 v9, v9
	v_rcp_f32_e32 v4, v4
	v_rcp_f32_e32 v5, v5
	v_cvt_pk_bf16_f32 v10, v14, v15
	v_cvt_pk_bf16_f32 v11, v16, v17
	v_cvt_pk_bf16_f32 v12, v26, v27
	v_cvt_pk_bf16_f32 v13, v28, v29
	v_lshlrev_b32_e32 v50, 16, v184
	v_and_b32_e32 v51, 0xffff0000, v184
	v_lshlrev_b32_e32 v66, 16, v185
	v_and_b32_e32 v67, 0xffff0000, v185
	v_pk_mul_f32 v[18:19], v[174:175], s[36:37] op_sel_hi:[1,0]
	v_pk_mul_f32 v[20:21], v[68:69], s[36:37] op_sel_hi:[1,0]
	v_pk_mul_f32 v[22:23], v[52:53], s[36:37] op_sel_hi:[1,0]
	v_pk_mul_f32 v[24:25], v[182:183], s[36:37] op_sel_hi:[1,0]
	v_pk_fma_f32 v[20:21], v[6:7], v[20:21], v[30:31]
	v_pk_fma_f32 v[18:19], v[8:9], v[18:19], v[32:33]
	v_pk_fma_f32 v[24:25], v[2:3], v[24:25], v[50:51]
	v_pk_fma_f32 v[22:23], v[4:5], v[22:23], v[66:67]
	v_cvt_pk_bf16_f32 v2, v20, v21
	v_cvt_pk_bf16_f32 v3, v18, v19
	v_cvt_pk_bf16_f32 v4, v24, v25
	s_add_u32 s41, s66, s50
	v_cvt_pk_bf16_f32 v5, v22, v23
	ds_write_b128 v181, v[10:13]
	ds_write_b128 v181, v[2:5] offset:64
	s_addc_u32 s47, s67, s51
	ds_read_b128 v[2:5], v180
	ds_read_b128 v[6:9], v180 offset:1152
	s_add_u32 s48, s41, s48
	s_addc_u32 s49, s47, s49
	v_lshl_add_u64 v[10:11], s[48:49], 0, v[166:167]
	v_lshl_add_u64 v[10:11], v[10:11], 0, v[164:165]
	s_waitcnt lgkmcnt(1)
	global_store_dwordx4 v[10:11], v[2:5], off
	v_mul_f32_e32 v10, v103, v103
	v_fmac_f32_e32 v10, v102, v102
	v_lshl_add_u64 v[2:3], s[48:49], 0, v[168:169]
	v_lshl_add_u64 v[2:3], v[2:3], 0, v[164:165]
	s_waitcnt lgkmcnt(0)
	global_store_dwordx4 v[2:3], v[6:9], off
	v_mul_f32_e32 v2, v27, v27
	v_mul_f32_e32 v3, v29, v29
	v_fmac_f32_e32 v2, v26, v26
	v_fmac_f32_e32 v3, v28, v28
	v_add_f32_e32 v2, v2, v3
	v_mul_f32_e32 v3, v15, v15
	v_mul_f32_e32 v4, v17, v17
	v_fmac_f32_e32 v3, v14, v14
	v_fmac_f32_e32 v4, v16, v16
	v_add_f32_e32 v3, v3, v4
	v_add_f32_e32 v2, v3, v2
	v_mul_f32_e32 v3, v25, v25
	v_mul_f32_e32 v4, v23, v23
	v_fmac_f32_e32 v3, v24, v24
	v_fmac_f32_e32 v4, v22, v22
	v_add_f32_e32 v3, v3, v4
	v_mul_f32_e32 v4, v21, v21
	v_mul_f32_e32 v5, v19, v19
	v_fmac_f32_e32 v4, v20, v20
	v_fmac_f32_e32 v5, v18, v18
	v_add_f32_e32 v4, v4, v5
	v_add_f32_e32 v3, v4, v3
	v_add_f32_e32 v2, v2, v3
	v_mul_f32_e32 v3, v47, v47
	v_mul_f32_e32 v4, v49, v49
	v_fmac_f32_e32 v3, v46, v46
	v_fmac_f32_e32 v4, v48, v48
	v_add_f32_e32 v3, v3, v4
	v_mul_f32_e32 v4, v43, v43
	v_mul_f32_e32 v5, v45, v45
	v_fmac_f32_e32 v4, v42, v42
	v_fmac_f32_e32 v5, v44, v44
	v_add_f32_e32 v4, v4, v5
	v_add_f32_e32 v3, v4, v3
	v_mul_f32_e32 v4, v39, v39
	v_mul_f32_e32 v5, v41, v41
	v_fmac_f32_e32 v4, v38, v38
	v_fmac_f32_e32 v5, v40, v40
	v_add_f32_e32 v4, v4, v5
	v_mul_f32_e32 v5, v35, v35
	v_mul_f32_e32 v6, v37, v37
	v_fmac_f32_e32 v5, v34, v34
	v_fmac_f32_e32 v6, v36, v36
	v_add_f32_e32 v5, v5, v6
	v_add_f32_e32 v4, v5, v4
	v_add_f32_e32 v3, v3, v4
	v_mul_f32_e32 v4, v63, v63
	v_mul_f32_e32 v5, v65, v65
	v_fmac_f32_e32 v4, v62, v62
	v_fmac_f32_e32 v5, v64, v64
	v_add_f32_e32 v4, v4, v5
	v_mul_f32_e32 v5, v59, v59
	v_mul_f32_e32 v6, v61, v61
	v_fmac_f32_e32 v5, v58, v58
	v_fmac_f32_e32 v6, v60, v60
	v_add_f32_e32 v5, v5, v6
	v_add_f32_e32 v4, v5, v4
	v_mul_f32_e32 v5, v83, v83
	v_mul_f32_e32 v6, v85, v85
	v_fmac_f32_e32 v5, v82, v82
	v_fmac_f32_e32 v6, v84, v84
	v_add_f32_e32 v5, v5, v6
	v_mul_f32_e32 v6, v55, v55
	v_mul_f32_e32 v7, v57, v57
	v_fmac_f32_e32 v6, v54, v54
	v_fmac_f32_e32 v7, v56, v56
	v_add_f32_e32 v6, v6, v7
	v_add_f32_e32 v5, v6, v5
	v_add_f32_e32 v4, v4, v5
	v_mul_f32_e32 v5, v79, v79
	v_mul_f32_e32 v6, v81, v81
	v_fmac_f32_e32 v5, v78, v78
	v_fmac_f32_e32 v6, v80, v80
	v_add_f32_e32 v5, v5, v6
	v_mul_f32_e32 v6, v75, v75
	v_mul_f32_e32 v7, v77, v77
	v_fmac_f32_e32 v6, v74, v74
	v_fmac_f32_e32 v7, v76, v76
	v_add_f32_e32 v6, v6, v7
	v_add_f32_e32 v5, v6, v5
	v_mul_f32_e32 v6, v99, v99
	v_mul_f32_e32 v7, v101, v101
	v_fmac_f32_e32 v6, v98, v98
	v_fmac_f32_e32 v7, v100, v100
	v_add_f32_e32 v6, v6, v7
	v_mul_f32_e32 v7, v71, v71
	v_mul_f32_e32 v8, v73, v73
	v_fmac_f32_e32 v7, v70, v70
	v_fmac_f32_e32 v8, v72, v72
	v_add_f32_e32 v7, v7, v8
	v_add_f32_e32 v6, v7, v6
	v_add_f32_e32 v5, v5, v6
	v_mul_f32_e32 v6, v97, v97
	v_mul_f32_e32 v7, v95, v95
	v_fmac_f32_e32 v6, v96, v96
	v_fmac_f32_e32 v7, v94, v94
	v_add_f32_e32 v6, v6, v7
	v_mul_f32_e32 v7, v93, v93
	v_mul_f32_e32 v8, v91, v91
	v_fmac_f32_e32 v7, v92, v92
	v_fmac_f32_e32 v8, v90, v90
	v_add_f32_e32 v7, v7, v8
	v_add_f32_e32 v6, v7, v6
	v_mul_f32_e32 v7, v117, v117
	v_mul_f32_e32 v8, v115, v115
	v_fmac_f32_e32 v7, v116, v116
	v_fmac_f32_e32 v8, v114, v114
	v_add_f32_e32 v7, v7, v8
	v_mul_f32_e32 v8, v89, v89
	v_mul_f32_e32 v9, v87, v87
	v_fmac_f32_e32 v8, v88, v88
	v_fmac_f32_e32 v9, v86, v86
	v_add_f32_e32 v8, v8, v9
	v_add_f32_e32 v7, v8, v7
	v_add_f32_e32 v6, v6, v7
	v_mul_f32_e32 v7, v113, v113
	v_mul_f32_e32 v8, v111, v111
	v_fmac_f32_e32 v7, v112, v112
	v_fmac_f32_e32 v8, v110, v110
	v_add_f32_e32 v7, v7, v8
	v_mul_f32_e32 v8, v109, v109
	v_mul_f32_e32 v9, v107, v107
	v_fmac_f32_e32 v8, v108, v108
	v_fmac_f32_e32 v9, v106, v106
	v_add_f32_e32 v8, v8, v9
	v_add_f32_e32 v7, v8, v7
	v_mul_f32_e32 v8, v133, v133
	v_mul_f32_e32 v9, v131, v131
	v_fmac_f32_e32 v8, v132, v132
	v_fmac_f32_e32 v9, v130, v130
	v_add_f32_e32 v8, v8, v9
	v_mul_f32_e32 v9, v105, v105
	v_fmac_f32_e32 v9, v104, v104
	v_add_f32_e32 v9, v9, v10
	v_add_f32_e32 v8, v9, v8
	v_add_f32_e32 v7, v7, v8
	v_mul_f32_e32 v8, v129, v129
	v_mul_f32_e32 v9, v127, v127
	v_fmac_f32_e32 v8, v128, v128
	v_fmac_f32_e32 v9, v126, v126
	v_add_f32_e32 v8, v8, v9
	v_mul_f32_e32 v9, v125, v125
	v_mul_f32_e32 v10, v123, v123
	v_fmac_f32_e32 v9, v124, v124
	v_fmac_f32_e32 v10, v122, v122
	v_add_f32_e32 v9, v9, v10
	v_add_f32_e32 v8, v9, v8
	v_mul_f32_e32 v9, v141, v141
	v_mul_f32_e32 v10, v139, v139
	v_fmac_f32_e32 v9, v140, v140
	v_fmac_f32_e32 v10, v138, v138
	v_add_f32_e32 v9, v9, v10
	v_mul_f32_e32 v10, v121, v121
	v_mul_f32_e32 v11, v119, v119
	v_fmac_f32_e32 v10, v120, v120
	v_fmac_f32_e32 v11, v118, v118
	v_add_f32_e32 v10, v10, v11
	v_add_f32_e32 v9, v10, v9
	v_add_f32_e32 v8, v8, v9
	v_mul_f32_e32 v9, v163, v163
	v_mul_f32_e32 v10, v161, v161
	v_fmac_f32_e32 v9, v162, v162
	v_fmac_f32_e32 v10, v160, v160
	v_add_f32_e32 v9, v9, v10
	v_mul_f32_e32 v10, v145, v145
	v_mul_f32_e32 v11, v143, v143
	v_fmac_f32_e32 v10, v144, v144
	v_fmac_f32_e32 v11, v142, v142
	v_add_f32_e32 v10, v10, v11
	v_add_f32_e32 v9, v10, v9
	v_mul_f32_e32 v10, v173, v173
	v_mul_f32_e32 v11, v171, v171
	v_fmac_f32_e32 v10, v172, v172
	v_fmac_f32_e32 v11, v170, v170
	v_add_f32_e32 v10, v10, v11
	v_mul_f32_e32 v11, v137, v137
	v_mul_f32_e32 v12, v135, v135
	v_fmac_f32_e32 v11, v136, v136
	v_fmac_f32_e32 v12, v134, v134
	v_add_f32_e32 v11, v11, v12
	v_add_f32_e32 v10, v11, v10
	v_add_f32_e32 v9, v9, v10
	v_lshrrev_b32_e32 v10, 2, v178
	s_lshl_b32 s41, s70, 2
	v_and_b32_e32 v10, 12, v10
	v_lshlrev_b32_e32 v11, 4, v179
	s_or_b32 s48, s39, s41
	v_add3_u32 v10, s9, v10, v11
	ds_write2st64_b32 v10, v9, v8 offset1:1
	ds_write2st64_b32 v10, v7, v6 offset0:2 offset1:3
	ds_write2st64_b32 v10, v5, v4 offset0:4 offset1:5
	ds_write2st64_b32 v10, v3, v2 offset0:6 offset1:7
	v_add_u32_e32 v6, s9, v154
	s_ashr_i32 s49, s48, 31
	s_ashr_i32 s47, s46, 31
	s_ashr_i32 s9, s8, 31
	s_lshl_b64 s[48:49], s[48:49], 18
	ds_read_b128 v[2:5], v6
	s_add_u32 s39, s68, s48
	s_addc_u32 s41, s69, s49
	s_lshl_b64 s[46:47], s[46:47], 2
	ds_read_b128 v[6:9], v6 offset:1024
	s_add_u32 s39, s39, s46
	s_addc_u32 s41, s41, s47
	s_lshl_b64 s[8:9], s[8:9], 2
	s_add_u32 s8, s39, s8
	s_waitcnt lgkmcnt(1)
	v_add_f32_e32 v2, v2, v3
	v_add_f32_e32 v3, v4, v5
	s_addc_u32 s9, s41, s9
	v_lshlrev_b32_e32 v10, 2, v177
	v_add_f32_e32 v2, v2, v3
	global_store_dword v10, v2, s[8:9]
	s_waitcnt lgkmcnt(0)
	v_add_f32_e32 v2, v6, v7
	v_add_f32_e32 v3, v8, v9
	v_add_f32_e32 v2, v2, v3
	s_and_b64 vcc, exec, s[6:7]
	s_mov_b64 s[6:7], -1
	global_store_dword v10, v2, s[8:9] offset:512
	s_cbranch_vccnz .LBB0_3571
	v_mov_b32_e32 v2, v0
	s_nop 0
	v_readfirstlane_b32 s6, v2
	s_and_b32 s8, s6, 0xc0
	s_lshl_b32 s6, s38, 8
	s_ashr_i32 s7, s6, 31
	s_lshl_b64 s[6:7], s[6:7], 2
	s_add_u32 s6, s5, s6
	s_addc_u32 s7, s31, s7
	s_lshl_b32 s8, s8, 2
	s_add_u32 s6, s6, s8
	v_lshlrev_b32_e32 v2, 1, v2
	s_addc_u32 s7, s7, 0
	v_and_b32_e32 v6, 0x60, v2
	global_load_dwordx4 v[10:13], v6, s[6:7] offset:16 nt
	global_load_dwordx4 v[14:17], v6, s[6:7] nt
	global_load_dwordx4 v[2:5], v6, s[6:7] offset:144 nt
	s_nop 0
	global_load_dwordx4 v[6:9], v6, s[6:7] offset:128 nt
	s_andn2_b64 vcc, exec, s[12:13]
	s_cbranch_vccnz .LBB0_3570
	s_barrier
	s_branch .LBB0_3570
